# GEMM K-loops: per-segment priority inverted (load segments at priority 1, MFMA blocks at 0) (on top of v59)
# baseline (speedup 1.0000x reference)
.LBB0_120:
	ds_read_b128 v[136:139], v211
	ds_read_b128 v[140:143], v211 offset:1024
	ds_read_b128 v[144:147], v211 offset:2048
	ds_read_b128 v[148:151], v211 offset:3072
	ds_read_b128 v[152:155], v212
	ds_read_b128 v[156:159], v212 offset:1024
	ds_read_b128 v[160:163], v212 offset:2048
	ds_read_b128 v[186:189], v212 offset:3072
	s_add_u32 s41, s15, s18
	s_addc_u32 s42, s24, s19
	s_add_u32 s66, s18, 0x100
	s_addc_u32 s67, s19, 0
	s_cmp_eq_u32 s40, 28
	s_cselect_b64 s[70:71], -1, 0
	s_and_b64 s[2:3], s[70:71], exec
	s_cselect_b32 s69, s5, s42
	s_cselect_b32 s68, s13, s41
	s_cselect_b32 s41, 0, s66
	v_lshl_add_u64 v[198:199], v[132:133], 0, s[18:19]
	s_add_i32 m0, s92, 0xc000
	ds_read_b128 v[190:193], v213
	ds_read_b128 v[194:197], v213 offset:1024
	ds_read_b128 v[214:217], v213 offset:2048
	ds_read_b128 v[218:221], v213 offset:3072
	ds_read_b128 v[222:225], v213 offset:4096
	ds_read_b128 v[226:229], v213 offset:5120
	ds_read_b128 v[230:233], v213 offset:6144
	ds_read_b128 v[234:237], v213 offset:7168
	global_load_lds_dwordx4 v[198:199], off
	v_lshl_add_u64 v[198:199], v[134:135], 0, s[18:19]
	s_add_i32 m0, s92, 0xe000
	s_nop 0
	global_load_lds_dwordx4 v[198:199], off
	s_waitcnt vmcnt(8)
	s_waitcnt lgkmcnt(0)
	s_barrier
	s_setprio 0
	s_waitcnt lgkmcnt(0)
	v_mfma_f32_16x16x32_bf16 v[128:131], v[136:139], v[190:193], v[128:131]
	v_mfma_f32_16x16x32_bf16 v[124:127], v[144:147], v[190:193], v[124:127]
	v_mfma_f32_16x16x32_bf16 v[120:123], v[136:139], v[214:217], v[120:123]
	v_mfma_f32_16x16x32_bf16 v[112:115], v[144:147], v[214:217], v[112:115]
	v_mfma_f32_16x16x32_bf16 v[104:107], v[136:139], v[222:225], v[104:107]
	v_mfma_f32_16x16x32_bf16 v[96:99], v[144:147], v[222:225], v[96:99]
	v_mfma_f32_16x16x32_bf16 v[88:91], v[136:139], v[230:233], v[88:91]
	v_mfma_f32_16x16x32_bf16 v[80:83], v[144:147], v[230:233], v[80:83]
	v_mfma_f32_16x16x32_bf16 v[128:131], v[140:143], v[194:197], v[128:131]
	v_mfma_f32_16x16x32_bf16 v[124:127], v[148:151], v[194:197], v[124:127]
	v_mfma_f32_16x16x32_bf16 v[120:123], v[140:143], v[218:221], v[120:123]
	v_mfma_f32_16x16x32_bf16 v[112:115], v[148:151], v[218:221], v[112:115]
	v_mfma_f32_16x16x32_bf16 v[104:107], v[140:143], v[226:229], v[104:107]
	v_mfma_f32_16x16x32_bf16 v[96:99], v[148:151], v[226:229], v[96:99]
	v_mfma_f32_16x16x32_bf16 v[88:91], v[140:143], v[234:237], v[88:91]
	v_mfma_f32_16x16x32_bf16 v[80:83], v[148:151], v[234:237], v[80:83]
	v_mfma_f32_16x16x32_bf16 v[116:119], v[152:155], v[190:193], v[116:119]
	v_mfma_f32_16x16x32_bf16 v[108:111], v[160:163], v[190:193], v[108:111]
	v_mfma_f32_16x16x32_bf16 v[100:103], v[152:155], v[214:217], v[100:103]
	v_mfma_f32_16x16x32_bf16 v[92:95], v[160:163], v[214:217], v[92:95]
	v_mfma_f32_16x16x32_bf16 v[84:87], v[152:155], v[222:225], v[84:87]
	v_mfma_f32_16x16x32_bf16 v[76:79], v[160:163], v[222:225], v[76:79]
	v_mfma_f32_16x16x32_bf16 v[72:75], v[152:155], v[230:233], v[72:75]
	v_mfma_f32_16x16x32_bf16 v[68:71], v[160:163], v[230:233], v[68:71]
	v_mfma_f32_16x16x32_bf16 v[116:119], v[156:159], v[194:197], v[116:119]
	v_mfma_f32_16x16x32_bf16 v[108:111], v[186:189], v[194:197], v[108:111]
	v_mfma_f32_16x16x32_bf16 v[100:103], v[156:159], v[218:221], v[100:103]
	v_mfma_f32_16x16x32_bf16 v[92:95], v[186:189], v[218:221], v[92:95]
	v_mfma_f32_16x16x32_bf16 v[84:87], v[156:159], v[226:229], v[84:87]
	v_mfma_f32_16x16x32_bf16 v[76:79], v[186:189], v[226:229], v[76:79]
	v_mfma_f32_16x16x32_bf16 v[72:75], v[156:159], v[234:237], v[72:75]
	v_mfma_f32_16x16x32_bf16 v[68:71], v[186:189], v[234:237], v[68:71]
	s_setprio 1
	s_barrier
	s_add_i32 s2, s54, s96
	v_lshl_add_u64 v[198:199], s[68:69], 0, v[166:167]
	s_mov_b32 m0, s2
	ds_read_b128 v[190:193], v213 offset:16384
	ds_read_b128 v[194:197], v213 offset:17408
	ds_read_b128 v[214:217], v213 offset:18432
	ds_read_b128 v[218:221], v213 offset:19456
	ds_read_b128 v[222:225], v213 offset:20480
	ds_read_b128 v[226:229], v213 offset:21504
	ds_read_b128 v[230:233], v213 offset:22528
	ds_read_b128 v[234:237], v213 offset:23552
	global_load_lds_dwordx4 v[198:199], off
	s_add_i32 m0, s2, 0x2000
	s_add_u32 s2, s68, 0x80000
	v_lshl_add_u64 v[238:239], s[68:69], 0, v[170:171]
	s_addc_u32 s3, s69, 0
	s_add_i32 s18, s55, s96
	global_load_lds_dwordx4 v[238:239], off
	v_lshl_add_u64 v[240:241], s[2:3], 0, v[166:167]
	s_mov_b32 m0, s18
	s_nop 0
	global_load_lds_dwordx4 v[240:241], off
	v_lshl_add_u64 v[240:241], s[2:3], 0, v[170:171]
	s_add_i32 m0, s18, 0x2000
	s_and_b64 s[2:3], s[10:11], s[70:71]
	s_and_b64 s[2:3], s[2:3], exec
	s_cselect_b32 s2, s62, s16
	s_cselect_b32 s3, s63, s17
	s_add_u32 s2, s2, s41
	s_addc_u32 s3, s3, 0
	global_load_lds_dwordx4 v[240:241], off
	v_lshl_add_u64 v[240:241], s[2:3], 0, v[164:165]
	s_mov_b32 m0, s92
	v_lshl_add_u64 v[244:245], s[2:3], 0, v[168:169]
	global_load_lds_dwordx4 v[240:241], off
	s_mov_b32 m0, s52
	s_nop 0
	global_load_lds_dwordx4 v[244:245], off
	s_waitcnt vmcnt(8)
	s_waitcnt lgkmcnt(0)
	s_barrier
	s_setprio 0
	s_waitcnt lgkmcnt(0)
	v_mfma_f32_16x16x32_bf16 v[64:67], v[136:139], v[190:193], v[64:67]
	v_mfma_f32_16x16x32_bf16 v[60:63], v[144:147], v[190:193], v[60:63]
	v_mfma_f32_16x16x32_bf16 v[52:55], v[136:139], v[214:217], v[52:55]
	v_mfma_f32_16x16x32_bf16 v[44:47], v[144:147], v[214:217], v[44:47]
	v_mfma_f32_16x16x32_bf16 v[36:39], v[136:139], v[222:225], v[36:39]
	v_mfma_f32_16x16x32_bf16 v[28:31], v[144:147], v[222:225], v[28:31]
	v_mfma_f32_16x16x32_bf16 v[20:23], v[136:139], v[230:233], v[20:23]
	v_mfma_f32_16x16x32_bf16 v[12:15], v[144:147], v[230:233], v[12:15]
	v_mfma_f32_16x16x32_bf16 v[64:67], v[140:143], v[194:197], v[64:67]
	v_mfma_f32_16x16x32_bf16 v[60:63], v[148:151], v[194:197], v[60:63]
	v_mfma_f32_16x16x32_bf16 v[52:55], v[140:143], v[218:221], v[52:55]
	v_mfma_f32_16x16x32_bf16 v[44:47], v[148:151], v[218:221], v[44:47]
	v_mfma_f32_16x16x32_bf16 v[36:39], v[140:143], v[226:229], v[36:39]
	v_mfma_f32_16x16x32_bf16 v[28:31], v[148:151], v[226:229], v[28:31]
	v_mfma_f32_16x16x32_bf16 v[20:23], v[140:143], v[234:237], v[20:23]
	v_mfma_f32_16x16x32_bf16 v[12:15], v[148:151], v[234:237], v[12:15]
	v_mfma_f32_16x16x32_bf16 v[56:59], v[152:155], v[190:193], v[56:59]
	v_mfma_f32_16x16x32_bf16 v[48:51], v[160:163], v[190:193], v[48:51]
	v_mfma_f32_16x16x32_bf16 v[40:43], v[152:155], v[214:217], v[40:43]
	v_mfma_f32_16x16x32_bf16 v[32:35], v[160:163], v[214:217], v[32:35]
	v_mfma_f32_16x16x32_bf16 v[24:27], v[152:155], v[222:225], v[24:27]
	v_mfma_f32_16x16x32_bf16 v[16:19], v[160:163], v[222:225], v[16:19]
	v_mfma_f32_16x16x32_bf16 v[8:11], v[152:155], v[230:233], v[8:11]
	v_mfma_f32_16x16x32_bf16 v[4:7], v[160:163], v[230:233], v[4:7]
	v_mfma_f32_16x16x32_bf16 v[56:59], v[156:159], v[194:197], v[56:59]
	v_mfma_f32_16x16x32_bf16 v[48:51], v[186:189], v[194:197], v[48:51]
	v_mfma_f32_16x16x32_bf16 v[40:43], v[156:159], v[218:221], v[40:43]
	v_mfma_f32_16x16x32_bf16 v[32:35], v[186:189], v[218:221], v[32:35]
	v_mfma_f32_16x16x32_bf16 v[24:27], v[156:159], v[226:229], v[24:27]
	v_mfma_f32_16x16x32_bf16 v[16:19], v[186:189], v[226:229], v[16:19]
	v_mfma_f32_16x16x32_bf16 v[8:11], v[156:159], v[234:237], v[8:11]
	v_mfma_f32_16x16x32_bf16 v[4:7], v[186:189], v[234:237], v[4:7]
	s_setprio 1
	s_barrier
	s_add_i32 s18, 0, 0x18000
	v_add_u32_e32 v3, s18, v209
	s_add_i32 s19, 0, 0x1c000
	ds_read_b128 v[136:139], v3
	ds_read_b128 v[140:143], v3 offset:1024
	ds_read_b128 v[144:147], v3 offset:2048
	ds_read_b128 v[148:151], v3 offset:3072
	v_add_u32_e32 v3, s19, v209
	ds_read_b128 v[152:155], v3
	ds_read_b128 v[156:159], v3 offset:1024
	ds_read_b128 v[160:163], v3 offset:2048
	ds_read_b128 v[186:189], v3 offset:3072
	s_add_u32 s2, s2, 0x80000
	s_addc_u32 s3, s3, 0
	s_mov_b32 m0, s53
	v_lshl_add_u64 v[246:247], s[2:3], 0, v[164:165]
	ds_read_b128 v[190:193], v213 offset:32768
	ds_read_b128 v[194:197], v213 offset:33792
	ds_read_b128 v[214:217], v213 offset:34816
	ds_read_b128 v[218:221], v213 offset:35840
	ds_read_b128 v[222:225], v213 offset:36864
	ds_read_b128 v[226:229], v213 offset:37888
	ds_read_b128 v[230:233], v213 offset:38912
	ds_read_b128 v[234:237], v213 offset:39936
	global_load_lds_dwordx4 v[246:247], off
	v_lshl_add_u64 v[246:247], s[2:3], 0, v[168:169]
	s_mov_b32 m0, s50
	s_nop 0
	global_load_lds_dwordx4 v[246:247], off
	s_waitcnt vmcnt(8)
	s_waitcnt lgkmcnt(0)
	s_barrier
	s_setprio 0
	s_waitcnt lgkmcnt(0)
	v_mfma_f32_16x16x32_bf16 v[128:131], v[136:139], v[190:193], v[128:131]
	v_mfma_f32_16x16x32_bf16 v[124:127], v[144:147], v[190:193], v[124:127]
	v_mfma_f32_16x16x32_bf16 v[120:123], v[136:139], v[214:217], v[120:123]
	v_mfma_f32_16x16x32_bf16 v[112:115], v[144:147], v[214:217], v[112:115]
	v_mfma_f32_16x16x32_bf16 v[104:107], v[136:139], v[222:225], v[104:107]
	v_mfma_f32_16x16x32_bf16 v[96:99], v[144:147], v[222:225], v[96:99]
	v_mfma_f32_16x16x32_bf16 v[88:91], v[136:139], v[230:233], v[88:91]
	v_mfma_f32_16x16x32_bf16 v[80:83], v[144:147], v[230:233], v[80:83]
	v_mfma_f32_16x16x32_bf16 v[128:131], v[140:143], v[194:197], v[128:131]
	v_mfma_f32_16x16x32_bf16 v[124:127], v[148:151], v[194:197], v[124:127]
	v_mfma_f32_16x16x32_bf16 v[120:123], v[140:143], v[218:221], v[120:123]
	v_mfma_f32_16x16x32_bf16 v[112:115], v[148:151], v[218:221], v[112:115]
	v_mfma_f32_16x16x32_bf16 v[104:107], v[140:143], v[226:229], v[104:107]
	v_mfma_f32_16x16x32_bf16 v[96:99], v[148:151], v[226:229], v[96:99]
	v_mfma_f32_16x16x32_bf16 v[88:91], v[140:143], v[234:237], v[88:91]
	v_mfma_f32_16x16x32_bf16 v[80:83], v[148:151], v[234:237], v[80:83]
	v_mfma_f32_16x16x32_bf16 v[116:119], v[152:155], v[190:193], v[116:119]
	v_mfma_f32_16x16x32_bf16 v[108:111], v[160:163], v[190:193], v[108:111]
	v_mfma_f32_16x16x32_bf16 v[100:103], v[152:155], v[214:217], v[100:103]
	v_mfma_f32_16x16x32_bf16 v[92:95], v[160:163], v[214:217], v[92:95]
	v_mfma_f32_16x16x32_bf16 v[84:87], v[152:155], v[222:225], v[84:87]
	v_mfma_f32_16x16x32_bf16 v[76:79], v[160:163], v[222:225], v[76:79]
	v_mfma_f32_16x16x32_bf16 v[72:75], v[152:155], v[230:233], v[72:75]
	v_mfma_f32_16x16x32_bf16 v[68:71], v[160:163], v[230:233], v[68:71]
	v_mfma_f32_16x16x32_bf16 v[116:119], v[156:159], v[194:197], v[116:119]
	v_mfma_f32_16x16x32_bf16 v[108:111], v[186:189], v[194:197], v[108:111]
	v_mfma_f32_16x16x32_bf16 v[100:103], v[156:159], v[218:221], v[100:103]
	v_mfma_f32_16x16x32_bf16 v[92:95], v[186:189], v[218:221], v[92:95]
	v_mfma_f32_16x16x32_bf16 v[84:87], v[156:159], v[226:229], v[84:87]
	v_mfma_f32_16x16x32_bf16 v[76:79], v[186:189], v[226:229], v[76:79]
	v_mfma_f32_16x16x32_bf16 v[72:75], v[156:159], v[234:237], v[72:75]
	v_mfma_f32_16x16x32_bf16 v[68:71], v[186:189], v[234:237], v[68:71]
	s_setprio 1
	s_barrier
	s_add_i32 s2, s18, s96
	v_lshl_add_u64 v[198:199], v[198:199], 0, s[38:39]
	s_mov_b32 m0, s2
	ds_read_b128 v[190:193], v213 offset:49152
	ds_read_b128 v[194:197], v213 offset:50176
	ds_read_b128 v[214:217], v213 offset:51200
	ds_read_b128 v[218:221], v213 offset:52224
	ds_read_b128 v[222:225], v213 offset:53248
	ds_read_b128 v[226:229], v213 offset:54272
	ds_read_b128 v[230:233], v213 offset:55296
	ds_read_b128 v[234:237], v213 offset:56320
	global_load_lds_dwordx4 v[198:199], off
	s_add_i32 m0, s2, 0x2000
	s_add_u32 s2, s68, 0x80080
	v_lshl_add_u64 v[198:199], v[238:239], 0, s[38:39]
	s_addc_u32 s3, s69, 0
	s_add_i32 s18, s19, s96
	global_load_lds_dwordx4 v[198:199], off
	v_lshl_add_u64 v[198:199], s[2:3], 0, v[166:167]
	s_mov_b32 m0, s18
	s_nop 0
	global_load_lds_dwordx4 v[198:199], off
	v_lshl_add_u64 v[198:199], s[2:3], 0, v[170:171]
	s_add_i32 m0, s18, 0x2000
	s_nop 0
	global_load_lds_dwordx4 v[198:199], off
	v_lshl_add_u64 v[198:199], v[240:241], 0, s[38:39]
	s_mov_b32 m0, s56
	s_nop 0
	global_load_lds_dwordx4 v[198:199], off
	v_lshl_add_u64 v[198:199], v[244:245], 0, s[38:39]
	s_mov_b32 m0, s57
	s_nop 0
	global_load_lds_dwordx4 v[198:199], off
	s_waitcnt vmcnt(8)
	s_waitcnt lgkmcnt(0)
	s_barrier
	s_setprio 0
	s_waitcnt lgkmcnt(0)
	v_mfma_f32_16x16x32_bf16 v[64:67], v[136:139], v[190:193], v[64:67]
	v_mfma_f32_16x16x32_bf16 v[60:63], v[144:147], v[190:193], v[60:63]
	v_mfma_f32_16x16x32_bf16 v[52:55], v[136:139], v[214:217], v[52:55]
	v_mfma_f32_16x16x32_bf16 v[44:47], v[144:147], v[214:217], v[44:47]
	v_mfma_f32_16x16x32_bf16 v[36:39], v[136:139], v[222:225], v[36:39]
	v_mfma_f32_16x16x32_bf16 v[28:31], v[144:147], v[222:225], v[28:31]
	v_mfma_f32_16x16x32_bf16 v[20:23], v[136:139], v[230:233], v[20:23]
	v_mfma_f32_16x16x32_bf16 v[12:15], v[144:147], v[230:233], v[12:15]
	v_mfma_f32_16x16x32_bf16 v[64:67], v[140:143], v[194:197], v[64:67]
	v_mfma_f32_16x16x32_bf16 v[60:63], v[148:151], v[194:197], v[60:63]
	v_mfma_f32_16x16x32_bf16 v[52:55], v[140:143], v[218:221], v[52:55]
	v_mfma_f32_16x16x32_bf16 v[44:47], v[148:151], v[218:221], v[44:47]
	v_mfma_f32_16x16x32_bf16 v[36:39], v[140:143], v[226:229], v[36:39]
	v_mfma_f32_16x16x32_bf16 v[28:31], v[148:151], v[226:229], v[28:31]
	v_mfma_f32_16x16x32_bf16 v[20:23], v[140:143], v[234:237], v[20:23]
	v_mfma_f32_16x16x32_bf16 v[12:15], v[148:151], v[234:237], v[12:15]
	v_mfma_f32_16x16x32_bf16 v[56:59], v[152:155], v[190:193], v[56:59]
	v_mfma_f32_16x16x32_bf16 v[48:51], v[160:163], v[190:193], v[48:51]
	v_mfma_f32_16x16x32_bf16 v[40:43], v[152:155], v[214:217], v[40:43]
	v_mfma_f32_16x16x32_bf16 v[32:35], v[160:163], v[214:217], v[32:35]
	v_mfma_f32_16x16x32_bf16 v[24:27], v[152:155], v[222:225], v[24:27]
	v_mfma_f32_16x16x32_bf16 v[16:19], v[160:163], v[222:225], v[16:19]
	v_mfma_f32_16x16x32_bf16 v[8:11], v[152:155], v[230:233], v[8:11]
	v_mfma_f32_16x16x32_bf16 v[4:7], v[160:163], v[230:233], v[4:7]
	v_mfma_f32_16x16x32_bf16 v[56:59], v[156:159], v[194:197], v[56:59]
	v_mfma_f32_16x16x32_bf16 v[48:51], v[186:189], v[194:197], v[48:51]
	v_mfma_f32_16x16x32_bf16 v[40:43], v[156:159], v[218:221], v[40:43]
	v_mfma_f32_16x16x32_bf16 v[32:35], v[186:189], v[218:221], v[32:35]
	v_mfma_f32_16x16x32_bf16 v[24:27], v[156:159], v[226:229], v[24:27]
	v_mfma_f32_16x16x32_bf16 v[16:19], v[186:189], v[226:229], v[16:19]
	v_mfma_f32_16x16x32_bf16 v[8:11], v[156:159], v[234:237], v[8:11]
	v_mfma_f32_16x16x32_bf16 v[4:7], v[186:189], v[234:237], v[4:7]
	s_setprio 1
	s_barrier
	s_add_i32 s40, s40, 2
	s_cmp_gt_u32 s40, 29
	s_mov_b64 s[18:19], s[66:67]
	s_cbranch_scc0 .LBB0_120
	v_readlane_b32 s2, v252, 27
	v_readlane_b32 s3, v252, 28
	s_and_b64 vcc, exec, s[2:3]
	s_cbranch_vccz .LBB0_123
	s_barrier

.LBB0_346:
	ds_read_b128 v[148:151], v1
	ds_read_b128 v[152:155], v1 offset:1024
	ds_read_b128 v[156:159], v1 offset:2048
	ds_read_b128 v[160:163], v1 offset:3072
	ds_read_b128 v[172:175], v145
	ds_read_b128 v[176:179], v145 offset:1024
	ds_read_b128 v[180:183], v145 offset:2048
	ds_read_b128 v[184:187], v145 offset:3072
	s_add_u32 s34, s51, s28
	s_addc_u32 s35, s52, s29
	s_add_u32 s30, s28, 0x100
	s_addc_u32 s31, s29, 0
	s_cmp_eq_u32 s53, 28
	s_cselect_b64 s[36:37], -1, 0
	s_and_b64 s[2:3], s[36:37], exec
	s_cselect_b32 s35, s15, s35
	s_cselect_b32 s34, s17, s34
	s_cselect_b32 s54, 0, s30
	v_lshl_add_u64 v[220:221], v[140:141], 0, s[28:29]
	s_add_i32 m0, s21, 0xc000
	ds_read_b128 v[188:191], v146
	ds_read_b128 v[192:195], v146 offset:1024
	ds_read_b128 v[196:199], v146 offset:2048
	ds_read_b128 v[200:203], v146 offset:3072
	ds_read_b128 v[204:207], v146 offset:4096
	ds_read_b128 v[208:211], v146 offset:5120
	ds_read_b128 v[212:215], v146 offset:6144
	ds_read_b128 v[216:219], v146 offset:7168
	global_load_lds_dwordx4 v[220:221], off
	v_lshl_add_u64 v[220:221], v[142:143], 0, s[28:29]
	s_add_i32 m0, s21, 0xe000
	s_nop 0
	global_load_lds_dwordx4 v[220:221], off
	s_waitcnt vmcnt(8)
	s_waitcnt lgkmcnt(0)
	s_barrier
	s_setprio 0
	s_waitcnt lgkmcnt(0)
	v_mfma_f32_16x16x32_bf16 v[126:129], v[188:191], v[148:151], v[126:129]
	v_mfma_f32_16x16x32_bf16 v[114:117], v[188:191], v[156:159], v[114:117]
	v_mfma_f32_16x16x32_bf16 v[122:125], v[196:199], v[148:151], v[122:125]
	v_mfma_f32_16x16x32_bf16 v[106:109], v[196:199], v[156:159], v[106:109]
	v_mfma_f32_16x16x32_bf16 v[118:121], v[204:207], v[148:151], v[118:121]
	v_mfma_f32_16x16x32_bf16 v[102:105], v[204:207], v[156:159], v[102:105]
	v_mfma_f32_16x16x32_bf16 v[110:113], v[212:215], v[148:151], v[110:113]
	v_mfma_f32_16x16x32_bf16 v[98:101], v[212:215], v[156:159], v[98:101]
	v_mfma_f32_16x16x32_bf16 v[126:129], v[192:195], v[152:155], v[126:129]
	v_mfma_f32_16x16x32_bf16 v[114:117], v[192:195], v[160:163], v[114:117]
	v_mfma_f32_16x16x32_bf16 v[122:125], v[200:203], v[152:155], v[122:125]
	v_mfma_f32_16x16x32_bf16 v[106:109], v[200:203], v[160:163], v[106:109]
	v_mfma_f32_16x16x32_bf16 v[118:121], v[208:211], v[152:155], v[118:121]
	v_mfma_f32_16x16x32_bf16 v[102:105], v[208:211], v[160:163], v[102:105]
	v_mfma_f32_16x16x32_bf16 v[110:113], v[216:219], v[152:155], v[110:113]
	v_mfma_f32_16x16x32_bf16 v[98:101], v[216:219], v[160:163], v[98:101]
	v_mfma_f32_16x16x32_bf16 v[94:97], v[188:191], v[172:175], v[94:97]
	v_mfma_f32_16x16x32_bf16 v[82:85], v[188:191], v[180:183], v[82:85]
	v_mfma_f32_16x16x32_bf16 v[90:93], v[196:199], v[172:175], v[90:93]
	v_mfma_f32_16x16x32_bf16 v[74:77], v[196:199], v[180:183], v[74:77]
	v_mfma_f32_16x16x32_bf16 v[86:89], v[204:207], v[172:175], v[86:89]
	v_mfma_f32_16x16x32_bf16 v[70:73], v[204:207], v[180:183], v[70:73]
	v_mfma_f32_16x16x32_bf16 v[78:81], v[212:215], v[172:175], v[78:81]
	v_mfma_f32_16x16x32_bf16 v[66:69], v[212:215], v[180:183], v[66:69]
	v_mfma_f32_16x16x32_bf16 v[94:97], v[192:195], v[176:179], v[94:97]
	v_mfma_f32_16x16x32_bf16 v[82:85], v[192:195], v[184:187], v[82:85]
	v_mfma_f32_16x16x32_bf16 v[90:93], v[200:203], v[176:179], v[90:93]
	v_mfma_f32_16x16x32_bf16 v[74:77], v[200:203], v[184:187], v[74:77]
	v_mfma_f32_16x16x32_bf16 v[86:89], v[208:211], v[176:179], v[86:89]
	v_mfma_f32_16x16x32_bf16 v[70:73], v[208:211], v[184:187], v[70:73]
	v_mfma_f32_16x16x32_bf16 v[78:81], v[216:219], v[176:179], v[78:81]
	v_mfma_f32_16x16x32_bf16 v[66:69], v[216:219], v[184:187], v[66:69]
	s_setprio 1
	s_barrier
	s_add_i32 s2, s49, s20
	v_lshl_add_u64 v[220:221], s[34:35], 0, v[164:165]
	s_mov_b32 m0, s2
	ds_read_b128 v[188:191], v146 offset:16384
	ds_read_b128 v[192:195], v146 offset:17408
	ds_read_b128 v[196:199], v146 offset:18432
	ds_read_b128 v[200:203], v146 offset:19456
	ds_read_b128 v[204:207], v146 offset:20480
	ds_read_b128 v[208:211], v146 offset:21504
	ds_read_b128 v[212:215], v146 offset:22528
	ds_read_b128 v[216:219], v146 offset:23552
	global_load_lds_dwordx4 v[220:221], off
	s_add_i32 m0, s2, 0x2000
	s_add_u32 s2, s34, 0x80000
	v_lshl_add_u64 v[222:223], s[34:35], 0, v[168:169]
	s_addc_u32 s3, s35, 0
	s_add_i32 s28, s50, s20
	global_load_lds_dwordx4 v[222:223], off
	v_lshl_add_u64 v[224:225], s[2:3], 0, v[164:165]
	s_mov_b32 m0, s28
	s_nop 0
	global_load_lds_dwordx4 v[224:225], off
	v_lshl_add_u64 v[224:225], s[2:3], 0, v[168:169]
	s_add_i32 m0, s28, 0x2000
	s_and_b64 s[2:3], s[6:7], s[36:37]
	s_and_b64 s[2:3], s[2:3], exec
	s_cselect_b32 s2, s18, s26
	s_cselect_b32 s3, s19, s27
	s_add_u32 s2, s2, s54
	s_addc_u32 s3, s3, 0
	global_load_lds_dwordx4 v[224:225], off
	v_lshl_add_u64 v[224:225], s[2:3], 0, v[166:167]
	s_mov_b32 m0, s21
	v_lshl_add_u64 v[226:227], s[2:3], 0, v[170:171]
	global_load_lds_dwordx4 v[224:225], off
	s_mov_b32 m0, s33
	s_nop 0
	global_load_lds_dwordx4 v[226:227], off
	s_waitcnt vmcnt(8)
	s_waitcnt lgkmcnt(0)
	s_barrier
	s_setprio 0
	s_waitcnt lgkmcnt(0)
	v_mfma_f32_16x16x32_bf16 v[62:65], v[188:191], v[148:151], v[62:65]
	v_mfma_f32_16x16x32_bf16 v[50:53], v[188:191], v[156:159], v[50:53]
	v_mfma_f32_16x16x32_bf16 v[58:61], v[196:199], v[148:151], v[58:61]
	v_mfma_f32_16x16x32_bf16 v[42:45], v[196:199], v[156:159], v[42:45]
	v_mfma_f32_16x16x32_bf16 v[54:57], v[204:207], v[148:151], v[54:57]
	v_mfma_f32_16x16x32_bf16 v[38:41], v[204:207], v[156:159], v[38:41]
	v_mfma_f32_16x16x32_bf16 v[46:49], v[212:215], v[148:151], v[46:49]
	v_mfma_f32_16x16x32_bf16 v[34:37], v[212:215], v[156:159], v[34:37]
	v_mfma_f32_16x16x32_bf16 v[62:65], v[192:195], v[152:155], v[62:65]
	v_mfma_f32_16x16x32_bf16 v[50:53], v[192:195], v[160:163], v[50:53]
	v_mfma_f32_16x16x32_bf16 v[58:61], v[200:203], v[152:155], v[58:61]
	v_mfma_f32_16x16x32_bf16 v[42:45], v[200:203], v[160:163], v[42:45]
	v_mfma_f32_16x16x32_bf16 v[54:57], v[208:211], v[152:155], v[54:57]
	v_mfma_f32_16x16x32_bf16 v[38:41], v[208:211], v[160:163], v[38:41]
	v_mfma_f32_16x16x32_bf16 v[46:49], v[216:219], v[152:155], v[46:49]
	v_mfma_f32_16x16x32_bf16 v[34:37], v[216:219], v[160:163], v[34:37]
	v_mfma_f32_16x16x32_bf16 v[30:33], v[188:191], v[172:175], v[30:33]
	v_mfma_f32_16x16x32_bf16 v[18:21], v[188:191], v[180:183], v[18:21]
	v_mfma_f32_16x16x32_bf16 v[26:29], v[196:199], v[172:175], v[26:29]
	v_mfma_f32_16x16x32_bf16 v[10:13], v[196:199], v[180:183], v[10:13]
	v_mfma_f32_16x16x32_bf16 v[22:25], v[204:207], v[172:175], v[22:25]
	v_mfma_f32_16x16x32_bf16 v[6:9], v[204:207], v[180:183], v[6:9]
	v_mfma_f32_16x16x32_bf16 v[14:17], v[212:215], v[172:175], v[14:17]
	v_mfma_f32_16x16x32_bf16 v[2:5], v[212:215], v[180:183], v[2:5]
	v_mfma_f32_16x16x32_bf16 v[30:33], v[192:195], v[176:179], v[30:33]
	v_mfma_f32_16x16x32_bf16 v[18:21], v[192:195], v[184:187], v[18:21]
	v_mfma_f32_16x16x32_bf16 v[26:29], v[200:203], v[176:179], v[26:29]
	v_mfma_f32_16x16x32_bf16 v[10:13], v[200:203], v[184:187], v[10:13]
	v_mfma_f32_16x16x32_bf16 v[22:25], v[208:211], v[176:179], v[22:25]
	v_mfma_f32_16x16x32_bf16 v[6:9], v[208:211], v[184:187], v[6:9]
	v_mfma_f32_16x16x32_bf16 v[14:17], v[216:219], v[176:179], v[14:17]
	v_mfma_f32_16x16x32_bf16 v[2:5], v[216:219], v[184:187], v[2:5]
	s_setprio 1
	s_barrier
	s_add_i32 s28, 0, 0x18000
	v_add_u32_e32 v147, s28, v144
	s_add_i32 s29, 0, 0x1c000
	ds_read_b128 v[148:151], v147
	ds_read_b128 v[152:155], v147 offset:1024
	ds_read_b128 v[156:159], v147 offset:2048
	ds_read_b128 v[160:163], v147 offset:3072
	v_add_u32_e32 v147, s29, v144
	ds_read_b128 v[172:175], v147
	ds_read_b128 v[176:179], v147 offset:1024
	ds_read_b128 v[180:183], v147 offset:2048
	ds_read_b128 v[184:187], v147 offset:3072
	s_add_u32 s2, s2, 0x80000
	s_addc_u32 s3, s3, 0
	s_mov_b32 m0, s38
	v_lshl_add_u64 v[228:229], s[2:3], 0, v[166:167]
	ds_read_b128 v[188:191], v146 offset:32768
	ds_read_b128 v[192:195], v146 offset:33792
	ds_read_b128 v[196:199], v146 offset:34816
	ds_read_b128 v[200:203], v146 offset:35840
	ds_read_b128 v[204:207], v146 offset:36864
	ds_read_b128 v[208:211], v146 offset:37888
	ds_read_b128 v[212:215], v146 offset:38912
	ds_read_b128 v[216:219], v146 offset:39936
	global_load_lds_dwordx4 v[228:229], off
	v_lshl_add_u64 v[228:229], s[2:3], 0, v[170:171]
	s_mov_b32 m0, s39
	s_nop 0
	global_load_lds_dwordx4 v[228:229], off
	s_waitcnt vmcnt(8)
	s_waitcnt lgkmcnt(0)
	s_barrier
	s_setprio 0
	s_waitcnt lgkmcnt(0)
	v_mfma_f32_16x16x32_bf16 v[126:129], v[188:191], v[148:151], v[126:129]
	v_mfma_f32_16x16x32_bf16 v[114:117], v[188:191], v[156:159], v[114:117]
	v_mfma_f32_16x16x32_bf16 v[122:125], v[196:199], v[148:151], v[122:125]
	v_mfma_f32_16x16x32_bf16 v[106:109], v[196:199], v[156:159], v[106:109]
	v_mfma_f32_16x16x32_bf16 v[118:121], v[204:207], v[148:151], v[118:121]
	v_mfma_f32_16x16x32_bf16 v[102:105], v[204:207], v[156:159], v[102:105]
	v_mfma_f32_16x16x32_bf16 v[110:113], v[212:215], v[148:151], v[110:113]
	v_mfma_f32_16x16x32_bf16 v[98:101], v[212:215], v[156:159], v[98:101]
	v_mfma_f32_16x16x32_bf16 v[126:129], v[192:195], v[152:155], v[126:129]
	v_mfma_f32_16x16x32_bf16 v[114:117], v[192:195], v[160:163], v[114:117]
	v_mfma_f32_16x16x32_bf16 v[122:125], v[200:203], v[152:155], v[122:125]
	v_mfma_f32_16x16x32_bf16 v[106:109], v[200:203], v[160:163], v[106:109]
	v_mfma_f32_16x16x32_bf16 v[118:121], v[208:211], v[152:155], v[118:121]
	v_mfma_f32_16x16x32_bf16 v[102:105], v[208:211], v[160:163], v[102:105]
	v_mfma_f32_16x16x32_bf16 v[110:113], v[216:219], v[152:155], v[110:113]
	v_mfma_f32_16x16x32_bf16 v[98:101], v[216:219], v[160:163], v[98:101]
	v_mfma_f32_16x16x32_bf16 v[94:97], v[188:191], v[172:175], v[94:97]
	v_mfma_f32_16x16x32_bf16 v[82:85], v[188:191], v[180:183], v[82:85]
	v_mfma_f32_16x16x32_bf16 v[90:93], v[196:199], v[172:175], v[90:93]
	v_mfma_f32_16x16x32_bf16 v[74:77], v[196:199], v[180:183], v[74:77]
	v_mfma_f32_16x16x32_bf16 v[86:89], v[204:207], v[172:175], v[86:89]
	v_mfma_f32_16x16x32_bf16 v[70:73], v[204:207], v[180:183], v[70:73]
	v_mfma_f32_16x16x32_bf16 v[78:81], v[212:215], v[172:175], v[78:81]
	v_mfma_f32_16x16x32_bf16 v[66:69], v[212:215], v[180:183], v[66:69]
	v_mfma_f32_16x16x32_bf16 v[94:97], v[192:195], v[176:179], v[94:97]
	v_mfma_f32_16x16x32_bf16 v[82:85], v[192:195], v[184:187], v[82:85]
	v_mfma_f32_16x16x32_bf16 v[90:93], v[200:203], v[176:179], v[90:93]
	v_mfma_f32_16x16x32_bf16 v[74:77], v[200:203], v[184:187], v[74:77]
	v_mfma_f32_16x16x32_bf16 v[86:89], v[208:211], v[176:179], v[86:89]
	v_mfma_f32_16x16x32_bf16 v[70:73], v[208:211], v[184:187], v[70:73]
	v_mfma_f32_16x16x32_bf16 v[78:81], v[216:219], v[176:179], v[78:81]
	v_mfma_f32_16x16x32_bf16 v[66:69], v[216:219], v[184:187], v[66:69]
	s_setprio 1
	s_barrier
	s_add_i32 s2, s28, s20
	v_lshl_add_u64 v[220:221], v[220:221], 0, s[10:11]
	s_mov_b32 m0, s2
	ds_read_b128 v[188:191], v146 offset:49152
	ds_read_b128 v[192:195], v146 offset:50176
	ds_read_b128 v[196:199], v146 offset:51200
	ds_read_b128 v[200:203], v146 offset:52224
	ds_read_b128 v[204:207], v146 offset:53248
	ds_read_b128 v[208:211], v146 offset:54272
	ds_read_b128 v[212:215], v146 offset:55296
	ds_read_b128 v[216:219], v146 offset:56320
	global_load_lds_dwordx4 v[220:221], off
	s_add_i32 m0, s2, 0x2000
	s_add_u32 s2, s34, 0x80080
	v_lshl_add_u64 v[220:221], v[222:223], 0, s[10:11]
	s_addc_u32 s3, s35, 0
	s_add_i32 s28, s29, s20
	global_load_lds_dwordx4 v[220:221], off
	v_lshl_add_u64 v[220:221], s[2:3], 0, v[164:165]
	s_mov_b32 m0, s28
	s_nop 0
	global_load_lds_dwordx4 v[220:221], off
	v_lshl_add_u64 v[220:221], s[2:3], 0, v[168:169]
	s_add_i32 m0, s28, 0x2000
	s_nop 0
	global_load_lds_dwordx4 v[220:221], off
	v_lshl_add_u64 v[220:221], v[224:225], 0, s[10:11]
	s_mov_b32 m0, s43
	s_nop 0
	global_load_lds_dwordx4 v[220:221], off
	v_lshl_add_u64 v[220:221], v[226:227], 0, s[10:11]
	s_mov_b32 m0, s48
	s_nop 0
	global_load_lds_dwordx4 v[220:221], off
	s_waitcnt vmcnt(8)
	s_waitcnt lgkmcnt(0)
	s_barrier
	s_setprio 0
	s_waitcnt lgkmcnt(0)
	v_mfma_f32_16x16x32_bf16 v[62:65], v[188:191], v[148:151], v[62:65]
	v_mfma_f32_16x16x32_bf16 v[50:53], v[188:191], v[156:159], v[50:53]
	v_mfma_f32_16x16x32_bf16 v[58:61], v[196:199], v[148:151], v[58:61]
	v_mfma_f32_16x16x32_bf16 v[42:45], v[196:199], v[156:159], v[42:45]
	v_mfma_f32_16x16x32_bf16 v[54:57], v[204:207], v[148:151], v[54:57]
	v_mfma_f32_16x16x32_bf16 v[38:41], v[204:207], v[156:159], v[38:41]
	v_mfma_f32_16x16x32_bf16 v[46:49], v[212:215], v[148:151], v[46:49]
	v_mfma_f32_16x16x32_bf16 v[34:37], v[212:215], v[156:159], v[34:37]
	v_mfma_f32_16x16x32_bf16 v[62:65], v[192:195], v[152:155], v[62:65]
	v_mfma_f32_16x16x32_bf16 v[50:53], v[192:195], v[160:163], v[50:53]
	v_mfma_f32_16x16x32_bf16 v[58:61], v[200:203], v[152:155], v[58:61]
	v_mfma_f32_16x16x32_bf16 v[42:45], v[200:203], v[160:163], v[42:45]
	v_mfma_f32_16x16x32_bf16 v[54:57], v[208:211], v[152:155], v[54:57]
	v_mfma_f32_16x16x32_bf16 v[38:41], v[208:211], v[160:163], v[38:41]
	v_mfma_f32_16x16x32_bf16 v[46:49], v[216:219], v[152:155], v[46:49]
	v_mfma_f32_16x16x32_bf16 v[34:37], v[216:219], v[160:163], v[34:37]
	v_mfma_f32_16x16x32_bf16 v[30:33], v[188:191], v[172:175], v[30:33]
	v_mfma_f32_16x16x32_bf16 v[18:21], v[188:191], v[180:183], v[18:21]
	v_mfma_f32_16x16x32_bf16 v[26:29], v[196:199], v[172:175], v[26:29]
	v_mfma_f32_16x16x32_bf16 v[10:13], v[196:199], v[180:183], v[10:13]
	v_mfma_f32_16x16x32_bf16 v[22:25], v[204:207], v[172:175], v[22:25]
	v_mfma_f32_16x16x32_bf16 v[6:9], v[204:207], v[180:183], v[6:9]
	v_mfma_f32_16x16x32_bf16 v[14:17], v[212:215], v[172:175], v[14:17]
	v_mfma_f32_16x16x32_bf16 v[2:5], v[212:215], v[180:183], v[2:5]
	v_mfma_f32_16x16x32_bf16 v[30:33], v[192:195], v[176:179], v[30:33]
	v_mfma_f32_16x16x32_bf16 v[18:21], v[192:195], v[184:187], v[18:21]
	v_mfma_f32_16x16x32_bf16 v[26:29], v[200:203], v[176:179], v[26:29]
	v_mfma_f32_16x16x32_bf16 v[10:13], v[200:203], v[184:187], v[10:13]
	v_mfma_f32_16x16x32_bf16 v[22:25], v[208:211], v[176:179], v[22:25]
	v_mfma_f32_16x16x32_bf16 v[6:9], v[208:211], v[184:187], v[6:9]
	v_mfma_f32_16x16x32_bf16 v[14:17], v[216:219], v[176:179], v[14:17]
	v_mfma_f32_16x16x32_bf16 v[2:5], v[216:219], v[184:187], v[2:5]
	s_setprio 1
	s_barrier
	s_add_i32 s53, s53, 2
	s_cmp_gt_u32 s53, 29
	s_mov_b64 s[28:29], s[30:31]
	s_cbranch_scc0 .LBB0_346
	s_and_b64 vcc, exec, s[12:13]
	s_cbranch_vccz .LBB0_349
	s_barrier

.LBB0_712:
	ds_read_b128 v[140:143], v205
	ds_read_b128 v[144:147], v205 offset:1024
	ds_read_b128 v[148:151], v205 offset:2048
	ds_read_b128 v[152:155], v205 offset:3072
	ds_read_b128 v[182:185], v207
	ds_read_b128 v[186:189], v207 offset:1024
	ds_read_b128 v[196:199], v207 offset:2048
	ds_read_b128 v[212:215], v207 offset:3072
	s_mov_b64 s[72:73], s[56:57]
	s_add_u32 s2, s69, s72
	s_addc_u32 s74, s70, s73
	s_add_u32 s56, s72, 0x100
	s_addc_u32 s57, s73, 0
	s_cmpk_eq_i32 s72, 0xf00
	s_cselect_b64 s[58:59], -1, 0
	s_and_b64 s[60:61], s[58:59], exec
	s_cselect_b32 s61, s35, s74
	s_cselect_b32 s60, s68, s2
	s_cselect_b32 s2, 0, s56
	v_lshl_add_u64 v[4:5], v[136:137], 0, s[72:73]
	s_add_i32 m0, s42, 0xc000
	ds_read_b128 v[216:219], v210
	ds_read_b128 v[220:223], v210 offset:1024
	ds_read_b128 v[224:227], v210 offset:2048
	ds_read_b128 v[228:231], v210 offset:3072
	ds_read_b128 v[232:235], v210 offset:4096
	ds_read_b128 v[236:239], v210 offset:5120
	ds_read_b128 v[244:247], v210 offset:6144
	ds_read_b128 v[248:251], v210 offset:7168
	global_load_lds_dwordx4 v[4:5], off
	v_lshl_add_u64 v[4:5], v[134:135], 0, s[72:73]
	s_add_i32 m0, s42, 0xe000
	s_nop 0
	global_load_lds_dwordx4 v[4:5], off
	s_waitcnt vmcnt(8)
	s_waitcnt lgkmcnt(0)
	s_barrier
	s_setprio 0
	s_waitcnt lgkmcnt(0)
	v_mfma_f32_16x16x32_bf16 v[130:133], v[140:143], v[216:219], v[130:133]
	v_mfma_f32_16x16x32_bf16 v[126:129], v[148:151], v[216:219], v[126:129]
	v_mfma_f32_16x16x32_bf16 v[114:117], v[140:143], v[224:227], v[114:117]
	v_mfma_f32_16x16x32_bf16 v[110:113], v[148:151], v[224:227], v[110:113]
	v_mfma_f32_16x16x32_bf16 v[98:101], v[140:143], v[232:235], v[98:101]
	v_mfma_f32_16x16x32_bf16 v[94:97], v[148:151], v[232:235], v[94:97]
	v_mfma_f32_16x16x32_bf16 v[82:85], v[140:143], v[244:247], v[82:85]
	v_mfma_f32_16x16x32_bf16 v[78:81], v[148:151], v[244:247], v[78:81]
	v_mfma_f32_16x16x32_bf16 v[130:133], v[144:147], v[220:223], v[130:133]
	v_mfma_f32_16x16x32_bf16 v[126:129], v[152:155], v[220:223], v[126:129]
	v_mfma_f32_16x16x32_bf16 v[114:117], v[144:147], v[228:231], v[114:117]
	v_mfma_f32_16x16x32_bf16 v[110:113], v[152:155], v[228:231], v[110:113]
	v_mfma_f32_16x16x32_bf16 v[98:101], v[144:147], v[236:239], v[98:101]
	v_mfma_f32_16x16x32_bf16 v[94:97], v[152:155], v[236:239], v[94:97]
	v_mfma_f32_16x16x32_bf16 v[82:85], v[144:147], v[248:251], v[82:85]
	v_mfma_f32_16x16x32_bf16 v[78:81], v[152:155], v[248:251], v[78:81]
	v_mfma_f32_16x16x32_bf16 v[122:125], v[182:185], v[216:219], v[122:125]
	v_mfma_f32_16x16x32_bf16 v[118:121], v[196:199], v[216:219], v[118:121]
	v_mfma_f32_16x16x32_bf16 v[106:109], v[182:185], v[224:227], v[106:109]
	v_mfma_f32_16x16x32_bf16 v[102:105], v[196:199], v[224:227], v[102:105]
	v_mfma_f32_16x16x32_bf16 v[90:93], v[182:185], v[232:235], v[90:93]
	v_mfma_f32_16x16x32_bf16 v[86:89], v[196:199], v[232:235], v[86:89]
	v_mfma_f32_16x16x32_bf16 v[74:77], v[182:185], v[244:247], v[74:77]
	v_mfma_f32_16x16x32_bf16 v[70:73], v[196:199], v[244:247], v[70:73]
	v_mfma_f32_16x16x32_bf16 v[122:125], v[186:189], v[220:223], v[122:125]
	v_mfma_f32_16x16x32_bf16 v[118:121], v[212:215], v[220:223], v[118:121]
	v_mfma_f32_16x16x32_bf16 v[106:109], v[186:189], v[228:231], v[106:109]
	v_mfma_f32_16x16x32_bf16 v[102:105], v[212:215], v[228:231], v[102:105]
	v_mfma_f32_16x16x32_bf16 v[90:93], v[186:189], v[236:239], v[90:93]
	v_mfma_f32_16x16x32_bf16 v[86:89], v[212:215], v[236:239], v[86:89]
	v_mfma_f32_16x16x32_bf16 v[74:77], v[186:189], v[248:251], v[74:77]
	v_mfma_f32_16x16x32_bf16 v[70:73], v[212:215], v[248:251], v[70:73]
	s_setprio 1
	s_barrier
	s_add_i32 s72, s63, s15
	v_lshl_add_u64 v[156:157], s[60:61], 0, v[160:161]
	s_mov_b32 m0, s72
	ds_read_b128 v[216:219], v210 offset:16384
	ds_read_b128 v[220:223], v210 offset:17408
	ds_read_b128 v[224:227], v210 offset:18432
	ds_read_b128 v[228:231], v210 offset:19456
	ds_read_b128 v[232:235], v210 offset:20480
	ds_read_b128 v[236:239], v210 offset:21504
	ds_read_b128 v[244:247], v210 offset:22528
	ds_read_b128 v[248:251], v210 offset:23552
	global_load_lds_dwordx4 v[156:157], off
	s_add_i32 m0, s72, 0x2000
	s_add_u32 s72, s60, 0x80000
	v_lshl_add_u64 v[178:179], s[60:61], 0, v[164:165]
	s_addc_u32 s73, s61, 0
	s_add_i32 s74, s64, s15
	global_load_lds_dwordx4 v[178:179], off
	v_lshl_add_u64 v[4:5], s[72:73], 0, v[160:161]
	s_mov_b32 m0, s74
	s_nop 0
	global_load_lds_dwordx4 v[4:5], off
	v_lshl_add_u64 v[4:5], s[72:73], 0, v[164:165]
	s_add_i32 m0, s74, 0x2000
	s_and_b64 s[72:73], s[10:11], s[58:59]
	s_and_b64 s[72:73], s[72:73], exec
	s_cselect_b32 s72, s38, s54
	s_cselect_b32 s73, s39, s55
	s_add_u32 s72, s72, s2
	s_addc_u32 s73, s73, 0
	global_load_lds_dwordx4 v[4:5], off
	v_lshl_add_u64 v[192:193], s[72:73], 0, v[158:159]
	s_mov_b32 m0, s42
	v_lshl_add_u64 v[202:203], s[72:73], 0, v[162:163]
	global_load_lds_dwordx4 v[192:193], off
	s_mov_b32 m0, s43
	s_nop 0
	global_load_lds_dwordx4 v[202:203], off
	s_waitcnt vmcnt(8)
	s_waitcnt lgkmcnt(0)
	s_barrier
	s_setprio 0
	s_waitcnt lgkmcnt(0)
	v_mfma_f32_16x16x32_bf16 v[66:69], v[140:143], v[216:219], v[66:69]
	v_mfma_f32_16x16x32_bf16 v[62:65], v[148:151], v[216:219], v[62:65]
	v_mfma_f32_16x16x32_bf16 v[50:53], v[140:143], v[224:227], v[50:53]
	v_mfma_f32_16x16x32_bf16 v[46:49], v[148:151], v[224:227], v[46:49]
	v_mfma_f32_16x16x32_bf16 v[34:37], v[140:143], v[232:235], v[34:37]
	v_mfma_f32_16x16x32_bf16 v[30:33], v[148:151], v[232:235], v[30:33]
	v_mfma_f32_16x16x32_bf16 v[18:21], v[140:143], v[244:247], v[18:21]
	v_mfma_f32_16x16x32_bf16 v[14:17], v[148:151], v[244:247], v[14:17]
	v_mfma_f32_16x16x32_bf16 v[66:69], v[144:147], v[220:223], v[66:69]
	v_mfma_f32_16x16x32_bf16 v[62:65], v[152:155], v[220:223], v[62:65]
	v_mfma_f32_16x16x32_bf16 v[50:53], v[144:147], v[228:231], v[50:53]
	v_mfma_f32_16x16x32_bf16 v[46:49], v[152:155], v[228:231], v[46:49]
	v_mfma_f32_16x16x32_bf16 v[34:37], v[144:147], v[236:239], v[34:37]
	v_mfma_f32_16x16x32_bf16 v[30:33], v[152:155], v[236:239], v[30:33]
	v_mfma_f32_16x16x32_bf16 v[18:21], v[144:147], v[248:251], v[18:21]
	v_mfma_f32_16x16x32_bf16 v[14:17], v[152:155], v[248:251], v[14:17]
	v_mfma_f32_16x16x32_bf16 v[58:61], v[182:185], v[216:219], v[58:61]
	v_mfma_f32_16x16x32_bf16 v[54:57], v[196:199], v[216:219], v[54:57]
	v_mfma_f32_16x16x32_bf16 v[42:45], v[182:185], v[224:227], v[42:45]
	v_mfma_f32_16x16x32_bf16 v[38:41], v[196:199], v[224:227], v[38:41]
	v_mfma_f32_16x16x32_bf16 v[26:29], v[182:185], v[232:235], v[26:29]
	v_mfma_f32_16x16x32_bf16 v[22:25], v[196:199], v[232:235], v[22:25]
	v_mfma_f32_16x16x32_bf16 v[10:13], v[182:185], v[244:247], v[10:13]
	v_mfma_f32_16x16x32_bf16 v[4:7], v[196:199], v[244:247], v[6:9]
	v_mfma_f32_16x16x32_bf16 v[58:61], v[186:189], v[220:223], v[58:61]
	v_mfma_f32_16x16x32_bf16 v[54:57], v[212:215], v[220:223], v[54:57]
	v_mfma_f32_16x16x32_bf16 v[42:45], v[186:189], v[228:231], v[42:45]
	v_mfma_f32_16x16x32_bf16 v[38:41], v[212:215], v[228:231], v[38:41]
	v_mfma_f32_16x16x32_bf16 v[26:29], v[186:189], v[236:239], v[26:29]
	v_mfma_f32_16x16x32_bf16 v[22:25], v[212:215], v[236:239], v[22:25]
	v_mfma_f32_16x16x32_bf16 v[10:13], v[186:189], v[248:251], v[10:13]
	v_mfma_f32_16x16x32_bf16 v[4:7], v[212:215], v[248:251], v[4:7]
	s_setprio 1
	s_barrier
	s_add_i32 s2, 0, 0x18000
	v_add_u32_e32 v3, s2, v177
	s_add_i32 s74, 0, 0x1c000
	ds_read_b128 v[140:143], v3
	ds_read_b128 v[144:147], v3 offset:1024
	ds_read_b128 v[148:151], v3 offset:2048
	ds_read_b128 v[152:155], v3 offset:3072
	v_add_u32_e32 v3, s74, v177
	ds_read_b128 v[182:185], v3
	ds_read_b128 v[186:189], v3 offset:1024
	ds_read_b128 v[196:199], v3 offset:2048
	ds_read_b128 v[212:215], v3 offset:3072
	s_add_u32 s72, s72, 0x80000
	s_addc_u32 s73, s73, 0
	s_mov_b32 m0, s48
	v_lshl_add_u64 v[8:9], s[72:73], 0, v[158:159]
	ds_read_b128 v[216:219], v210 offset:32768
	ds_read_b128 v[220:223], v210 offset:33792
	ds_read_b128 v[224:227], v210 offset:34816
	ds_read_b128 v[228:231], v210 offset:35840
	ds_read_b128 v[232:235], v210 offset:36864
	ds_read_b128 v[236:239], v210 offset:37888
	ds_read_b128 v[244:247], v210 offset:38912
	ds_read_b128 v[248:251], v210 offset:39936
	global_load_lds_dwordx4 v[8:9], off
	v_lshl_add_u64 v[8:9], s[72:73], 0, v[162:163]
	s_mov_b32 m0, s49
	s_nop 0
	global_load_lds_dwordx4 v[8:9], off
	s_waitcnt vmcnt(8)
	s_waitcnt lgkmcnt(0)
	s_barrier
	s_setprio 0
	s_waitcnt lgkmcnt(0)
	v_mfma_f32_16x16x32_bf16 v[130:133], v[140:143], v[216:219], v[130:133]
	v_mfma_f32_16x16x32_bf16 v[126:129], v[148:151], v[216:219], v[126:129]
	v_mfma_f32_16x16x32_bf16 v[114:117], v[140:143], v[224:227], v[114:117]
	v_mfma_f32_16x16x32_bf16 v[110:113], v[148:151], v[224:227], v[110:113]
	v_mfma_f32_16x16x32_bf16 v[98:101], v[140:143], v[232:235], v[98:101]
	v_mfma_f32_16x16x32_bf16 v[94:97], v[148:151], v[232:235], v[94:97]
	v_mfma_f32_16x16x32_bf16 v[82:85], v[140:143], v[244:247], v[82:85]
	v_mfma_f32_16x16x32_bf16 v[78:81], v[148:151], v[244:247], v[78:81]
	v_mfma_f32_16x16x32_bf16 v[130:133], v[144:147], v[220:223], v[130:133]
	v_mfma_f32_16x16x32_bf16 v[126:129], v[152:155], v[220:223], v[126:129]
	v_mfma_f32_16x16x32_bf16 v[114:117], v[144:147], v[228:231], v[114:117]
	v_mfma_f32_16x16x32_bf16 v[110:113], v[152:155], v[228:231], v[110:113]
	v_mfma_f32_16x16x32_bf16 v[98:101], v[144:147], v[236:239], v[98:101]
	v_mfma_f32_16x16x32_bf16 v[94:97], v[152:155], v[236:239], v[94:97]
	v_mfma_f32_16x16x32_bf16 v[82:85], v[144:147], v[248:251], v[82:85]
	v_mfma_f32_16x16x32_bf16 v[78:81], v[152:155], v[248:251], v[78:81]
	v_mfma_f32_16x16x32_bf16 v[122:125], v[182:185], v[216:219], v[122:125]
	v_mfma_f32_16x16x32_bf16 v[118:121], v[196:199], v[216:219], v[118:121]
	v_mfma_f32_16x16x32_bf16 v[106:109], v[182:185], v[224:227], v[106:109]
	v_mfma_f32_16x16x32_bf16 v[102:105], v[196:199], v[224:227], v[102:105]
	v_mfma_f32_16x16x32_bf16 v[90:93], v[182:185], v[232:235], v[90:93]
	v_mfma_f32_16x16x32_bf16 v[86:89], v[196:199], v[232:235], v[86:89]
	v_mfma_f32_16x16x32_bf16 v[74:77], v[182:185], v[244:247], v[74:77]
	v_mfma_f32_16x16x32_bf16 v[70:73], v[196:199], v[244:247], v[70:73]
	v_mfma_f32_16x16x32_bf16 v[122:125], v[186:189], v[220:223], v[122:125]
	v_mfma_f32_16x16x32_bf16 v[118:121], v[212:215], v[220:223], v[118:121]
	v_mfma_f32_16x16x32_bf16 v[106:109], v[186:189], v[228:231], v[106:109]
	v_mfma_f32_16x16x32_bf16 v[102:105], v[212:215], v[228:231], v[102:105]
	v_mfma_f32_16x16x32_bf16 v[90:93], v[186:189], v[236:239], v[90:93]
	v_mfma_f32_16x16x32_bf16 v[86:89], v[212:215], v[236:239], v[86:89]
	v_mfma_f32_16x16x32_bf16 v[74:77], v[186:189], v[248:251], v[74:77]
	v_mfma_f32_16x16x32_bf16 v[70:73], v[212:215], v[248:251], v[70:73]
	s_setprio 1
	s_barrier
	s_add_i32 s2, s2, s15
	v_lshl_add_u64 v[8:9], v[156:157], 0, s[28:29]
	s_mov_b32 m0, s2
	ds_read_b128 v[216:219], v210 offset:49152
	ds_read_b128 v[220:223], v210 offset:50176
	ds_read_b128 v[224:227], v210 offset:51200
	ds_read_b128 v[228:231], v210 offset:52224
	ds_read_b128 v[232:235], v210 offset:53248
	ds_read_b128 v[236:239], v210 offset:54272
	ds_read_b128 v[244:247], v210 offset:55296
	ds_read_b128 v[248:251], v210 offset:56320
	global_load_lds_dwordx4 v[8:9], off
	s_add_i32 m0, s2, 0x2000
	s_add_u32 s60, s60, 0x80080
	v_lshl_add_u64 v[8:9], v[178:179], 0, s[28:29]
	s_addc_u32 s61, s61, 0
	s_add_i32 s2, s74, s15
	global_load_lds_dwordx4 v[8:9], off
	v_lshl_add_u64 v[8:9], s[60:61], 0, v[160:161]
	s_mov_b32 m0, s2
	s_nop 0
	global_load_lds_dwordx4 v[8:9], off
	v_lshl_add_u64 v[8:9], s[60:61], 0, v[164:165]
	s_add_i32 m0, s2, 0x2000
	s_nop 0
	global_load_lds_dwordx4 v[8:9], off
	v_lshl_add_u64 v[8:9], v[192:193], 0, s[28:29]
	s_mov_b32 m0, s51
	s_nop 0
	global_load_lds_dwordx4 v[8:9], off
	v_lshl_add_u64 v[8:9], v[202:203], 0, s[28:29]
	s_mov_b32 m0, s52
	s_nop 0
	global_load_lds_dwordx4 v[8:9], off
	s_waitcnt vmcnt(8)
	s_waitcnt lgkmcnt(0)
	s_barrier
	s_setprio 0
	s_waitcnt lgkmcnt(0)
	v_mfma_f32_16x16x32_bf16 v[66:69], v[140:143], v[216:219], v[66:69]
	v_mfma_f32_16x16x32_bf16 v[62:65], v[148:151], v[216:219], v[62:65]
	v_mfma_f32_16x16x32_bf16 v[50:53], v[140:143], v[224:227], v[50:53]
	v_mfma_f32_16x16x32_bf16 v[46:49], v[148:151], v[224:227], v[46:49]
	v_mfma_f32_16x16x32_bf16 v[34:37], v[140:143], v[232:235], v[34:37]
	v_mfma_f32_16x16x32_bf16 v[30:33], v[148:151], v[232:235], v[30:33]
	v_mfma_f32_16x16x32_bf16 v[18:21], v[140:143], v[244:247], v[18:21]
	v_mfma_f32_16x16x32_bf16 v[14:17], v[148:151], v[244:247], v[14:17]
	v_mfma_f32_16x16x32_bf16 v[66:69], v[144:147], v[220:223], v[66:69]
	v_mfma_f32_16x16x32_bf16 v[62:65], v[152:155], v[220:223], v[62:65]
	v_mfma_f32_16x16x32_bf16 v[50:53], v[144:147], v[228:231], v[50:53]
	v_mfma_f32_16x16x32_bf16 v[46:49], v[152:155], v[228:231], v[46:49]
	v_mfma_f32_16x16x32_bf16 v[34:37], v[144:147], v[236:239], v[34:37]
	v_mfma_f32_16x16x32_bf16 v[30:33], v[152:155], v[236:239], v[30:33]
	v_mfma_f32_16x16x32_bf16 v[18:21], v[144:147], v[248:251], v[18:21]
	v_mfma_f32_16x16x32_bf16 v[14:17], v[152:155], v[248:251], v[14:17]
	v_mfma_f32_16x16x32_bf16 v[58:61], v[182:185], v[216:219], v[58:61]
	v_mfma_f32_16x16x32_bf16 v[54:57], v[196:199], v[216:219], v[54:57]
	v_mfma_f32_16x16x32_bf16 v[42:45], v[182:185], v[224:227], v[42:45]
	v_mfma_f32_16x16x32_bf16 v[38:41], v[196:199], v[224:227], v[38:41]
	v_mfma_f32_16x16x32_bf16 v[26:29], v[182:185], v[232:235], v[26:29]
	v_mfma_f32_16x16x32_bf16 v[22:25], v[196:199], v[232:235], v[22:25]
	v_mfma_f32_16x16x32_bf16 v[8:11], v[182:185], v[244:247], v[10:13]
	v_mfma_f32_16x16x32_bf16 v[4:7], v[196:199], v[244:247], v[4:7]
	v_mfma_f32_16x16x32_bf16 v[58:61], v[186:189], v[220:223], v[58:61]
	v_mfma_f32_16x16x32_bf16 v[54:57], v[212:215], v[220:223], v[54:57]
	v_mfma_f32_16x16x32_bf16 v[42:45], v[186:189], v[228:231], v[42:45]
	v_mfma_f32_16x16x32_bf16 v[38:41], v[212:215], v[228:231], v[38:41]
	v_mfma_f32_16x16x32_bf16 v[26:29], v[186:189], v[236:239], v[26:29]
	v_mfma_f32_16x16x32_bf16 v[22:25], v[212:215], v[236:239], v[22:25]
	v_mfma_f32_16x16x32_bf16 v[10:13], v[186:189], v[248:251], v[8:11]
	v_mfma_f32_16x16x32_bf16 v[6:9], v[212:215], v[248:251], v[4:7]
	s_setprio 1
	s_barrier
	s_add_i32 s2, s71, 4
	s_and_b32 s2, s2, 6
	s_cmp_lg_u32 s2, 0
	s_cselect_b64 s[60:61], -1, 0
	s_or_b64 s[58:59], s[58:59], s[60:61]
	s_and_b64 vcc, exec, s[58:59]
	s_cbranch_vccnz .LBB0_711
	ds_read2st64_b32 v[4:5], v138 offset1:1
	ds_read2st64_b32 v[140:141], v138 offset0:2 offset1:3
	ds_read2st64_b32 v[142:143], v138 offset0:8 offset1:9
	ds_read2st64_b32 v[144:145], v138 offset0:10 offset1:11
	s_waitcnt lgkmcnt(0)
	v_pk_mul_f32 v[132:133], v[132:133], v[4:5] op_sel_hi:[1,0]
	v_pk_mul_f32 v[130:131], v[130:131], v[4:5] op_sel_hi:[1,0]
	v_pk_mul_f32 v[128:129], v[128:129], v[4:5] op_sel_hi:[1,0]
	v_pk_mul_f32 v[126:127], v[126:127], v[4:5] op_sel_hi:[1,0]
	v_pk_mul_f32 v[124:125], v[124:125], v[4:5] op_sel_hi:[1,0]
	v_pk_mul_f32 v[122:123], v[122:123], v[4:5] op_sel_hi:[1,0]
	v_pk_mul_f32 v[120:121], v[120:121], v[4:5] op_sel_hi:[1,0]
	v_pk_mul_f32 v[118:119], v[118:119], v[4:5] op_sel_hi:[1,0]
	v_mov_b32_e32 v4, v5
	v_pk_mul_f32 v[116:117], v[116:117], v[4:5] op_sel_hi:[1,0]
	v_pk_mul_f32 v[114:115], v[114:115], v[4:5] op_sel_hi:[1,0]
	v_pk_mul_f32 v[112:113], v[112:113], v[4:5] op_sel_hi:[1,0]
	v_pk_mul_f32 v[110:111], v[110:111], v[4:5] op_sel_hi:[1,0]
	v_pk_mul_f32 v[108:109], v[108:109], v[4:5] op_sel_hi:[1,0]
	v_pk_mul_f32 v[106:107], v[106:107], v[4:5] op_sel_hi:[1,0]
	v_pk_mul_f32 v[104:105], v[104:105], v[4:5] op_sel_hi:[1,0]
	v_pk_mul_f32 v[102:103], v[102:103], v[4:5] op_sel_hi:[1,0]
	v_mov_b32_e32 v4, v141
	v_pk_mul_f32 v[84:85], v[84:85], v[4:5] op_sel_hi:[1,0]
	v_pk_mul_f32 v[82:83], v[82:83], v[4:5] op_sel_hi:[1,0]
	v_pk_mul_f32 v[80:81], v[80:81], v[4:5] op_sel_hi:[1,0]
	v_pk_mul_f32 v[78:79], v[78:79], v[4:5] op_sel_hi:[1,0]
	v_pk_mul_f32 v[76:77], v[76:77], v[4:5] op_sel_hi:[1,0]
	v_pk_mul_f32 v[74:75], v[74:75], v[4:5] op_sel_hi:[1,0]
	v_pk_mul_f32 v[72:73], v[72:73], v[4:5] op_sel_hi:[1,0]
	v_pk_mul_f32 v[70:71], v[70:71], v[4:5] op_sel_hi:[1,0]
	v_mov_b32_e32 v4, v143
	v_pk_mul_f32 v[52:53], v[52:53], v[4:5] op_sel_hi:[1,0]
	v_pk_mul_f32 v[50:51], v[50:51], v[4:5] op_sel_hi:[1,0]
	v_pk_mul_f32 v[48:49], v[48:49], v[4:5] op_sel_hi:[1,0]
	v_pk_mul_f32 v[46:47], v[46:47], v[4:5] op_sel_hi:[1,0]
	v_pk_mul_f32 v[44:45], v[44:45], v[4:5] op_sel_hi:[1,0]
	v_pk_mul_f32 v[42:43], v[42:43], v[4:5] op_sel_hi:[1,0]
	v_pk_mul_f32 v[40:41], v[40:41], v[4:5] op_sel_hi:[1,0]
	v_pk_mul_f32 v[38:39], v[38:39], v[4:5] op_sel_hi:[1,0]
	v_mov_b32_e32 v4, v145
	v_pk_mul_f32 v[100:101], v[100:101], v[140:141] op_sel_hi:[1,0]
	v_pk_mul_f32 v[98:99], v[98:99], v[140:141] op_sel_hi:[1,0]
	v_pk_mul_f32 v[96:97], v[96:97], v[140:141] op_sel_hi:[1,0]
	v_pk_mul_f32 v[94:95], v[94:95], v[140:141] op_sel_hi:[1,0]
	v_pk_mul_f32 v[92:93], v[92:93], v[140:141] op_sel_hi:[1,0]
	v_pk_mul_f32 v[90:91], v[90:91], v[140:141] op_sel_hi:[1,0]
	v_pk_mul_f32 v[88:89], v[88:89], v[140:141] op_sel_hi:[1,0]
	v_pk_mul_f32 v[86:87], v[86:87], v[140:141] op_sel_hi:[1,0]
	v_pk_mul_f32 v[68:69], v[68:69], v[142:143] op_sel_hi:[1,0]
	v_pk_mul_f32 v[66:67], v[66:67], v[142:143] op_sel_hi:[1,0]
	v_pk_mul_f32 v[64:65], v[64:65], v[142:143] op_sel_hi:[1,0]
	v_pk_mul_f32 v[62:63], v[62:63], v[142:143] op_sel_hi:[1,0]
	v_pk_mul_f32 v[60:61], v[60:61], v[142:143] op_sel_hi:[1,0]
	v_pk_mul_f32 v[58:59], v[58:59], v[142:143] op_sel_hi:[1,0]
	v_pk_mul_f32 v[56:57], v[56:57], v[142:143] op_sel_hi:[1,0]
	v_pk_mul_f32 v[54:55], v[54:55], v[142:143] op_sel_hi:[1,0]
	v_pk_mul_f32 v[36:37], v[36:37], v[144:145] op_sel_hi:[1,0]
	v_pk_mul_f32 v[34:35], v[34:35], v[144:145] op_sel_hi:[1,0]
	v_pk_mul_f32 v[32:33], v[32:33], v[144:145] op_sel_hi:[1,0]
	v_pk_mul_f32 v[30:31], v[30:31], v[144:145] op_sel_hi:[1,0]
	v_pk_mul_f32 v[28:29], v[28:29], v[144:145] op_sel_hi:[1,0]
	v_pk_mul_f32 v[26:27], v[26:27], v[144:145] op_sel_hi:[1,0]
	v_pk_mul_f32 v[24:25], v[24:25], v[144:145] op_sel_hi:[1,0]
	v_pk_mul_f32 v[22:23], v[22:23], v[144:145] op_sel_hi:[1,0]
	v_pk_mul_f32 v[20:21], v[20:21], v[4:5] op_sel_hi:[1,0]
	v_pk_mul_f32 v[18:19], v[18:19], v[4:5] op_sel_hi:[1,0]
	v_pk_mul_f32 v[16:17], v[16:17], v[4:5] op_sel_hi:[1,0]
	v_pk_mul_f32 v[14:15], v[14:15], v[4:5] op_sel_hi:[1,0]
	v_pk_mul_f32 v[12:13], v[12:13], v[4:5] op_sel_hi:[1,0]
	v_pk_mul_f32 v[10:11], v[10:11], v[4:5] op_sel_hi:[1,0]
	v_pk_mul_f32 v[8:9], v[8:9], v[4:5] op_sel_hi:[1,0]
	v_pk_mul_f32 v[6:7], v[6:7], v[4:5] op_sel_hi:[1,0]
	s_branch .LBB0_711

.LBB0_810:
.LBB0_811:
	s_setprio 0
	s_waitcnt lgkmcnt(0)
	v_mfma_f32_16x16x32_bf16 v[58:61], v[66:69], v[106:109], v[58:61]
	v_mfma_f32_16x16x32_bf16 v[50:53], v[74:77], v[106:109], v[50:53]
	v_mfma_f32_16x16x32_bf16 v[34:37], v[66:69], v[98:101], v[34:37]
	v_mfma_f32_16x16x32_bf16 v[26:29], v[74:77], v[98:101], v[26:29]
	v_mfma_f32_16x16x32_bf16 v[14:17], v[66:69], v[90:93], v[14:17]
	v_mfma_f32_16x16x32_bf16 v[10:13], v[74:77], v[90:93], v[10:13]
	v_mfma_f32_16x16x32_bf16 v[6:9], v[66:69], v[82:85], v[6:9]
	v_mfma_f32_16x16x32_bf16 v[2:5], v[74:77], v[82:85], v[2:5]
	v_mfma_f32_16x16x32_bf16 v[58:61], v[70:73], v[110:113], v[58:61]
	v_mfma_f32_16x16x32_bf16 v[50:53], v[78:81], v[110:113], v[50:53]
	v_mfma_f32_16x16x32_bf16 v[34:37], v[70:73], v[102:105], v[34:37]
	v_mfma_f32_16x16x32_bf16 v[26:29], v[78:81], v[102:105], v[26:29]
	v_mfma_f32_16x16x32_bf16 v[14:17], v[70:73], v[94:97], v[14:17]
	v_mfma_f32_16x16x32_bf16 v[10:13], v[78:81], v[94:97], v[10:13]
	v_mfma_f32_16x16x32_bf16 v[6:9], v[70:73], v[86:89], v[6:9]
	v_mfma_f32_16x16x32_bf16 v[2:5], v[78:81], v[86:89], v[2:5]
	s_setprio 1
	s_barrier
	s_add_i32 s73, s73, 2
	s_cmp_gt_u32 s73, 13
	s_cbranch_scc1 .LBB0_815
.LBB0_812:
	s_mov_b64 s[56:57], s[38:39]
	s_add_u32 s74, s71, s56
	s_addc_u32 s75, s72, s57
	s_add_u32 s38, s56, 0x100
	s_addc_u32 s39, s57, 0
	s_cmp_eq_u32 s73, 12
	s_cselect_b64 s[40:41], -1, 0
	s_and_b64 s[54:55], s[40:41], exec
	s_cselect_b32 s75, s27, s75
	s_cselect_b32 s74, s29, s74
	s_cselect_b32 s54, 0, s38
	s_add_i32 s81, s68, s43
	s_add_i32 m0, s48, 0xc000
	s_add_i32 s80, s48, 0xe000
	s_add_i32 s82, s81, 0x2000
	s_add_u32 s76, s74, 0x80000
	s_addc_u32 s77, s75, 0
	s_and_b64 s[40:41], s[6:7], s[40:41]
	s_and_b64 s[40:41], s[40:41], exec
	s_cselect_b32 s41, s30, s14
	s_cselect_b32 s40, s31, s15
	s_add_u32 s78, s41, s54
	ds_read_b128 v[66:69], v135
	ds_read_b128 v[70:73], v135 offset:1024
	ds_read_b128 v[74:77], v135 offset:2048
	ds_read_b128 v[78:81], v135 offset:3072
	s_addc_u32 s79, s40, 0
	s_add_i32 s83, 0, 0x18000
	s_add_u32 s54, s78, 0x80000
	s_addc_u32 s55, s79, 0
	s_add_i32 s84, s83, s43
	s_add_i32 s85, s84, 0x2000
	s_add_u32 s40, s74, 0x80080
	s_addc_u32 s41, s75, 0
	s_cmp_lg_u32 s73, 12
	v_lshl_add_u64 v[138:139], v[128:129], 0, s[56:57]
	ds_read_b128 v[82:85], v136
	ds_read_b128 v[86:89], v136 offset:1024
	ds_read_b128 v[90:93], v136 offset:2048
	ds_read_b128 v[94:97], v136 offset:3072
	ds_read_b128 v[98:101], v136 offset:4096
	ds_read_b128 v[102:105], v136 offset:5120
	ds_read_b128 v[106:109], v136 offset:6144
	ds_read_b128 v[110:113], v136 offset:7168
	global_load_lds_dwordx4 v[138:139], off
	v_lshl_add_u64 v[138:139], v[130:131], 0, s[56:57]
	s_mov_b32 m0, s80
	s_nop 0
	global_load_lds_dwordx4 v[138:139], off
	s_waitcnt vmcnt(8)
	s_waitcnt lgkmcnt(0)
	s_barrier
	s_setprio 0
	s_waitcnt lgkmcnt(0)
	v_mfma_f32_16x16x32_bf16 v[62:65], v[66:69], v[82:85], v[62:65]
	v_mfma_f32_16x16x32_bf16 v[54:57], v[74:77], v[82:85], v[54:57]
	v_mfma_f32_16x16x32_bf16 v[46:49], v[66:69], v[90:93], v[46:49]
	v_mfma_f32_16x16x32_bf16 v[42:45], v[74:77], v[90:93], v[42:45]
	v_mfma_f32_16x16x32_bf16 v[38:41], v[66:69], v[98:101], v[38:41]
	v_mfma_f32_16x16x32_bf16 v[30:33], v[74:77], v[98:101], v[30:33]
	v_mfma_f32_16x16x32_bf16 v[22:25], v[66:69], v[106:109], v[22:25]
	v_mfma_f32_16x16x32_bf16 v[18:21], v[74:77], v[106:109], v[18:21]
	v_mfma_f32_16x16x32_bf16 v[62:65], v[70:73], v[86:89], v[62:65]
	v_mfma_f32_16x16x32_bf16 v[54:57], v[78:81], v[86:89], v[54:57]
	v_mfma_f32_16x16x32_bf16 v[46:49], v[70:73], v[94:97], v[46:49]
	v_mfma_f32_16x16x32_bf16 v[42:45], v[78:81], v[94:97], v[42:45]
	v_mfma_f32_16x16x32_bf16 v[38:41], v[70:73], v[102:105], v[38:41]
	v_mfma_f32_16x16x32_bf16 v[30:33], v[78:81], v[102:105], v[30:33]
	v_mfma_f32_16x16x32_bf16 v[22:25], v[70:73], v[110:113], v[22:25]
	v_mfma_f32_16x16x32_bf16 v[18:21], v[78:81], v[110:113], v[18:21]
	s_setprio 1
	s_barrier
	s_mov_b32 m0, s81
	v_lshl_add_u64 v[138:139], s[74:75], 0, v[114:115]
	ds_read_b128 v[82:85], v136 offset:16384
	ds_read_b128 v[86:89], v136 offset:17408
	ds_read_b128 v[90:93], v136 offset:18432
	ds_read_b128 v[94:97], v136 offset:19456
	ds_read_b128 v[98:101], v136 offset:20480
	ds_read_b128 v[102:105], v136 offset:21504
	ds_read_b128 v[106:109], v136 offset:22528
	ds_read_b128 v[110:113], v136 offset:23552
	global_load_lds_dwordx4 v[138:139], off
	v_lshl_add_u64 v[140:141], s[74:75], 0, v[116:117]
	s_mov_b32 m0, s82
	v_lshl_add_u64 v[142:143], s[76:77], 0, v[114:115]
	global_load_lds_dwordx4 v[140:141], off
	s_mov_b32 m0, s49
	v_lshl_add_u64 v[144:145], s[78:79], 0, v[116:117]
	global_load_lds_dwordx4 v[142:143], off
	v_lshl_add_u64 v[142:143], s[76:77], 0, v[116:117]
	s_mov_b32 m0, s50
	s_nop 0
	global_load_lds_dwordx4 v[142:143], off
	v_lshl_add_u64 v[142:143], s[78:79], 0, v[114:115]
	s_mov_b32 m0, s48
	s_nop 0
	global_load_lds_dwordx4 v[142:143], off
	s_mov_b32 m0, s51
	s_nop 0
	global_load_lds_dwordx4 v[144:145], off
	s_waitcnt vmcnt(8)
	s_waitcnt lgkmcnt(0)
	s_barrier
	s_setprio 0
	s_waitcnt lgkmcnt(0)
	v_mfma_f32_16x16x32_bf16 v[58:61], v[66:69], v[82:85], v[58:61]
	v_mfma_f32_16x16x32_bf16 v[50:53], v[74:77], v[82:85], v[50:53]
	v_mfma_f32_16x16x32_bf16 v[34:37], v[66:69], v[90:93], v[34:37]
	v_mfma_f32_16x16x32_bf16 v[26:29], v[74:77], v[90:93], v[26:29]
	v_mfma_f32_16x16x32_bf16 v[14:17], v[66:69], v[98:101], v[14:17]
	v_mfma_f32_16x16x32_bf16 v[10:13], v[74:77], v[98:101], v[10:13]
	v_mfma_f32_16x16x32_bf16 v[6:9], v[66:69], v[106:109], v[6:9]
	v_mfma_f32_16x16x32_bf16 v[2:5], v[74:77], v[106:109], v[2:5]
	v_mfma_f32_16x16x32_bf16 v[58:61], v[70:73], v[86:89], v[58:61]
	v_mfma_f32_16x16x32_bf16 v[50:53], v[78:81], v[86:89], v[50:53]
	v_mfma_f32_16x16x32_bf16 v[34:37], v[70:73], v[94:97], v[34:37]
	v_mfma_f32_16x16x32_bf16 v[26:29], v[78:81], v[94:97], v[26:29]
	v_mfma_f32_16x16x32_bf16 v[14:17], v[70:73], v[102:105], v[14:17]
	v_mfma_f32_16x16x32_bf16 v[10:13], v[78:81], v[102:105], v[10:13]
	v_mfma_f32_16x16x32_bf16 v[6:9], v[70:73], v[110:113], v[6:9]
	v_mfma_f32_16x16x32_bf16 v[2:5], v[78:81], v[110:113], v[2:5]
	s_setprio 1
	s_barrier
	v_add_u32_e32 v78, s83, v133
	ds_read_b128 v[66:69], v78
	ds_read_b128 v[70:73], v78 offset:1024
	ds_read_b128 v[74:77], v78 offset:2048
	ds_read_b128 v[78:81], v78 offset:3072
	s_mov_b32 m0, s52
	v_lshl_add_u64 v[146:147], s[54:55], 0, v[114:115]
	ds_read_b128 v[82:85], v136 offset:32768
	ds_read_b128 v[86:89], v136 offset:33792
	ds_read_b128 v[90:93], v136 offset:34816
	ds_read_b128 v[94:97], v136 offset:35840
	ds_read_b128 v[98:101], v136 offset:36864
	ds_read_b128 v[102:105], v136 offset:37888
	ds_read_b128 v[106:109], v136 offset:38912
	ds_read_b128 v[110:113], v136 offset:39936
	global_load_lds_dwordx4 v[146:147], off
	v_lshl_add_u64 v[146:147], s[54:55], 0, v[116:117]
	s_mov_b32 m0, s53
	s_nop 0
	global_load_lds_dwordx4 v[146:147], off
	s_waitcnt vmcnt(8)
	s_waitcnt lgkmcnt(0)
	s_barrier
	s_setprio 0
	s_waitcnt lgkmcnt(0)
	v_mfma_f32_16x16x32_bf16 v[62:65], v[66:69], v[82:85], v[62:65]
	v_mfma_f32_16x16x32_bf16 v[54:57], v[74:77], v[82:85], v[54:57]
	v_mfma_f32_16x16x32_bf16 v[46:49], v[66:69], v[90:93], v[46:49]
	v_mfma_f32_16x16x32_bf16 v[42:45], v[74:77], v[90:93], v[42:45]
	v_mfma_f32_16x16x32_bf16 v[38:41], v[66:69], v[98:101], v[38:41]
	v_mfma_f32_16x16x32_bf16 v[30:33], v[74:77], v[98:101], v[30:33]
	v_mfma_f32_16x16x32_bf16 v[22:25], v[66:69], v[106:109], v[22:25]
	v_mfma_f32_16x16x32_bf16 v[18:21], v[74:77], v[106:109], v[18:21]
	v_mfma_f32_16x16x32_bf16 v[62:65], v[70:73], v[86:89], v[62:65]
	v_mfma_f32_16x16x32_bf16 v[54:57], v[78:81], v[86:89], v[54:57]
	v_mfma_f32_16x16x32_bf16 v[46:49], v[70:73], v[94:97], v[46:49]
	v_mfma_f32_16x16x32_bf16 v[42:45], v[78:81], v[94:97], v[42:45]
	v_mfma_f32_16x16x32_bf16 v[38:41], v[70:73], v[102:105], v[38:41]
	v_mfma_f32_16x16x32_bf16 v[30:33], v[78:81], v[102:105], v[30:33]
	v_mfma_f32_16x16x32_bf16 v[22:25], v[70:73], v[110:113], v[22:25]
	v_mfma_f32_16x16x32_bf16 v[18:21], v[78:81], v[110:113], v[18:21]
	s_setprio 1
	s_barrier
	s_mov_b32 m0, s84
	v_lshl_add_u64 v[138:139], v[138:139], 0, s[12:13]
	ds_read_b128 v[106:109], v136 offset:49152
	ds_read_b128 v[110:113], v136 offset:50176
	ds_read_b128 v[98:101], v136 offset:51200
	ds_read_b128 v[102:105], v136 offset:52224
	ds_read_b128 v[90:93], v136 offset:53248
	ds_read_b128 v[94:97], v136 offset:54272
	ds_read_b128 v[82:85], v136 offset:55296
	ds_read_b128 v[86:89], v136 offset:56320
	global_load_lds_dwordx4 v[138:139], off
	v_lshl_add_u64 v[138:139], v[140:141], 0, s[12:13]
	s_mov_b32 m0, s85
	s_nop 0
	global_load_lds_dwordx4 v[138:139], off
	v_lshl_add_u64 v[138:139], s[40:41], 0, v[114:115]
	s_mov_b32 m0, s65
	s_nop 0
	global_load_lds_dwordx4 v[138:139], off
	v_lshl_add_u64 v[138:139], s[40:41], 0, v[116:117]
	s_mov_b32 m0, s66
	s_nop 0
	global_load_lds_dwordx4 v[138:139], off
	v_lshl_add_u64 v[138:139], v[142:143], 0, s[12:13]
	s_mov_b32 m0, s63
	s_nop 0
	global_load_lds_dwordx4 v[138:139], off
	v_lshl_add_u64 v[138:139], v[144:145], 0, s[12:13]
	s_mov_b32 m0, s64
	s_nop 0
	global_load_lds_dwordx4 v[138:139], off
	s_waitcnt vmcnt(8)
	s_waitcnt lgkmcnt(0)
	s_barrier
	s_cbranch_scc1 .LBB0_811
	v_mov_b32_e32 v137, v1
	v_mov_b32_e32 v138, v132
	s_andn2_b64 vcc, exec, s[16:17]
	s_cbranch_vccnz .LBB0_810
	v_add_u32_e32 v140, s70, v137
	v_ashrrev_i32_e32 v141, 31, v140
	v_lshl_add_u32 v138, v138, 2, s62
	v_lshlrev_b64 v[140:141], 8, v[140:141]
	v_ashrrev_i32_e32 v139, 31, v138
	v_lshl_add_u64 v[140:141], s[36:37], 0, v[140:141]
	v_lshl_add_u64 v[138:139], v[138:139], 2, v[140:141]
	v_add_co_u32_e32 v142, vcc, 0x1000, v138
	global_store_dwordx4 v[138:139], v[62:65], off
	global_store_dwordx4 v[138:139], v[54:57], off offset:64
	v_addc_co_u32_e32 v143, vcc, 0, v139, vcc
	v_lshl_add_u64 v[140:141], v[138:139], 0, s[20:21]
	global_store_dwordx4 v[142:143], v[46:49], off
	global_store_dwordx4 v[140:141], v[42:45], off offset:64
	v_add_co_u32_e32 v142, vcc, 0x2000, v138
	v_lshl_add_u64 v[140:141], v[138:139], 0, s[22:23]
	s_nop 0
	v_addc_co_u32_e32 v143, vcc, 0, v139, vcc
	global_store_dwordx4 v[142:143], v[38:41], off
	global_store_dwordx4 v[140:141], v[30:33], off offset:64
	v_lshl_add_u64 v[140:141], v[138:139], 0, s[24:25]
	v_add_co_u32_e32 v138, vcc, 0x3000, v138
	s_nop 1
	v_addc_co_u32_e32 v139, vcc, 0, v139, vcc
	global_store_dwordx4 v[138:139], v[22:25], off
	global_store_dwordx4 v[140:141], v[18:21], off offset:64
	s_branch .LBB0_810

.Lmoe_ix_ready_0:
.LBB0_1005:
	ds_read_b128 v[152:155], v158
	ds_read_b128 v[166:169], v158 offset:1024
	ds_read_b128 v[170:173], v158 offset:2048
	ds_read_b128 v[174:177], v158 offset:3072
	ds_read_b128 v[178:181], v159
	ds_read_b128 v[182:185], v159 offset:1024
	ds_read_b128 v[186:189], v159 offset:2048
	ds_read_b128 v[190:193], v159 offset:3072
	s_add_u32 s40, s64, s10
	s_addc_u32 s41, s65, s11
	s_add_u32 s38, s10, 0x100
	s_addc_u32 s39, s11, 0
	s_cmpk_eq_i32 s10, 0xf00
	s_cselect_b64 vcc, -1, 0
	s_and_b64 s[2:3], vcc, exec
	s_cselect_b32 s41, s31, s41
	s_cselect_b32 s40, s37, s40
	s_cselect_b32 s67, 0, s38
	v_lshl_add_u64 v[226:227], v[146:147], 0, s[10:11]
	s_add_i32 m0, s49, 0xc000
	ds_read_b128 v[194:197], v160
	ds_read_b128 v[198:201], v160 offset:1024
	ds_read_b128 v[202:205], v160 offset:2048
	ds_read_b128 v[206:209], v160 offset:3072
	ds_read_b128 v[210:213], v160 offset:4096
	ds_read_b128 v[214:217], v160 offset:5120
	ds_read_b128 v[218:221], v160 offset:6144
	ds_read_b128 v[222:225], v160 offset:7168
	global_load_lds_dwordx4 v[226:227], off
	v_lshl_add_u64 v[226:227], v[144:145], 0, s[10:11]
	s_add_i32 m0, s49, 0xe000
	s_nop 0
	global_load_lds_dwordx4 v[226:227], off
	s_waitcnt vmcnt(8)
	s_waitcnt lgkmcnt(0)
	s_barrier
	s_setprio 0
	s_waitcnt lgkmcnt(0)
	v_mfma_f32_16x16x32_bf16 v[126:129], v[152:155], v[194:197], v[126:129]
	v_mfma_f32_16x16x32_bf16 v[122:125], v[170:173], v[194:197], v[122:125]
	v_mfma_f32_16x16x32_bf16 v[110:113], v[152:155], v[202:205], v[110:113]
	v_mfma_f32_16x16x32_bf16 v[106:109], v[170:173], v[202:205], v[106:109]
	v_mfma_f32_16x16x32_bf16 v[94:97], v[152:155], v[210:213], v[94:97]
	v_mfma_f32_16x16x32_bf16 v[90:93], v[170:173], v[210:213], v[90:93]
	v_mfma_f32_16x16x32_bf16 v[78:81], v[152:155], v[218:221], v[78:81]
	v_mfma_f32_16x16x32_bf16 v[74:77], v[170:173], v[218:221], v[74:77]
	v_mfma_f32_16x16x32_bf16 v[126:129], v[166:169], v[198:201], v[126:129]
	v_mfma_f32_16x16x32_bf16 v[122:125], v[174:177], v[198:201], v[122:125]
	v_mfma_f32_16x16x32_bf16 v[110:113], v[166:169], v[206:209], v[110:113]
	v_mfma_f32_16x16x32_bf16 v[106:109], v[174:177], v[206:209], v[106:109]
	v_mfma_f32_16x16x32_bf16 v[94:97], v[166:169], v[214:217], v[94:97]
	v_mfma_f32_16x16x32_bf16 v[90:93], v[174:177], v[214:217], v[90:93]
	v_mfma_f32_16x16x32_bf16 v[78:81], v[166:169], v[222:225], v[78:81]
	v_mfma_f32_16x16x32_bf16 v[74:77], v[174:177], v[222:225], v[74:77]
	v_mfma_f32_16x16x32_bf16 v[118:121], v[178:181], v[194:197], v[118:121]
	v_mfma_f32_16x16x32_bf16 v[114:117], v[186:189], v[194:197], v[114:117]
	v_mfma_f32_16x16x32_bf16 v[102:105], v[178:181], v[202:205], v[102:105]
	v_mfma_f32_16x16x32_bf16 v[98:101], v[186:189], v[202:205], v[98:101]
	v_mfma_f32_16x16x32_bf16 v[86:89], v[178:181], v[210:213], v[86:89]
	v_mfma_f32_16x16x32_bf16 v[82:85], v[186:189], v[210:213], v[82:85]
	v_mfma_f32_16x16x32_bf16 v[70:73], v[178:181], v[218:221], v[70:73]
	v_mfma_f32_16x16x32_bf16 v[66:69], v[186:189], v[218:221], v[66:69]
	v_mfma_f32_16x16x32_bf16 v[118:121], v[182:185], v[198:201], v[118:121]
	v_mfma_f32_16x16x32_bf16 v[114:117], v[190:193], v[198:201], v[114:117]
	v_mfma_f32_16x16x32_bf16 v[102:105], v[182:185], v[206:209], v[102:105]
	v_mfma_f32_16x16x32_bf16 v[98:101], v[190:193], v[206:209], v[98:101]
	v_mfma_f32_16x16x32_bf16 v[86:89], v[182:185], v[214:217], v[86:89]
	v_mfma_f32_16x16x32_bf16 v[82:85], v[190:193], v[214:217], v[82:85]
	v_mfma_f32_16x16x32_bf16 v[70:73], v[182:185], v[222:225], v[70:73]
	v_mfma_f32_16x16x32_bf16 v[66:69], v[190:193], v[222:225], v[66:69]
	s_setprio 1
	s_barrier
	s_add_i32 s2, s61, s48
	v_lshl_add_u64 v[226:227], s[40:41], 0, v[132:133]
	s_mov_b32 m0, s2
	ds_read_b128 v[194:197], v160 offset:16384
	ds_read_b128 v[198:201], v160 offset:17408
	ds_read_b128 v[202:205], v160 offset:18432
	ds_read_b128 v[206:209], v160 offset:19456
	ds_read_b128 v[210:213], v160 offset:20480
	ds_read_b128 v[214:217], v160 offset:21504
	ds_read_b128 v[218:221], v160 offset:22528
	ds_read_b128 v[222:225], v160 offset:23552
	global_load_lds_dwordx4 v[226:227], off
	s_add_i32 m0, s2, 0x2000
	s_add_u32 s2, s40, 0x80000
	v_lshl_add_u64 v[228:229], s[40:41], 0, v[134:135]
	s_addc_u32 s3, s41, 0
	s_add_i32 s10, s62, s48
	global_load_lds_dwordx4 v[228:229], off
	v_lshl_add_u64 v[230:231], s[2:3], 0, v[132:133]
	s_mov_b32 m0, s10
	v_cndmask_b32_e32 v130, v148, v164, vcc
	global_load_lds_dwordx4 v[230:231], off
	s_add_i32 m0, s10, 0x2000
	v_lshl_add_u64 v[230:231], s[2:3], 0, v[134:135]
	s_add_u32 s2, s16, s67
	global_load_lds_dwordx4 v[230:231], off
	s_addc_u32 s3, s17, 0
	s_mov_b32 m0, s49
	v_lshl_add_u64 v[230:231], s[2:3], 0, v[130:131]
	global_load_lds_dwordx4 v130, s[2:3]
	v_cndmask_b32_e32 v130, v140, v163, vcc
	s_mov_b32 m0, s50
	v_lshl_add_u64 v[232:233], s[2:3], 0, v[130:131]
	global_load_lds_dwordx4 v130, s[2:3]
	s_waitcnt vmcnt(8)
	s_waitcnt lgkmcnt(0)
	s_barrier
	s_setprio 0
	s_waitcnt lgkmcnt(0)
	v_mfma_f32_16x16x32_bf16 v[62:65], v[152:155], v[194:197], v[62:65]
	v_mfma_f32_16x16x32_bf16 v[58:61], v[170:173], v[194:197], v[58:61]
	v_mfma_f32_16x16x32_bf16 v[46:49], v[152:155], v[202:205], v[46:49]
	v_mfma_f32_16x16x32_bf16 v[42:45], v[170:173], v[202:205], v[42:45]
	v_mfma_f32_16x16x32_bf16 v[30:33], v[152:155], v[210:213], v[30:33]
	v_mfma_f32_16x16x32_bf16 v[26:29], v[170:173], v[210:213], v[26:29]
	v_mfma_f32_16x16x32_bf16 v[14:17], v[152:155], v[218:221], v[14:17]
	v_mfma_f32_16x16x32_bf16 v[10:13], v[170:173], v[218:221], v[10:13]
	v_mfma_f32_16x16x32_bf16 v[62:65], v[166:169], v[198:201], v[62:65]
	v_mfma_f32_16x16x32_bf16 v[58:61], v[174:177], v[198:201], v[58:61]
	v_mfma_f32_16x16x32_bf16 v[46:49], v[166:169], v[206:209], v[46:49]
	v_mfma_f32_16x16x32_bf16 v[42:45], v[174:177], v[206:209], v[42:45]
	v_mfma_f32_16x16x32_bf16 v[30:33], v[166:169], v[214:217], v[30:33]
	v_mfma_f32_16x16x32_bf16 v[26:29], v[174:177], v[214:217], v[26:29]
	v_mfma_f32_16x16x32_bf16 v[14:17], v[166:169], v[222:225], v[14:17]
	v_mfma_f32_16x16x32_bf16 v[10:13], v[174:177], v[222:225], v[10:13]
	v_mfma_f32_16x16x32_bf16 v[54:57], v[178:181], v[194:197], v[54:57]
	v_mfma_f32_16x16x32_bf16 v[50:53], v[186:189], v[194:197], v[50:53]
	v_mfma_f32_16x16x32_bf16 v[38:41], v[178:181], v[202:205], v[38:41]
	v_mfma_f32_16x16x32_bf16 v[34:37], v[186:189], v[202:205], v[34:37]
	v_mfma_f32_16x16x32_bf16 v[22:25], v[178:181], v[210:213], v[22:25]
	v_mfma_f32_16x16x32_bf16 v[18:21], v[186:189], v[210:213], v[18:21]
	v_mfma_f32_16x16x32_bf16 v[6:9], v[178:181], v[218:221], v[6:9]
	v_mfma_f32_16x16x32_bf16 v[2:5], v[186:189], v[218:221], v[2:5]
	v_mfma_f32_16x16x32_bf16 v[54:57], v[182:185], v[198:201], v[54:57]
	v_mfma_f32_16x16x32_bf16 v[50:53], v[190:193], v[198:201], v[50:53]
	v_mfma_f32_16x16x32_bf16 v[38:41], v[182:185], v[206:209], v[38:41]
	v_mfma_f32_16x16x32_bf16 v[34:37], v[190:193], v[206:209], v[34:37]
	v_mfma_f32_16x16x32_bf16 v[22:25], v[182:185], v[214:217], v[22:25]
	v_mfma_f32_16x16x32_bf16 v[18:21], v[190:193], v[214:217], v[18:21]
	v_mfma_f32_16x16x32_bf16 v[6:9], v[182:185], v[222:225], v[6:9]
	v_mfma_f32_16x16x32_bf16 v[2:5], v[190:193], v[222:225], v[2:5]
	s_setprio 1
	s_barrier
	s_add_i32 s10, 0, 0x18000
	v_add_u32_e32 v130, s10, v156
	s_add_i32 s11, 0, 0x1c000
	ds_read_b128 v[152:155], v130
	ds_read_b128 v[166:169], v130 offset:1024
	ds_read_b128 v[170:173], v130 offset:2048
	ds_read_b128 v[174:177], v130 offset:3072
	v_add_u32_e32 v130, s11, v156
	ds_read_b128 v[178:181], v130
	ds_read_b128 v[182:185], v130 offset:1024
	ds_read_b128 v[186:189], v130 offset:2048
	ds_read_b128 v[190:193], v130 offset:3072
	s_mov_b32 m0, s51
	v_cndmask_b32_e32 v130, v138, v161, vcc
	ds_read_b128 v[194:197], v160 offset:32768
	ds_read_b128 v[198:201], v160 offset:33792
	ds_read_b128 v[202:205], v160 offset:34816
	ds_read_b128 v[206:209], v160 offset:35840
	ds_read_b128 v[210:213], v160 offset:36864
	ds_read_b128 v[214:217], v160 offset:37888
	ds_read_b128 v[218:221], v160 offset:38912
	ds_read_b128 v[222:225], v160 offset:39936
	global_load_lds_dwordx4 v130, s[2:3]
	v_cndmask_b32_e32 v130, v142, v162, vcc
	s_mov_b32 m0, s52
	s_nop 0
	global_load_lds_dwordx4 v130, s[2:3]
	s_waitcnt vmcnt(8)
	s_waitcnt lgkmcnt(0)
	s_barrier
	s_setprio 0
	s_waitcnt lgkmcnt(0)
	v_mfma_f32_16x16x32_bf16 v[126:129], v[152:155], v[194:197], v[126:129]
	v_mfma_f32_16x16x32_bf16 v[122:125], v[170:173], v[194:197], v[122:125]
	v_mfma_f32_16x16x32_bf16 v[110:113], v[152:155], v[202:205], v[110:113]
	v_mfma_f32_16x16x32_bf16 v[106:109], v[170:173], v[202:205], v[106:109]
	v_mfma_f32_16x16x32_bf16 v[94:97], v[152:155], v[210:213], v[94:97]
	v_mfma_f32_16x16x32_bf16 v[90:93], v[170:173], v[210:213], v[90:93]
	v_mfma_f32_16x16x32_bf16 v[78:81], v[152:155], v[218:221], v[78:81]
	v_mfma_f32_16x16x32_bf16 v[74:77], v[170:173], v[218:221], v[74:77]
	v_mfma_f32_16x16x32_bf16 v[126:129], v[166:169], v[198:201], v[126:129]
	v_mfma_f32_16x16x32_bf16 v[122:125], v[174:177], v[198:201], v[122:125]
	v_mfma_f32_16x16x32_bf16 v[110:113], v[166:169], v[206:209], v[110:113]
	v_mfma_f32_16x16x32_bf16 v[106:109], v[174:177], v[206:209], v[106:109]
	v_mfma_f32_16x16x32_bf16 v[94:97], v[166:169], v[214:217], v[94:97]
	v_mfma_f32_16x16x32_bf16 v[90:93], v[174:177], v[214:217], v[90:93]
	v_mfma_f32_16x16x32_bf16 v[78:81], v[166:169], v[222:225], v[78:81]
	v_mfma_f32_16x16x32_bf16 v[74:77], v[174:177], v[222:225], v[74:77]
	v_mfma_f32_16x16x32_bf16 v[118:121], v[178:181], v[194:197], v[118:121]
	v_mfma_f32_16x16x32_bf16 v[114:117], v[186:189], v[194:197], v[114:117]
	v_mfma_f32_16x16x32_bf16 v[102:105], v[178:181], v[202:205], v[102:105]
	v_mfma_f32_16x16x32_bf16 v[98:101], v[186:189], v[202:205], v[98:101]
	v_mfma_f32_16x16x32_bf16 v[86:89], v[178:181], v[210:213], v[86:89]
	v_mfma_f32_16x16x32_bf16 v[82:85], v[186:189], v[210:213], v[82:85]
	v_mfma_f32_16x16x32_bf16 v[70:73], v[178:181], v[218:221], v[70:73]
	v_mfma_f32_16x16x32_bf16 v[66:69], v[186:189], v[218:221], v[66:69]
	v_mfma_f32_16x16x32_bf16 v[118:121], v[182:185], v[198:201], v[118:121]
	v_mfma_f32_16x16x32_bf16 v[114:117], v[190:193], v[198:201], v[114:117]
	v_mfma_f32_16x16x32_bf16 v[102:105], v[182:185], v[206:209], v[102:105]
	v_mfma_f32_16x16x32_bf16 v[98:101], v[190:193], v[206:209], v[98:101]
	v_mfma_f32_16x16x32_bf16 v[86:89], v[182:185], v[214:217], v[86:89]
	v_mfma_f32_16x16x32_bf16 v[82:85], v[190:193], v[214:217], v[82:85]
	v_mfma_f32_16x16x32_bf16 v[70:73], v[182:185], v[222:225], v[70:73]
	v_mfma_f32_16x16x32_bf16 v[66:69], v[190:193], v[222:225], v[66:69]
	s_setprio 1
	s_barrier
	s_add_i32 s2, s10, s48
	v_lshl_add_u64 v[226:227], v[226:227], 0, s[20:21]
	s_mov_b32 m0, s2
	ds_read_b128 v[194:197], v160 offset:49152
	ds_read_b128 v[198:201], v160 offset:50176
	ds_read_b128 v[202:205], v160 offset:51200
	ds_read_b128 v[206:209], v160 offset:52224
	ds_read_b128 v[210:213], v160 offset:53248
	ds_read_b128 v[214:217], v160 offset:54272
	ds_read_b128 v[218:221], v160 offset:55296
	ds_read_b128 v[222:225], v160 offset:56320
	global_load_lds_dwordx4 v[226:227], off
	s_add_i32 m0, s2, 0x2000
	s_add_u32 s2, s40, 0x80080
	v_lshl_add_u64 v[226:227], v[228:229], 0, s[20:21]
	s_addc_u32 s3, s41, 0
	s_add_i32 s10, s11, s48
	global_load_lds_dwordx4 v[226:227], off
	v_lshl_add_u64 v[226:227], s[2:3], 0, v[132:133]
	s_mov_b32 m0, s10
	s_nop 0
	global_load_lds_dwordx4 v[226:227], off
	v_lshl_add_u64 v[226:227], s[2:3], 0, v[134:135]
	s_add_i32 m0, s10, 0x2000
	s_nop 0
	global_load_lds_dwordx4 v[226:227], off
	v_lshl_add_u64 v[226:227], v[230:231], 0, s[20:21]
	s_mov_b32 m0, s58
	s_nop 0
	global_load_lds_dwordx4 v[226:227], off
	v_lshl_add_u64 v[226:227], v[232:233], 0, s[20:21]
	s_mov_b32 m0, s59
	s_nop 0
	global_load_lds_dwordx4 v[226:227], off
	s_waitcnt vmcnt(8)
	s_waitcnt lgkmcnt(0)
	s_barrier
	s_setprio 0
	s_waitcnt lgkmcnt(0)
	v_mfma_f32_16x16x32_bf16 v[62:65], v[152:155], v[194:197], v[62:65]
	v_mfma_f32_16x16x32_bf16 v[58:61], v[170:173], v[194:197], v[58:61]
	v_mfma_f32_16x16x32_bf16 v[46:49], v[152:155], v[202:205], v[46:49]
	v_mfma_f32_16x16x32_bf16 v[42:45], v[170:173], v[202:205], v[42:45]
	v_mfma_f32_16x16x32_bf16 v[30:33], v[152:155], v[210:213], v[30:33]
	v_mfma_f32_16x16x32_bf16 v[26:29], v[170:173], v[210:213], v[26:29]
	v_mfma_f32_16x16x32_bf16 v[14:17], v[152:155], v[218:221], v[14:17]
	v_mfma_f32_16x16x32_bf16 v[10:13], v[170:173], v[218:221], v[10:13]
	v_mfma_f32_16x16x32_bf16 v[62:65], v[166:169], v[198:201], v[62:65]
	v_mfma_f32_16x16x32_bf16 v[58:61], v[174:177], v[198:201], v[58:61]
	v_mfma_f32_16x16x32_bf16 v[46:49], v[166:169], v[206:209], v[46:49]
	v_mfma_f32_16x16x32_bf16 v[42:45], v[174:177], v[206:209], v[42:45]
	v_mfma_f32_16x16x32_bf16 v[30:33], v[166:169], v[214:217], v[30:33]
	v_mfma_f32_16x16x32_bf16 v[26:29], v[174:177], v[214:217], v[26:29]
	v_mfma_f32_16x16x32_bf16 v[14:17], v[166:169], v[222:225], v[14:17]
	v_mfma_f32_16x16x32_bf16 v[10:13], v[174:177], v[222:225], v[10:13]
	v_mfma_f32_16x16x32_bf16 v[54:57], v[178:181], v[194:197], v[54:57]
	v_mfma_f32_16x16x32_bf16 v[50:53], v[186:189], v[194:197], v[50:53]
	v_mfma_f32_16x16x32_bf16 v[38:41], v[178:181], v[202:205], v[38:41]
	v_mfma_f32_16x16x32_bf16 v[34:37], v[186:189], v[202:205], v[34:37]
	v_mfma_f32_16x16x32_bf16 v[22:25], v[178:181], v[210:213], v[22:25]
	v_mfma_f32_16x16x32_bf16 v[18:21], v[186:189], v[210:213], v[18:21]
	v_mfma_f32_16x16x32_bf16 v[6:9], v[178:181], v[218:221], v[6:9]
	v_mfma_f32_16x16x32_bf16 v[2:5], v[186:189], v[218:221], v[2:5]
	v_mfma_f32_16x16x32_bf16 v[54:57], v[182:185], v[198:201], v[54:57]
	v_mfma_f32_16x16x32_bf16 v[50:53], v[190:193], v[198:201], v[50:53]
	v_mfma_f32_16x16x32_bf16 v[38:41], v[182:185], v[206:209], v[38:41]
	v_mfma_f32_16x16x32_bf16 v[34:37], v[190:193], v[206:209], v[34:37]
	v_mfma_f32_16x16x32_bf16 v[22:25], v[182:185], v[214:217], v[22:25]
	v_mfma_f32_16x16x32_bf16 v[18:21], v[190:193], v[214:217], v[18:21]
	v_mfma_f32_16x16x32_bf16 v[6:9], v[182:185], v[222:225], v[6:9]
	v_mfma_f32_16x16x32_bf16 v[2:5], v[190:193], v[222:225], v[2:5]
	s_setprio 1
	s_barrier
	s_add_i32 s66, s66, 2
	s_cmp_gt_u32 s66, 29
	s_mov_b64 s[10:11], s[38:39]
	s_cbranch_scc0 .LBB0_1005
	s_and_b64 vcc, exec, s[24:25]
	s_cbranch_vccz .LBB0_1008
	s_barrier

.LBB0_1104:
	s_setprio 0
	s_waitcnt lgkmcnt(0)
	v_mfma_f32_16x16x32_bf16 v[126:129], v[146:149], v[186:189], v[126:129]
	v_mfma_f32_16x16x32_bf16 v[122:125], v[154:157], v[186:189], v[122:125]
	v_mfma_f32_16x16x32_bf16 v[110:113], v[146:149], v[178:181], v[110:113]
	v_mfma_f32_16x16x32_bf16 v[106:109], v[154:157], v[178:181], v[106:109]
	v_mfma_f32_16x16x32_bf16 v[94:97], v[146:149], v[170:173], v[94:97]
	v_mfma_f32_16x16x32_bf16 v[90:93], v[154:157], v[170:173], v[90:93]
	v_mfma_f32_16x16x32_bf16 v[22:25], v[146:149], v[162:165], v[22:25]
	v_mfma_f32_16x16x32_bf16 v[14:17], v[154:157], v[162:165], v[14:17]
	v_mfma_f32_16x16x32_bf16 v[126:129], v[150:153], v[190:193], v[126:129]
	v_mfma_f32_16x16x32_bf16 v[122:125], v[158:161], v[190:193], v[122:125]
	v_mfma_f32_16x16x32_bf16 v[110:113], v[150:153], v[182:185], v[110:113]
	v_mfma_f32_16x16x32_bf16 v[106:109], v[158:161], v[182:185], v[106:109]
	v_mfma_f32_16x16x32_bf16 v[94:97], v[150:153], v[174:177], v[94:97]
	v_mfma_f32_16x16x32_bf16 v[90:93], v[158:161], v[174:177], v[90:93]
	v_mfma_f32_16x16x32_bf16 v[22:25], v[150:153], v[166:169], v[22:25]
	v_mfma_f32_16x16x32_bf16 v[14:17], v[158:161], v[166:169], v[14:17]
	v_mfma_f32_16x16x32_bf16 v[118:121], v[130:133], v[186:189], v[118:121]
	v_mfma_f32_16x16x32_bf16 v[114:117], v[138:141], v[186:189], v[114:117]
	v_mfma_f32_16x16x32_bf16 v[102:105], v[130:133], v[178:181], v[102:105]
	v_mfma_f32_16x16x32_bf16 v[98:101], v[138:141], v[178:181], v[98:101]
	v_mfma_f32_16x16x32_bf16 v[38:41], v[130:133], v[170:173], v[38:41]
	v_mfma_f32_16x16x32_bf16 v[30:33], v[138:141], v[170:173], v[30:33]
	v_mfma_f32_16x16x32_bf16 v[6:9], v[130:133], v[162:165], v[6:9]
	v_mfma_f32_16x16x32_bf16 v[2:5], v[138:141], v[162:165], v[2:5]
	v_mfma_f32_16x16x32_bf16 v[118:121], v[134:137], v[190:193], v[118:121]
	v_mfma_f32_16x16x32_bf16 v[114:117], v[142:145], v[190:193], v[114:117]
	v_mfma_f32_16x16x32_bf16 v[102:105], v[134:137], v[182:185], v[102:105]
	v_mfma_f32_16x16x32_bf16 v[98:101], v[142:145], v[182:185], v[98:101]
	v_mfma_f32_16x16x32_bf16 v[38:41], v[134:137], v[174:177], v[38:41]
	v_mfma_f32_16x16x32_bf16 v[30:33], v[142:145], v[174:177], v[30:33]
	v_mfma_f32_16x16x32_bf16 v[6:9], v[134:137], v[166:169], v[6:9]
	v_mfma_f32_16x16x32_bf16 v[2:5], v[142:145], v[166:169], v[2:5]
	s_setprio 1
	s_barrier
	s_add_i32 s2, s87, 2
	s_cmp_gt_u32 s87, 5
	s_mov_b32 s87, s2
	s_cbranch_scc1 .LBB0_1124

.LBB0_1122:
	s_lshl_b32 s2, s87, 7
	v_add_u32_e32 v142, s80, v205
	v_add_u32_e32 v158, s81, v205
	s_add_u32 s64, s38, s2
	ds_read_b128 v[130:133], v142
	ds_read_b128 v[134:137], v142 offset:1024
	ds_read_b128 v[138:141], v142 offset:2048
	ds_read_b128 v[142:145], v142 offset:3072
	ds_read_b128 v[146:149], v158
	ds_read_b128 v[150:153], v158 offset:1024
	ds_read_b128 v[154:157], v158 offset:2048
	ds_read_b128 v[158:161], v158 offset:3072
	s_addc_u32 s65, s39, 0
	s_add_u32 s66, s64, 0x100
	s_addc_u32 s67, s65, 0
	s_and_b64 s[64:65], s[60:61], exec
	s_cselect_b32 s65, s35, s67
	s_cselect_b32 s64, s83, s66
	s_add_i32 s68, s2, 0x100
	s_and_b64 s[66:67], s[60:61], exec
	s_cselect_b32 s68, 0, s68
	s_add_u32 s2, s36, s2
	s_addc_u32 s67, s37, 0
	s_add_u32 s66, s2, 0x20080
	s_addc_u32 s67, s67, 0
	v_lshl_add_u64 v[210:211], s[66:67], 0, v[194:195]
	s_add_i32 m0, s50, 0xc000
	ds_read_b128 v[162:165], v209
	ds_read_b128 v[166:169], v209 offset:1024
	ds_read_b128 v[170:173], v209 offset:2048
	ds_read_b128 v[174:177], v209 offset:3072
	ds_read_b128 v[178:181], v209 offset:4096
	ds_read_b128 v[182:185], v209 offset:5120
	ds_read_b128 v[186:189], v209 offset:6144
	ds_read_b128 v[190:193], v209 offset:7168
	global_load_lds_dwordx4 v[210:211], off
	v_lshl_add_u64 v[210:211], s[66:67], 0, v[198:199]
	s_add_i32 m0, s50, 0xe000
	s_nop 0
	global_load_lds_dwordx4 v[210:211], off
	s_waitcnt vmcnt(8)
	s_waitcnt lgkmcnt(0)
	s_barrier
	s_setprio 0
	s_waitcnt lgkmcnt(0)
	v_mfma_f32_16x16x32_bf16 v[86:89], v[130:133], v[162:165], v[86:89]
	v_mfma_f32_16x16x32_bf16 v[82:85], v[138:141], v[162:165], v[82:85]
	v_mfma_f32_16x16x32_bf16 v[78:81], v[130:133], v[170:173], v[78:81]
	v_mfma_f32_16x16x32_bf16 v[74:77], v[138:141], v[170:173], v[74:77]
	v_mfma_f32_16x16x32_bf16 v[70:73], v[130:133], v[178:181], v[70:73]
	v_mfma_f32_16x16x32_bf16 v[66:69], v[138:141], v[178:181], v[66:69]
	v_mfma_f32_16x16x32_bf16 v[62:65], v[130:133], v[186:189], v[62:65]
	v_mfma_f32_16x16x32_bf16 v[58:61], v[138:141], v[186:189], v[58:61]
	v_mfma_f32_16x16x32_bf16 v[86:89], v[134:137], v[166:169], v[86:89]
	v_mfma_f32_16x16x32_bf16 v[82:85], v[142:145], v[166:169], v[82:85]
	v_mfma_f32_16x16x32_bf16 v[78:81], v[134:137], v[174:177], v[78:81]
	v_mfma_f32_16x16x32_bf16 v[74:77], v[142:145], v[174:177], v[74:77]
	v_mfma_f32_16x16x32_bf16 v[70:73], v[134:137], v[182:185], v[70:73]
	v_mfma_f32_16x16x32_bf16 v[66:69], v[142:145], v[182:185], v[66:69]
	v_mfma_f32_16x16x32_bf16 v[62:65], v[134:137], v[190:193], v[62:65]
	v_mfma_f32_16x16x32_bf16 v[58:61], v[142:145], v[190:193], v[58:61]
	v_mfma_f32_16x16x32_bf16 v[54:57], v[146:149], v[162:165], v[54:57]
	v_mfma_f32_16x16x32_bf16 v[50:53], v[154:157], v[162:165], v[50:53]
	v_mfma_f32_16x16x32_bf16 v[46:49], v[146:149], v[170:173], v[46:49]
	v_mfma_f32_16x16x32_bf16 v[42:45], v[154:157], v[170:173], v[42:45]
	v_mfma_f32_16x16x32_bf16 v[34:37], v[146:149], v[178:181], v[34:37]
	v_mfma_f32_16x16x32_bf16 v[26:29], v[154:157], v[178:181], v[26:29]
	v_mfma_f32_16x16x32_bf16 v[18:21], v[146:149], v[186:189], v[18:21]
	v_mfma_f32_16x16x32_bf16 v[10:13], v[154:157], v[186:189], v[10:13]
	v_mfma_f32_16x16x32_bf16 v[54:57], v[150:153], v[166:169], v[54:57]
	v_mfma_f32_16x16x32_bf16 v[50:53], v[158:161], v[166:169], v[50:53]
	v_mfma_f32_16x16x32_bf16 v[46:49], v[150:153], v[174:177], v[46:49]
	v_mfma_f32_16x16x32_bf16 v[42:45], v[158:161], v[174:177], v[42:45]
	v_mfma_f32_16x16x32_bf16 v[34:37], v[150:153], v[182:185], v[34:37]
	v_mfma_f32_16x16x32_bf16 v[26:29], v[158:161], v[182:185], v[26:29]
	v_mfma_f32_16x16x32_bf16 v[18:21], v[150:153], v[190:193], v[18:21]
	v_mfma_f32_16x16x32_bf16 v[10:13], v[158:161], v[190:193], v[10:13]
	s_setprio 1
	s_barrier
	s_add_i32 s2, s80, s49
	v_lshl_add_u64 v[210:211], s[64:65], 0, v[196:197]
	s_mov_b32 m0, s2
	ds_read_b128 v[162:165], v209 offset:16384
	ds_read_b128 v[166:169], v209 offset:17408
	ds_read_b128 v[170:173], v209 offset:18432
	ds_read_b128 v[174:177], v209 offset:19456
	ds_read_b128 v[178:181], v209 offset:20480
	ds_read_b128 v[182:185], v209 offset:21504
	ds_read_b128 v[186:189], v209 offset:22528
	ds_read_b128 v[190:193], v209 offset:23552
	global_load_lds_dwordx4 v[210:211], off
	s_add_i32 m0, s2, 0x2000
	s_add_u32 s66, s64, 0x20000
	v_lshl_add_u64 v[212:213], s[64:65], 0, v[200:201]
	s_addc_u32 s67, s65, 0
	s_add_i32 s2, s81, s49
	global_load_lds_dwordx4 v[212:213], off
	v_lshl_add_u64 v[214:215], s[66:67], 0, v[196:197]
	s_mov_b32 m0, s2
	s_nop 0
	global_load_lds_dwordx4 v[214:215], off
	s_add_i32 m0, s2, 0x2000
	s_add_u32 s62, s62, s68
	v_lshl_add_u64 v[214:215], s[66:67], 0, v[200:201]
	s_addc_u32 s63, s63, 0
	global_load_lds_dwordx4 v[214:215], off
	v_lshl_add_u64 v[214:215], s[62:63], 0, v[194:195]
	s_mov_b32 m0, s50
	v_lshl_add_u64 v[216:217], s[62:63], 0, v[198:199]
	global_load_lds_dwordx4 v[214:215], off
	s_mov_b32 m0, s51
	s_nop 0
	global_load_lds_dwordx4 v[216:217], off
	s_waitcnt vmcnt(8)
	s_waitcnt lgkmcnt(0)
	s_barrier
	s_setprio 0
	s_waitcnt lgkmcnt(0)
	v_mfma_f32_16x16x32_bf16 v[126:129], v[130:133], v[162:165], v[126:129]
	v_mfma_f32_16x16x32_bf16 v[122:125], v[138:141], v[162:165], v[122:125]
	v_mfma_f32_16x16x32_bf16 v[110:113], v[130:133], v[170:173], v[110:113]
	v_mfma_f32_16x16x32_bf16 v[106:109], v[138:141], v[170:173], v[106:109]
	v_mfma_f32_16x16x32_bf16 v[94:97], v[130:133], v[178:181], v[94:97]
	v_mfma_f32_16x16x32_bf16 v[90:93], v[138:141], v[178:181], v[90:93]
	v_mfma_f32_16x16x32_bf16 v[22:25], v[130:133], v[186:189], v[22:25]
	v_mfma_f32_16x16x32_bf16 v[14:17], v[138:141], v[186:189], v[14:17]
	v_mfma_f32_16x16x32_bf16 v[126:129], v[134:137], v[166:169], v[126:129]
	v_mfma_f32_16x16x32_bf16 v[122:125], v[142:145], v[166:169], v[122:125]
	v_mfma_f32_16x16x32_bf16 v[110:113], v[134:137], v[174:177], v[110:113]
	v_mfma_f32_16x16x32_bf16 v[106:109], v[142:145], v[174:177], v[106:109]
	v_mfma_f32_16x16x32_bf16 v[94:97], v[134:137], v[182:185], v[94:97]
	v_mfma_f32_16x16x32_bf16 v[90:93], v[142:145], v[182:185], v[90:93]
	v_mfma_f32_16x16x32_bf16 v[22:25], v[134:137], v[190:193], v[22:25]
	v_mfma_f32_16x16x32_bf16 v[14:17], v[142:145], v[190:193], v[14:17]
	v_mfma_f32_16x16x32_bf16 v[118:121], v[146:149], v[162:165], v[118:121]
	v_mfma_f32_16x16x32_bf16 v[114:117], v[154:157], v[162:165], v[114:117]
	v_mfma_f32_16x16x32_bf16 v[102:105], v[146:149], v[170:173], v[102:105]
	v_mfma_f32_16x16x32_bf16 v[98:101], v[154:157], v[170:173], v[98:101]
	v_mfma_f32_16x16x32_bf16 v[38:41], v[146:149], v[178:181], v[38:41]
	v_mfma_f32_16x16x32_bf16 v[30:33], v[154:157], v[178:181], v[30:33]
	v_mfma_f32_16x16x32_bf16 v[6:9], v[146:149], v[186:189], v[6:9]
	v_mfma_f32_16x16x32_bf16 v[2:5], v[154:157], v[186:189], v[2:5]
	v_mfma_f32_16x16x32_bf16 v[118:121], v[150:153], v[166:169], v[118:121]
	v_mfma_f32_16x16x32_bf16 v[114:117], v[158:161], v[166:169], v[114:117]
	v_mfma_f32_16x16x32_bf16 v[102:105], v[150:153], v[174:177], v[102:105]
	v_mfma_f32_16x16x32_bf16 v[98:101], v[158:161], v[174:177], v[98:101]
	v_mfma_f32_16x16x32_bf16 v[38:41], v[150:153], v[182:185], v[38:41]
	v_mfma_f32_16x16x32_bf16 v[30:33], v[158:161], v[182:185], v[30:33]
	v_mfma_f32_16x16x32_bf16 v[6:9], v[150:153], v[190:193], v[6:9]
	v_mfma_f32_16x16x32_bf16 v[2:5], v[158:161], v[190:193], v[2:5]
	s_setprio 1
	s_barrier
	s_add_i32 s2, 0, 0x18000
	s_add_i32 s66, 0, 0x1c000
	v_add_u32_e32 v130, s2, v205
	v_add_u32_e32 v142, s66, v205
	ds_read_b128 v[146:149], v130
	ds_read_b128 v[150:153], v130 offset:1024
	ds_read_b128 v[154:157], v130 offset:2048
	ds_read_b128 v[158:161], v130 offset:3072
	ds_read_b128 v[130:133], v142
	ds_read_b128 v[134:137], v142 offset:1024
	ds_read_b128 v[138:141], v142 offset:2048
	ds_read_b128 v[142:145], v142 offset:3072
	s_add_u32 s62, s62, 0x20000
	s_addc_u32 s63, s63, 0
	s_mov_b32 m0, s52
	v_lshl_add_u64 v[218:219], s[62:63], 0, v[194:195]
	ds_read_b128 v[162:165], v209 offset:32768
	ds_read_b128 v[166:169], v209 offset:33792
	ds_read_b128 v[170:173], v209 offset:34816
	ds_read_b128 v[174:177], v209 offset:35840
	ds_read_b128 v[178:181], v209 offset:36864
	ds_read_b128 v[182:185], v209 offset:37888
	ds_read_b128 v[186:189], v209 offset:38912
	ds_read_b128 v[190:193], v209 offset:39936
	global_load_lds_dwordx4 v[218:219], off
	v_lshl_add_u64 v[218:219], s[62:63], 0, v[198:199]
	s_mov_b32 m0, s53
	s_nop 0
	global_load_lds_dwordx4 v[218:219], off
	s_waitcnt vmcnt(8)
	s_waitcnt lgkmcnt(0)
	s_barrier
	s_setprio 0
	s_waitcnt lgkmcnt(0)
	v_mfma_f32_16x16x32_bf16 v[86:89], v[146:149], v[162:165], v[86:89]
	v_mfma_f32_16x16x32_bf16 v[82:85], v[154:157], v[162:165], v[82:85]
	v_mfma_f32_16x16x32_bf16 v[78:81], v[146:149], v[170:173], v[78:81]
	v_mfma_f32_16x16x32_bf16 v[74:77], v[154:157], v[170:173], v[74:77]
	v_mfma_f32_16x16x32_bf16 v[70:73], v[146:149], v[178:181], v[70:73]
	v_mfma_f32_16x16x32_bf16 v[66:69], v[154:157], v[178:181], v[66:69]
	v_mfma_f32_16x16x32_bf16 v[62:65], v[146:149], v[186:189], v[62:65]
	v_mfma_f32_16x16x32_bf16 v[58:61], v[154:157], v[186:189], v[58:61]
	v_mfma_f32_16x16x32_bf16 v[86:89], v[150:153], v[166:169], v[86:89]
	v_mfma_f32_16x16x32_bf16 v[82:85], v[158:161], v[166:169], v[82:85]
	v_mfma_f32_16x16x32_bf16 v[78:81], v[150:153], v[174:177], v[78:81]
	v_mfma_f32_16x16x32_bf16 v[74:77], v[158:161], v[174:177], v[74:77]
	v_mfma_f32_16x16x32_bf16 v[70:73], v[150:153], v[182:185], v[70:73]
	v_mfma_f32_16x16x32_bf16 v[66:69], v[158:161], v[182:185], v[66:69]
	v_mfma_f32_16x16x32_bf16 v[62:65], v[150:153], v[190:193], v[62:65]
	v_mfma_f32_16x16x32_bf16 v[58:61], v[158:161], v[190:193], v[58:61]
	v_mfma_f32_16x16x32_bf16 v[54:57], v[130:133], v[162:165], v[54:57]
	v_mfma_f32_16x16x32_bf16 v[50:53], v[138:141], v[162:165], v[50:53]
	v_mfma_f32_16x16x32_bf16 v[46:49], v[130:133], v[170:173], v[46:49]
	v_mfma_f32_16x16x32_bf16 v[42:45], v[138:141], v[170:173], v[42:45]
	v_mfma_f32_16x16x32_bf16 v[34:37], v[130:133], v[178:181], v[34:37]
	v_mfma_f32_16x16x32_bf16 v[26:29], v[138:141], v[178:181], v[26:29]
	v_mfma_f32_16x16x32_bf16 v[18:21], v[130:133], v[186:189], v[18:21]
	v_mfma_f32_16x16x32_bf16 v[10:13], v[138:141], v[186:189], v[10:13]
	v_mfma_f32_16x16x32_bf16 v[54:57], v[134:137], v[166:169], v[54:57]
	v_mfma_f32_16x16x32_bf16 v[50:53], v[142:145], v[166:169], v[50:53]
	v_mfma_f32_16x16x32_bf16 v[46:49], v[134:137], v[174:177], v[46:49]
	v_mfma_f32_16x16x32_bf16 v[42:45], v[142:145], v[174:177], v[42:45]
	v_mfma_f32_16x16x32_bf16 v[34:37], v[134:137], v[182:185], v[34:37]
	v_mfma_f32_16x16x32_bf16 v[26:29], v[142:145], v[182:185], v[26:29]
	v_mfma_f32_16x16x32_bf16 v[18:21], v[134:137], v[190:193], v[18:21]
	v_mfma_f32_16x16x32_bf16 v[10:13], v[142:145], v[190:193], v[10:13]
	s_setprio 1
	s_barrier
	s_add_i32 s2, s2, s49
	v_lshl_add_u64 v[210:211], v[210:211], 0, s[12:13]
	s_mov_b32 m0, s2
	ds_read_b128 v[186:189], v209 offset:49152
	ds_read_b128 v[190:193], v209 offset:50176
	ds_read_b128 v[178:181], v209 offset:51200
	ds_read_b128 v[182:185], v209 offset:52224
	ds_read_b128 v[170:173], v209 offset:53248
	ds_read_b128 v[174:177], v209 offset:54272
	ds_read_b128 v[162:165], v209 offset:55296
	ds_read_b128 v[166:169], v209 offset:56320
	global_load_lds_dwordx4 v[210:211], off
	s_add_i32 m0, s2, 0x2000
	s_add_u32 s62, s64, 0x20080
	v_lshl_add_u64 v[210:211], v[212:213], 0, s[12:13]
	s_addc_u32 s63, s65, 0
	s_add_i32 s2, s66, s49
	global_load_lds_dwordx4 v[210:211], off
	v_lshl_add_u64 v[210:211], s[62:63], 0, v[196:197]
	s_mov_b32 m0, s2
	s_andn2_b64 vcc, exec, s[60:61]
	global_load_lds_dwordx4 v[210:211], off
	v_lshl_add_u64 v[210:211], s[62:63], 0, v[200:201]
	s_add_i32 m0, s2, 0x2000
	s_nop 0
	global_load_lds_dwordx4 v[210:211], off
	v_lshl_add_u64 v[210:211], v[214:215], 0, s[12:13]
	s_mov_b32 m0, s73
	s_nop 0
	global_load_lds_dwordx4 v[210:211], off
	v_lshl_add_u64 v[210:211], v[216:217], 0, s[12:13]
	s_mov_b32 m0, s74
	s_nop 0
	global_load_lds_dwordx4 v[210:211], off
	s_waitcnt vmcnt(8)
	s_waitcnt lgkmcnt(0)
	s_barrier
	s_cbranch_vccnz .LBB0_1104
	v_pk_mul_f32 v[214:215], v[86:87], s[20:21] op_sel_hi:[1,0]
	v_pk_mul_f32 v[216:217], v[82:83], s[20:21] op_sel_hi:[1,0]
	v_mov_b32_e32 v218, 0
	v_mov_b32_e32 v219, 0
	v_cvt_pk_fp8_f32 v218, v214, v215
	v_cvt_pk_fp8_f32 v219, v216, v217
	v_pk_mul_f32 v[214:215], v[88:89], s[20:21] op_sel_hi:[1,0]
	v_pk_mul_f32 v[216:217], v[84:85], s[20:21] op_sel_hi:[1,0]
	v_cvt_pk_fp8_f32 v218, v214, v215 op_sel:[0,0,1]
	v_cvt_pk_fp8_f32 v219, v216, v217 op_sel:[0,0,1]
	v_pk_mul_f32 v[214:215], v[54:55], s[20:21] op_sel_hi:[1,0]
	v_pk_mul_f32 v[216:217], v[50:51], s[20:21] op_sel_hi:[1,0]
	v_mov_b32_e32 v220, 0
	v_mov_b32_e32 v221, 0
	v_mov_b32_e32 v210, v1
	v_mov_b32_e32 v211, v204
	v_cvt_pk_fp8_f32 v220, v214, v215
	v_cvt_pk_fp8_f32 v221, v216, v217
	v_pk_mul_f32 v[214:215], v[56:57], s[20:21] op_sel_hi:[1,0]
	v_add_u32_e32 v210, s85, v210
	v_lshl_add_u32 v212, v211, 3, s86
	v_ashrrev_i32_e32 v211, 31, v210
	v_pk_mul_f32 v[216:217], v[52:53], s[20:21] op_sel_hi:[1,0]
	v_lshlrev_b64 v[210:211], 11, v[210:211]
	v_cvt_pk_fp8_f32 v220, v214, v215 op_sel:[0,0,1]
	v_cvt_pk_fp8_f32 v221, v216, v217 op_sel:[0,0,1]
	v_ashrrev_i32_e32 v213, 31, v212
	v_lshl_add_u64 v[210:211], s[10:11], 0, v[210:211]
	v_lshl_add_u64 v[210:211], v[210:211], 0, v[212:213]
	global_store_dwordx2 v[210:211], v[218:219], off
	global_store_dwordx2 v[210:211], v[220:221], off offset:128
	v_pk_mul_f32 v[214:215], v[78:79], s[20:21] op_sel_hi:[1,0]
	v_pk_mul_f32 v[216:217], v[74:75], s[20:21] op_sel_hi:[1,0]
	v_mov_b32_e32 v218, 0
	v_mov_b32_e32 v219, 0
	v_cvt_pk_fp8_f32 v218, v214, v215
	v_cvt_pk_fp8_f32 v219, v216, v217
	v_pk_mul_f32 v[214:215], v[80:81], s[20:21] op_sel_hi:[1,0]
	v_pk_mul_f32 v[216:217], v[76:77], s[20:21] op_sel_hi:[1,0]
	v_cvt_pk_fp8_f32 v218, v214, v215 op_sel:[0,0,1]
	v_cvt_pk_fp8_f32 v219, v216, v217 op_sel:[0,0,1]
	v_pk_mul_f32 v[214:215], v[46:47], s[20:21] op_sel_hi:[1,0]
	v_pk_mul_f32 v[216:217], v[42:43], s[20:21] op_sel_hi:[1,0]
	v_mov_b32_e32 v220, 0
	v_mov_b32_e32 v221, 0
	v_cvt_pk_fp8_f32 v220, v214, v215
	v_cvt_pk_fp8_f32 v221, v216, v217
	v_pk_mul_f32 v[214:215], v[48:49], s[20:21] op_sel_hi:[1,0]
	v_pk_mul_f32 v[216:217], v[44:45], s[20:21] op_sel_hi:[1,0]
	v_cvt_pk_fp8_f32 v220, v214, v215 op_sel:[0,0,1]
	v_cvt_pk_fp8_f32 v221, v216, v217 op_sel:[0,0,1]
	s_mov_b32 s2, 0x8000
	v_add_co_u32_e32 v214, vcc, s2, v210
	s_mov_b64 s[60:61], 0x8000
	s_nop 0
	v_addc_co_u32_e32 v215, vcc, 0, v211, vcc
	v_lshl_add_u64 v[212:213], v[210:211], 0, s[60:61]
	global_store_dwordx2 v[214:215], v[218:219], off
	global_store_dwordx2 v[212:213], v[220:221], off offset:128
	v_pk_mul_f32 v[214:215], v[70:71], s[20:21] op_sel_hi:[1,0]
	v_pk_mul_f32 v[216:217], v[66:67], s[20:21] op_sel_hi:[1,0]
	v_mov_b32_e32 v218, 0
	v_mov_b32_e32 v219, 0
	v_cvt_pk_fp8_f32 v218, v214, v215
	v_cvt_pk_fp8_f32 v219, v216, v217
	v_pk_mul_f32 v[214:215], v[72:73], s[20:21] op_sel_hi:[1,0]
	v_pk_mul_f32 v[216:217], v[68:69], s[20:21] op_sel_hi:[1,0]
	v_cvt_pk_fp8_f32 v218, v214, v215 op_sel:[0,0,1]
	v_cvt_pk_fp8_f32 v219, v216, v217 op_sel:[0,0,1]
	v_pk_mul_f32 v[214:215], v[34:35], s[20:21] op_sel_hi:[1,0]
	v_pk_mul_f32 v[216:217], v[26:27], s[20:21] op_sel_hi:[1,0]
	v_mov_b32_e32 v220, 0
	v_mov_b32_e32 v221, 0
	v_cvt_pk_fp8_f32 v220, v214, v215
	v_cvt_pk_fp8_f32 v221, v216, v217
	v_pk_mul_f32 v[214:215], v[36:37], s[20:21] op_sel_hi:[1,0]
	v_pk_mul_f32 v[216:217], v[28:29], s[20:21] op_sel_hi:[1,0]
	v_cvt_pk_fp8_f32 v220, v214, v215 op_sel:[0,0,1]
	v_cvt_pk_fp8_f32 v221, v216, v217 op_sel:[0,0,1]
	s_mov_b32 s2, 0x10000
	v_add_co_u32_e32 v214, vcc, s2, v210
	v_lshl_add_u64 v[212:213], v[210:211], 0, s[24:25]
	s_nop 0
	v_addc_co_u32_e32 v215, vcc, 0, v211, vcc
	global_store_dwordx2 v[214:215], v[218:219], off
	global_store_dwordx2 v[212:213], v[220:221], off offset:128
	v_pk_mul_f32 v[214:215], v[62:63], s[20:21] op_sel_hi:[1,0]
	v_pk_mul_f32 v[216:217], v[58:59], s[20:21] op_sel_hi:[1,0]
	v_mov_b32_e32 v218, 0
	v_mov_b32_e32 v219, 0
	v_cvt_pk_fp8_f32 v218, v214, v215
	v_cvt_pk_fp8_f32 v219, v216, v217
	v_pk_mul_f32 v[214:215], v[64:65], s[20:21] op_sel_hi:[1,0]
	v_pk_mul_f32 v[216:217], v[60:61], s[20:21] op_sel_hi:[1,0]
	v_cvt_pk_fp8_f32 v218, v214, v215 op_sel:[0,0,1]
	v_cvt_pk_fp8_f32 v219, v216, v217 op_sel:[0,0,1]
	v_pk_mul_f32 v[214:215], v[18:19], s[20:21] op_sel_hi:[1,0]
	v_pk_mul_f32 v[216:217], v[10:11], s[20:21] op_sel_hi:[1,0]
	v_mov_b32_e32 v220, 0
	v_mov_b32_e32 v221, 0
	v_cvt_pk_fp8_f32 v220, v214, v215
	v_cvt_pk_fp8_f32 v221, v216, v217
	v_pk_mul_f32 v[214:215], v[20:21], s[20:21] op_sel_hi:[1,0]
	v_pk_mul_f32 v[216:217], v[12:13], s[20:21] op_sel_hi:[1,0]
	v_cvt_pk_fp8_f32 v220, v214, v215 op_sel:[0,0,1]
	v_cvt_pk_fp8_f32 v221, v216, v217 op_sel:[0,0,1]
	s_mov_b32 s2, 0x18000
	v_lshl_add_u64 v[212:213], v[210:211], 0, s[28:29]
	v_add_co_u32_e32 v210, vcc, s2, v210
	s_nop 1
	v_addc_co_u32_e32 v211, vcc, 0, v211, vcc
	global_store_dwordx2 v[210:211], v[218:219], off
	global_store_dwordx2 v[212:213], v[220:221], off offset:128
	s_branch .LBB0_1104

.LBB0_1292:
.LBB0_1293:
	s_setprio 0
	s_waitcnt lgkmcnt(0)
	v_mfma_f32_16x16x32_bf16 v[126:129], v[146:149], v[186:189], v[126:129]
	v_mfma_f32_16x16x32_bf16 v[122:125], v[154:157], v[186:189], v[122:125]
	v_mfma_f32_16x16x32_bf16 v[114:117], v[146:149], v[178:181], v[114:117]
	v_mfma_f32_16x16x32_bf16 v[106:109], v[154:157], v[178:181], v[106:109]
	v_mfma_f32_16x16x32_bf16 v[102:105], v[146:149], v[170:173], v[102:105]
	v_mfma_f32_16x16x32_bf16 v[94:97], v[154:157], v[170:173], v[94:97]
	v_mfma_f32_16x16x32_bf16 v[86:89], v[146:149], v[162:165], v[86:89]
	v_mfma_f32_16x16x32_bf16 v[78:81], v[154:157], v[162:165], v[78:81]
	v_mfma_f32_16x16x32_bf16 v[126:129], v[150:153], v[190:193], v[126:129]
	v_mfma_f32_16x16x32_bf16 v[122:125], v[158:161], v[190:193], v[122:125]
	v_mfma_f32_16x16x32_bf16 v[114:117], v[150:153], v[182:185], v[114:117]
	v_mfma_f32_16x16x32_bf16 v[106:109], v[158:161], v[182:185], v[106:109]
	v_mfma_f32_16x16x32_bf16 v[102:105], v[150:153], v[174:177], v[102:105]
	v_mfma_f32_16x16x32_bf16 v[94:97], v[158:161], v[174:177], v[94:97]
	v_mfma_f32_16x16x32_bf16 v[86:89], v[150:153], v[166:169], v[86:89]
	v_mfma_f32_16x16x32_bf16 v[78:81], v[158:161], v[166:169], v[78:81]
	v_mfma_f32_16x16x32_bf16 v[118:121], v[130:133], v[186:189], v[118:121]
	v_mfma_f32_16x16x32_bf16 v[110:113], v[138:141], v[186:189], v[110:113]
	v_mfma_f32_16x16x32_bf16 v[98:101], v[130:133], v[178:181], v[98:101]
	v_mfma_f32_16x16x32_bf16 v[90:93], v[138:141], v[178:181], v[90:93]
	v_mfma_f32_16x16x32_bf16 v[82:85], v[130:133], v[170:173], v[82:85]
	v_mfma_f32_16x16x32_bf16 v[74:77], v[138:141], v[170:173], v[74:77]
	v_mfma_f32_16x16x32_bf16 v[70:73], v[130:133], v[162:165], v[70:73]
	v_mfma_f32_16x16x32_bf16 v[66:69], v[138:141], v[162:165], v[66:69]
	v_mfma_f32_16x16x32_bf16 v[118:121], v[134:137], v[190:193], v[118:121]
	v_mfma_f32_16x16x32_bf16 v[110:113], v[142:145], v[190:193], v[110:113]
	v_mfma_f32_16x16x32_bf16 v[98:101], v[134:137], v[182:185], v[98:101]
	v_mfma_f32_16x16x32_bf16 v[90:93], v[142:145], v[182:185], v[90:93]
	v_mfma_f32_16x16x32_bf16 v[82:85], v[134:137], v[174:177], v[82:85]
	v_mfma_f32_16x16x32_bf16 v[74:77], v[142:145], v[174:177], v[74:77]
	v_mfma_f32_16x16x32_bf16 v[70:73], v[134:137], v[166:169], v[70:73]
	v_mfma_f32_16x16x32_bf16 v[66:69], v[142:145], v[166:169], v[66:69]
	s_setprio 1
	s_barrier
	s_add_i32 s73, s73, 2
	s_cmp_gt_u32 s73, 29
	s_cbranch_scc1 .LBB0_1299
.LBB0_1294:
	s_mov_b64 s[56:57], s[40:41]
	s_add_u32 s2, s71, s56
	s_addc_u32 s22, s72, s57
	s_add_u32 s40, s56, 0x100
	s_addc_u32 s41, s57, 0
	s_cmp_eq_u32 s73, 28
	s_cselect_b64 s[8:9], -1, 0
	s_and_b64 s[12:13], s[8:9], exec
	s_cselect_b32 s61, s67, s22
	s_cselect_b32 s60, s68, s2
	s_cselect_b32 s2, 0, s40
	s_add_i32 s22, s86, s42
	s_add_i32 m0, s51, 0xc000
	s_add_i32 s13, s51, 0xe000
	s_add_i32 s23, s22, 0x2000
	s_add_u32 s62, s60, 0x80000
	s_addc_u32 s63, s61, 0
	s_add_i32 s24, s87, s42
	s_add_i32 s25, s24, 0x2000
	s_and_b64 s[8:9], s[6:7], s[8:9]
	ds_read_b128 v[130:133], v229
	ds_read_b128 v[134:137], v229 offset:1024
	ds_read_b128 v[138:141], v229 offset:2048
	ds_read_b128 v[142:145], v229 offset:3072
	ds_read_b128 v[146:149], v230
	ds_read_b128 v[150:153], v230 offset:1024
	ds_read_b128 v[154:157], v230 offset:2048
	ds_read_b128 v[158:161], v230 offset:3072
	s_and_b64 s[8:9], s[8:9], exec
	s_cselect_b32 s9, s30, s36
	s_cselect_b32 s8, s31, s37
	s_add_u32 s64, s9, s2
	s_addc_u32 s65, s8, 0
	s_add_i32 s82, 0, 0x18000
	s_add_i32 s83, 0, 0x1c000
	s_add_u32 s58, s64, 0x80000
	s_addc_u32 s59, s65, 0
	s_add_i32 s8, s82, s42
	s_add_i32 s2, s8, 0x2000
	s_add_u32 s54, s60, 0x80080
	s_addc_u32 s55, s61, 0
	s_add_i32 s12, s83, s42
	s_add_i32 s9, s12, 0x2000
	s_cmp_lg_u32 s73, 28
	v_lshl_add_u64 v[224:225], v[220:221], 0, s[56:57]
	ds_read_b128 v[162:165], v231
	ds_read_b128 v[166:169], v231 offset:1024
	ds_read_b128 v[170:173], v231 offset:2048
	ds_read_b128 v[174:177], v231 offset:3072
	ds_read_b128 v[178:181], v231 offset:4096
	ds_read_b128 v[182:185], v231 offset:5120
	ds_read_b128 v[186:189], v231 offset:6144
	ds_read_b128 v[190:193], v231 offset:7168
	global_load_lds_dwordx4 v[224:225], off
	v_lshl_add_u64 v[224:225], v[222:223], 0, s[56:57]
	s_mov_b32 m0, s13
	s_nop 0
	global_load_lds_dwordx4 v[224:225], off
	s_waitcnt vmcnt(8)
	s_waitcnt lgkmcnt(0)
	s_barrier
	s_setprio 0
	s_waitcnt lgkmcnt(0)
	v_mfma_f32_16x16x32_bf16 v[62:65], v[130:133], v[162:165], v[62:65]
	v_mfma_f32_16x16x32_bf16 v[58:61], v[138:141], v[162:165], v[58:61]
	v_mfma_f32_16x16x32_bf16 v[54:57], v[130:133], v[170:173], v[54:57]
	v_mfma_f32_16x16x32_bf16 v[50:53], v[138:141], v[170:173], v[50:53]
	v_mfma_f32_16x16x32_bf16 v[46:49], v[130:133], v[178:181], v[46:49]
	v_mfma_f32_16x16x32_bf16 v[42:45], v[138:141], v[178:181], v[42:45]
	v_mfma_f32_16x16x32_bf16 v[38:41], v[130:133], v[186:189], v[38:41]
	v_mfma_f32_16x16x32_bf16 v[34:37], v[138:141], v[186:189], v[34:37]
	v_mfma_f32_16x16x32_bf16 v[62:65], v[134:137], v[166:169], v[62:65]
	v_mfma_f32_16x16x32_bf16 v[58:61], v[142:145], v[166:169], v[58:61]
	v_mfma_f32_16x16x32_bf16 v[54:57], v[134:137], v[174:177], v[54:57]
	v_mfma_f32_16x16x32_bf16 v[50:53], v[142:145], v[174:177], v[50:53]
	v_mfma_f32_16x16x32_bf16 v[46:49], v[134:137], v[182:185], v[46:49]
	v_mfma_f32_16x16x32_bf16 v[42:45], v[142:145], v[182:185], v[42:45]
	v_mfma_f32_16x16x32_bf16 v[38:41], v[134:137], v[190:193], v[38:41]
	v_mfma_f32_16x16x32_bf16 v[34:37], v[142:145], v[190:193], v[34:37]
	v_mfma_f32_16x16x32_bf16 v[30:33], v[146:149], v[162:165], v[30:33]
	v_mfma_f32_16x16x32_bf16 v[26:29], v[154:157], v[162:165], v[26:29]
	v_mfma_f32_16x16x32_bf16 v[22:25], v[146:149], v[170:173], v[22:25]
	v_mfma_f32_16x16x32_bf16 v[18:21], v[154:157], v[170:173], v[18:21]
	v_mfma_f32_16x16x32_bf16 v[14:17], v[146:149], v[178:181], v[14:17]
	v_mfma_f32_16x16x32_bf16 v[10:13], v[154:157], v[178:181], v[10:13]
	v_mfma_f32_16x16x32_bf16 v[6:9], v[146:149], v[186:189], v[6:9]
	v_mfma_f32_16x16x32_bf16 v[2:5], v[154:157], v[186:189], v[2:5]
	v_mfma_f32_16x16x32_bf16 v[30:33], v[150:153], v[166:169], v[30:33]
	v_mfma_f32_16x16x32_bf16 v[26:29], v[158:161], v[166:169], v[26:29]
	v_mfma_f32_16x16x32_bf16 v[22:25], v[150:153], v[174:177], v[22:25]
	v_mfma_f32_16x16x32_bf16 v[18:21], v[158:161], v[174:177], v[18:21]
	v_mfma_f32_16x16x32_bf16 v[14:17], v[150:153], v[182:185], v[14:17]
	v_mfma_f32_16x16x32_bf16 v[10:13], v[158:161], v[182:185], v[10:13]
	v_mfma_f32_16x16x32_bf16 v[6:9], v[150:153], v[190:193], v[6:9]
	v_mfma_f32_16x16x32_bf16 v[2:5], v[158:161], v[190:193], v[2:5]
	s_setprio 1
	s_barrier
	s_mov_b32 m0, s22
	v_lshl_add_u64 v[224:225], s[60:61], 0, v[196:197]
	ds_read_b128 v[162:165], v231 offset:16384
	ds_read_b128 v[166:169], v231 offset:17408
	ds_read_b128 v[170:173], v231 offset:18432
	ds_read_b128 v[174:177], v231 offset:19456
	ds_read_b128 v[178:181], v231 offset:20480
	ds_read_b128 v[182:185], v231 offset:21504
	ds_read_b128 v[186:189], v231 offset:22528
	ds_read_b128 v[190:193], v231 offset:23552
	global_load_lds_dwordx4 v[224:225], off
	v_lshl_add_u64 v[232:233], s[60:61], 0, v[200:201]
	s_mov_b32 m0, s23
	v_lshl_add_u64 v[234:235], s[62:63], 0, v[196:197]
	global_load_lds_dwordx4 v[232:233], off
	s_mov_b32 m0, s24
	v_lshl_add_u64 v[236:237], s[64:65], 0, v[198:199]
	global_load_lds_dwordx4 v[234:235], off
	v_lshl_add_u64 v[234:235], s[62:63], 0, v[200:201]
	s_mov_b32 m0, s25
	s_nop 0
	global_load_lds_dwordx4 v[234:235], off
	v_lshl_add_u64 v[234:235], s[64:65], 0, v[194:195]
	s_mov_b32 m0, s51
	s_nop 0
	global_load_lds_dwordx4 v[234:235], off
	s_mov_b32 m0, s52
	s_nop 0
	global_load_lds_dwordx4 v[236:237], off
	s_waitcnt vmcnt(8)
	s_waitcnt lgkmcnt(0)
	s_barrier
	s_setprio 0
	s_waitcnt lgkmcnt(0)
	v_mfma_f32_16x16x32_bf16 v[126:129], v[130:133], v[162:165], v[126:129]
	v_mfma_f32_16x16x32_bf16 v[122:125], v[138:141], v[162:165], v[122:125]
	v_mfma_f32_16x16x32_bf16 v[114:117], v[130:133], v[170:173], v[114:117]
	v_mfma_f32_16x16x32_bf16 v[106:109], v[138:141], v[170:173], v[106:109]
	v_mfma_f32_16x16x32_bf16 v[102:105], v[130:133], v[178:181], v[102:105]
	v_mfma_f32_16x16x32_bf16 v[94:97], v[138:141], v[178:181], v[94:97]
	v_mfma_f32_16x16x32_bf16 v[86:89], v[130:133], v[186:189], v[86:89]
	v_mfma_f32_16x16x32_bf16 v[78:81], v[138:141], v[186:189], v[78:81]
	v_mfma_f32_16x16x32_bf16 v[126:129], v[134:137], v[166:169], v[126:129]
	v_mfma_f32_16x16x32_bf16 v[122:125], v[142:145], v[166:169], v[122:125]
	v_mfma_f32_16x16x32_bf16 v[114:117], v[134:137], v[174:177], v[114:117]
	v_mfma_f32_16x16x32_bf16 v[106:109], v[142:145], v[174:177], v[106:109]
	v_mfma_f32_16x16x32_bf16 v[102:105], v[134:137], v[182:185], v[102:105]
	v_mfma_f32_16x16x32_bf16 v[94:97], v[142:145], v[182:185], v[94:97]
	v_mfma_f32_16x16x32_bf16 v[86:89], v[134:137], v[190:193], v[86:89]
	v_mfma_f32_16x16x32_bf16 v[78:81], v[142:145], v[190:193], v[78:81]
	v_mfma_f32_16x16x32_bf16 v[118:121], v[146:149], v[162:165], v[118:121]
	v_mfma_f32_16x16x32_bf16 v[110:113], v[154:157], v[162:165], v[110:113]
	v_mfma_f32_16x16x32_bf16 v[98:101], v[146:149], v[170:173], v[98:101]
	v_mfma_f32_16x16x32_bf16 v[90:93], v[154:157], v[170:173], v[90:93]
	v_mfma_f32_16x16x32_bf16 v[82:85], v[146:149], v[178:181], v[82:85]
	v_mfma_f32_16x16x32_bf16 v[74:77], v[154:157], v[178:181], v[74:77]
	v_mfma_f32_16x16x32_bf16 v[70:73], v[146:149], v[186:189], v[70:73]
	v_mfma_f32_16x16x32_bf16 v[66:69], v[154:157], v[186:189], v[66:69]
	v_mfma_f32_16x16x32_bf16 v[118:121], v[150:153], v[166:169], v[118:121]
	v_mfma_f32_16x16x32_bf16 v[110:113], v[158:161], v[166:169], v[110:113]
	v_mfma_f32_16x16x32_bf16 v[98:101], v[150:153], v[174:177], v[98:101]
	v_mfma_f32_16x16x32_bf16 v[90:93], v[158:161], v[174:177], v[90:93]
	v_mfma_f32_16x16x32_bf16 v[82:85], v[150:153], v[182:185], v[82:85]
	v_mfma_f32_16x16x32_bf16 v[74:77], v[158:161], v[182:185], v[74:77]
	v_mfma_f32_16x16x32_bf16 v[70:73], v[150:153], v[190:193], v[70:73]
	v_mfma_f32_16x16x32_bf16 v[66:69], v[158:161], v[190:193], v[66:69]
	s_setprio 1
	s_barrier
	v_add_u32_e32 v130, s82, v227
	v_add_u32_e32 v142, s83, v227
	ds_read_b128 v[146:149], v130
	ds_read_b128 v[150:153], v130 offset:1024
	ds_read_b128 v[154:157], v130 offset:2048
	ds_read_b128 v[158:161], v130 offset:3072
	ds_read_b128 v[130:133], v142
	ds_read_b128 v[134:137], v142 offset:1024
	ds_read_b128 v[138:141], v142 offset:2048
	ds_read_b128 v[142:145], v142 offset:3072
	s_mov_b32 m0, s53
	v_lshl_add_u64 v[238:239], s[58:59], 0, v[194:195]
	ds_read_b128 v[162:165], v231 offset:32768
	ds_read_b128 v[166:169], v231 offset:33792
	ds_read_b128 v[170:173], v231 offset:34816
	ds_read_b128 v[174:177], v231 offset:35840
	ds_read_b128 v[178:181], v231 offset:36864
	ds_read_b128 v[182:185], v231 offset:37888
	ds_read_b128 v[186:189], v231 offset:38912
	ds_read_b128 v[190:193], v231 offset:39936
	global_load_lds_dwordx4 v[238:239], off
	v_lshl_add_u64 v[238:239], s[58:59], 0, v[198:199]
	s_mov_b32 m0, s74
	s_nop 0
	global_load_lds_dwordx4 v[238:239], off
	s_waitcnt vmcnt(8)
	s_waitcnt lgkmcnt(0)
	s_barrier
	s_setprio 0
	s_waitcnt lgkmcnt(0)
	v_mfma_f32_16x16x32_bf16 v[62:65], v[146:149], v[162:165], v[62:65]
	v_mfma_f32_16x16x32_bf16 v[58:61], v[154:157], v[162:165], v[58:61]
	v_mfma_f32_16x16x32_bf16 v[54:57], v[146:149], v[170:173], v[54:57]
	v_mfma_f32_16x16x32_bf16 v[50:53], v[154:157], v[170:173], v[50:53]
	v_mfma_f32_16x16x32_bf16 v[46:49], v[146:149], v[178:181], v[46:49]
	v_mfma_f32_16x16x32_bf16 v[42:45], v[154:157], v[178:181], v[42:45]
	v_mfma_f32_16x16x32_bf16 v[38:41], v[146:149], v[186:189], v[38:41]
	v_mfma_f32_16x16x32_bf16 v[34:37], v[154:157], v[186:189], v[34:37]
	v_mfma_f32_16x16x32_bf16 v[62:65], v[150:153], v[166:169], v[62:65]
	v_mfma_f32_16x16x32_bf16 v[58:61], v[158:161], v[166:169], v[58:61]
	v_mfma_f32_16x16x32_bf16 v[54:57], v[150:153], v[174:177], v[54:57]
	v_mfma_f32_16x16x32_bf16 v[50:53], v[158:161], v[174:177], v[50:53]
	v_mfma_f32_16x16x32_bf16 v[46:49], v[150:153], v[182:185], v[46:49]
	v_mfma_f32_16x16x32_bf16 v[42:45], v[158:161], v[182:185], v[42:45]
	v_mfma_f32_16x16x32_bf16 v[38:41], v[150:153], v[190:193], v[38:41]
	v_mfma_f32_16x16x32_bf16 v[34:37], v[158:161], v[190:193], v[34:37]
	v_mfma_f32_16x16x32_bf16 v[30:33], v[130:133], v[162:165], v[30:33]
	v_mfma_f32_16x16x32_bf16 v[26:29], v[138:141], v[162:165], v[26:29]
	v_mfma_f32_16x16x32_bf16 v[22:25], v[130:133], v[170:173], v[22:25]
	v_mfma_f32_16x16x32_bf16 v[18:21], v[138:141], v[170:173], v[18:21]
	v_mfma_f32_16x16x32_bf16 v[14:17], v[130:133], v[178:181], v[14:17]
	v_mfma_f32_16x16x32_bf16 v[10:13], v[138:141], v[178:181], v[10:13]
	v_mfma_f32_16x16x32_bf16 v[6:9], v[130:133], v[186:189], v[6:9]
	v_mfma_f32_16x16x32_bf16 v[2:5], v[138:141], v[186:189], v[2:5]
	v_mfma_f32_16x16x32_bf16 v[30:33], v[134:137], v[166:169], v[30:33]
	v_mfma_f32_16x16x32_bf16 v[26:29], v[142:145], v[166:169], v[26:29]
	v_mfma_f32_16x16x32_bf16 v[22:25], v[134:137], v[174:177], v[22:25]
	v_mfma_f32_16x16x32_bf16 v[18:21], v[142:145], v[174:177], v[18:21]
	v_mfma_f32_16x16x32_bf16 v[14:17], v[134:137], v[182:185], v[14:17]
	v_mfma_f32_16x16x32_bf16 v[10:13], v[142:145], v[182:185], v[10:13]
	v_mfma_f32_16x16x32_bf16 v[6:9], v[134:137], v[190:193], v[6:9]
	v_mfma_f32_16x16x32_bf16 v[2:5], v[142:145], v[190:193], v[2:5]
	s_setprio 1
	s_barrier
	s_mov_b32 m0, s8
	v_lshl_add_u64 v[224:225], v[224:225], 0, s[18:19]
	ds_read_b128 v[186:189], v231 offset:49152
	ds_read_b128 v[190:193], v231 offset:50176
	ds_read_b128 v[178:181], v231 offset:51200
	ds_read_b128 v[182:185], v231 offset:52224
	ds_read_b128 v[170:173], v231 offset:53248
	ds_read_b128 v[174:177], v231 offset:54272
	ds_read_b128 v[162:165], v231 offset:55296
	ds_read_b128 v[166:169], v231 offset:56320
	global_load_lds_dwordx4 v[224:225], off
	v_lshl_add_u64 v[224:225], v[232:233], 0, s[18:19]
	s_mov_b32 m0, s2
	s_nop 0
	global_load_lds_dwordx4 v[224:225], off
	v_lshl_add_u64 v[224:225], s[54:55], 0, v[196:197]
	s_mov_b32 m0, s12
	s_nop 0
	global_load_lds_dwordx4 v[224:225], off
	v_lshl_add_u64 v[224:225], s[54:55], 0, v[200:201]
	s_mov_b32 m0, s9
	s_nop 0
	global_load_lds_dwordx4 v[224:225], off
	v_lshl_add_u64 v[224:225], v[234:235], 0, s[18:19]
	s_mov_b32 m0, s78
	s_nop 0
	global_load_lds_dwordx4 v[224:225], off
	v_lshl_add_u64 v[224:225], v[236:237], 0, s[18:19]
	s_mov_b32 m0, s79
	s_nop 0
	global_load_lds_dwordx4 v[224:225], off
	s_waitcnt vmcnt(8)
	s_waitcnt lgkmcnt(0)
	s_barrier
	s_cbranch_scc1 .LBB0_1293
	v_mov_b32_e32 v202, v1
	v_mov_b32_e32 v224, v209
	s_mov_b64 s[54:55], -1
	v_add_u32_e32 v202, s69, v202
	v_lshlrev_b32_e32 v224, 3, v224
	s_and_b64 vcc, exec, s[38:39]
	v_add_u32_e32 v234, 16, v202
	v_add_u32_e32 v233, 32, v202
	v_add_u32_e32 v232, 48, v202
	s_cbranch_vccz .LBB0_1297
	v_add_u32_e32 v236, s70, v224
	v_ashrrev_i32_e32 v237, 31, v236
	v_mov_b64_e32 v[240:241], s[14:15]
	v_mad_i64_i32 v[238:239], s[8:9], v202, s88, v[240:241]
	v_lshlrev_b64 v[244:245], 1, v[236:237]
	v_lshl_add_u64 v[246:247], v[238:239], 0, v[244:245]
	v_cvt_pk_bf16_f32 v236, v62, v63
	v_cvt_pk_bf16_f32 v237, v64, v65
	v_cvt_pk_bf16_f32 v238, v58, v59
	v_cvt_pk_bf16_f32 v239, v60, v61
	global_store_dwordx4 v[246:247], v[236:239], off
	s_mov_b64 s[54:55], 0
	s_nop 0
	v_cvt_pk_bf16_f32 v236, v30, v31
	v_cvt_pk_bf16_f32 v237, v32, v33
	v_cvt_pk_bf16_f32 v238, v26, v27
	v_cvt_pk_bf16_f32 v239, v28, v29
	global_store_dwordx4 v[246:247], v[236:239], off offset:256
	s_nop 1
	v_mad_i64_i32 v[236:237], s[8:9], v234, s88, v[240:241]
	v_lshl_add_u64 v[246:247], v[236:237], 0, v[244:245]
	v_cvt_pk_bf16_f32 v236, v54, v55
	v_cvt_pk_bf16_f32 v237, v56, v57
	v_cvt_pk_bf16_f32 v238, v50, v51
	v_cvt_pk_bf16_f32 v239, v52, v53
	global_store_dwordx4 v[246:247], v[236:239], off
	s_nop 1
	v_cvt_pk_bf16_f32 v236, v22, v23
	v_cvt_pk_bf16_f32 v237, v24, v25
	v_cvt_pk_bf16_f32 v238, v18, v19
	v_cvt_pk_bf16_f32 v239, v20, v21
	global_store_dwordx4 v[246:247], v[236:239], off offset:256
	s_nop 1
	v_mad_i64_i32 v[236:237], s[8:9], v233, s88, v[240:241]
	v_lshl_add_u64 v[246:247], v[236:237], 0, v[244:245]
	v_cvt_pk_bf16_f32 v236, v46, v47
	v_cvt_pk_bf16_f32 v237, v48, v49
	v_cvt_pk_bf16_f32 v238, v42, v43
	v_cvt_pk_bf16_f32 v239, v44, v45
	global_store_dwordx4 v[246:247], v[236:239], off
	s_nop 1
	v_cvt_pk_bf16_f32 v236, v14, v15
	v_cvt_pk_bf16_f32 v237, v16, v17
	v_cvt_pk_bf16_f32 v238, v10, v11
	v_cvt_pk_bf16_f32 v239, v12, v13
	global_store_dwordx4 v[246:247], v[236:239], off offset:256
	s_nop 1
	v_mad_i64_i32 v[236:237], s[8:9], v232, s88, v[240:241]
	v_lshl_add_u64 v[240:241], v[236:237], 0, v[244:245]
	v_cvt_pk_bf16_f32 v236, v38, v39
	v_cvt_pk_bf16_f32 v237, v40, v41
	v_cvt_pk_bf16_f32 v238, v34, v35
	v_cvt_pk_bf16_f32 v239, v36, v37
	global_store_dwordx4 v[240:241], v[236:239], off
	s_nop 1
	v_cvt_pk_bf16_f32 v236, v6, v7
	v_cvt_pk_bf16_f32 v237, v8, v9
	v_cvt_pk_bf16_f32 v238, v2, v3
	v_cvt_pk_bf16_f32 v239, v4, v5
	global_store_dwordx4 v[240:241], v[236:239], off offset:256

.LBB0_1547:
	ds_read_b128 v[134:137], v189
	ds_read_b128 v[138:141], v189 offset:1024
	ds_read_b128 v[142:145], v189 offset:2048
	ds_read_b128 v[146:149], v189 offset:3072
	ds_read_b128 v[150:153], v190
	ds_read_b128 v[170:173], v190 offset:1024
	ds_read_b128 v[174:177], v190 offset:2048
	ds_read_b128 v[194:197], v190 offset:3072
	s_add_u32 s2, s66, s54
	s_addc_u32 s69, s67, s55
	s_add_u32 s56, s54, 0x100
	s_addc_u32 s57, s55, 0
	s_cmp_eq_u32 s68, 28
	s_cselect_b64 s[60:61], -1, 0
	s_and_b64 s[58:59], s[60:61], exec
	s_cselect_b32 s59, s31, s69
	s_cselect_b32 s58, s35, s2
	s_cselect_b32 s2, 0, s56
	v_lshl_add_u64 v[178:179], v[130:131], 0, s[54:55]
	s_add_i32 m0, s13, 0xc000
	ds_read_b128 v[198:201], v191
	ds_read_b128 v[202:205], v191 offset:1024
	ds_read_b128 v[206:209], v191 offset:2048
	ds_read_b128 v[210:213], v191 offset:3072
	ds_read_b128 v[214:217], v191 offset:4096
	ds_read_b128 v[218:221], v191 offset:5120
	ds_read_b128 v[222:225], v191 offset:6144
	ds_read_b128 v[226:229], v191 offset:7168
	global_load_lds_dwordx4 v[178:179], off
	v_lshl_add_u64 v[178:179], v[132:133], 0, s[54:55]
	s_add_i32 m0, s13, 0xe000
	s_nop 0
	global_load_lds_dwordx4 v[178:179], off
	s_waitcnt vmcnt(8)
	s_waitcnt lgkmcnt(0)
	s_barrier
	s_setprio 0
	s_waitcnt lgkmcnt(0)
	v_mfma_f32_16x16x32_bf16 v[126:129], v[134:137], v[198:201], v[126:129]
	v_mfma_f32_16x16x32_bf16 v[122:125], v[142:145], v[198:201], v[122:125]
	v_mfma_f32_16x16x32_bf16 v[110:113], v[134:137], v[206:209], v[110:113]
	v_mfma_f32_16x16x32_bf16 v[106:109], v[142:145], v[206:209], v[106:109]
	v_mfma_f32_16x16x32_bf16 v[94:97], v[134:137], v[214:217], v[94:97]
	v_mfma_f32_16x16x32_bf16 v[90:93], v[142:145], v[214:217], v[90:93]
	v_mfma_f32_16x16x32_bf16 v[78:81], v[134:137], v[222:225], v[78:81]
	v_mfma_f32_16x16x32_bf16 v[74:77], v[142:145], v[222:225], v[74:77]
	v_mfma_f32_16x16x32_bf16 v[126:129], v[138:141], v[202:205], v[126:129]
	v_mfma_f32_16x16x32_bf16 v[122:125], v[146:149], v[202:205], v[122:125]
	v_mfma_f32_16x16x32_bf16 v[110:113], v[138:141], v[210:213], v[110:113]
	v_mfma_f32_16x16x32_bf16 v[106:109], v[146:149], v[210:213], v[106:109]
	v_mfma_f32_16x16x32_bf16 v[94:97], v[138:141], v[218:221], v[94:97]
	v_mfma_f32_16x16x32_bf16 v[90:93], v[146:149], v[218:221], v[90:93]
	v_mfma_f32_16x16x32_bf16 v[78:81], v[138:141], v[226:229], v[78:81]
	v_mfma_f32_16x16x32_bf16 v[74:77], v[146:149], v[226:229], v[74:77]
	v_mfma_f32_16x16x32_bf16 v[118:121], v[150:153], v[198:201], v[118:121]
	v_mfma_f32_16x16x32_bf16 v[114:117], v[174:177], v[198:201], v[114:117]
	v_mfma_f32_16x16x32_bf16 v[102:105], v[150:153], v[206:209], v[102:105]
	v_mfma_f32_16x16x32_bf16 v[98:101], v[174:177], v[206:209], v[98:101]
	v_mfma_f32_16x16x32_bf16 v[86:89], v[150:153], v[214:217], v[86:89]
	v_mfma_f32_16x16x32_bf16 v[82:85], v[174:177], v[214:217], v[82:85]
	v_mfma_f32_16x16x32_bf16 v[70:73], v[150:153], v[222:225], v[70:73]
	v_mfma_f32_16x16x32_bf16 v[66:69], v[174:177], v[222:225], v[66:69]
	v_mfma_f32_16x16x32_bf16 v[118:121], v[170:173], v[202:205], v[118:121]
	v_mfma_f32_16x16x32_bf16 v[114:117], v[194:197], v[202:205], v[114:117]
	v_mfma_f32_16x16x32_bf16 v[102:105], v[170:173], v[210:213], v[102:105]
	v_mfma_f32_16x16x32_bf16 v[98:101], v[194:197], v[210:213], v[98:101]
	v_mfma_f32_16x16x32_bf16 v[86:89], v[170:173], v[218:221], v[86:89]
	v_mfma_f32_16x16x32_bf16 v[82:85], v[194:197], v[218:221], v[82:85]
	v_mfma_f32_16x16x32_bf16 v[70:73], v[170:173], v[226:229], v[70:73]
	v_mfma_f32_16x16x32_bf16 v[66:69], v[194:197], v[226:229], v[66:69]
	s_setprio 1
	s_barrier
	s_add_i32 s54, s63, s42
	v_lshl_add_u64 v[178:179], s[58:59], 0, v[156:157]
	s_mov_b32 m0, s54
	ds_read_b128 v[198:201], v191 offset:16384
	ds_read_b128 v[202:205], v191 offset:17408
	ds_read_b128 v[206:209], v191 offset:18432
	ds_read_b128 v[210:213], v191 offset:19456
	ds_read_b128 v[214:217], v191 offset:20480
	ds_read_b128 v[218:221], v191 offset:21504
	ds_read_b128 v[222:225], v191 offset:22528
	ds_read_b128 v[226:229], v191 offset:23552
	global_load_lds_dwordx4 v[178:179], off
	s_add_i32 m0, s54, 0x2000
	s_add_u32 s54, s58, 0x80000
	v_lshl_add_u64 v[182:183], s[58:59], 0, v[160:161]
	s_addc_u32 s55, s59, 0
	s_add_i32 s69, s64, s42
	global_load_lds_dwordx4 v[182:183], off
	v_lshl_add_u64 v[186:187], s[54:55], 0, v[156:157]
	s_mov_b32 m0, s69
	s_nop 0
	global_load_lds_dwordx4 v[186:187], off
	v_lshl_add_u64 v[186:187], s[54:55], 0, v[160:161]
	s_add_i32 m0, s69, 0x2000
	s_and_b64 s[54:55], s[8:9], s[60:61]
	s_and_b64 s[54:55], s[54:55], exec
	s_cselect_b32 s54, s36, s40
	s_cselect_b32 s55, s37, s41
	s_add_u32 s54, s54, s2
	s_addc_u32 s55, s55, 0
	global_load_lds_dwordx4 v[186:187], off
	v_lshl_add_u64 v[186:187], s[54:55], 0, v[154:155]
	s_mov_b32 m0, s13
	v_lshl_add_u64 v[230:231], s[54:55], 0, v[158:159]
	global_load_lds_dwordx4 v[186:187], off
	s_mov_b32 m0, s43
	s_nop 0
	global_load_lds_dwordx4 v[230:231], off
	s_waitcnt vmcnt(8)
	s_waitcnt lgkmcnt(0)
	s_barrier
	s_setprio 0
	s_waitcnt lgkmcnt(0)
	v_mfma_f32_16x16x32_bf16 v[62:65], v[134:137], v[198:201], v[62:65]
	v_mfma_f32_16x16x32_bf16 v[58:61], v[142:145], v[198:201], v[58:61]
	v_mfma_f32_16x16x32_bf16 v[46:49], v[134:137], v[206:209], v[46:49]
	v_mfma_f32_16x16x32_bf16 v[42:45], v[142:145], v[206:209], v[42:45]
	v_mfma_f32_16x16x32_bf16 v[30:33], v[134:137], v[214:217], v[30:33]
	v_mfma_f32_16x16x32_bf16 v[26:29], v[142:145], v[214:217], v[26:29]
	v_mfma_f32_16x16x32_bf16 v[14:17], v[134:137], v[222:225], v[14:17]
	v_mfma_f32_16x16x32_bf16 v[10:13], v[142:145], v[222:225], v[10:13]
	v_mfma_f32_16x16x32_bf16 v[62:65], v[138:141], v[202:205], v[62:65]
	v_mfma_f32_16x16x32_bf16 v[58:61], v[146:149], v[202:205], v[58:61]
	v_mfma_f32_16x16x32_bf16 v[46:49], v[138:141], v[210:213], v[46:49]
	v_mfma_f32_16x16x32_bf16 v[42:45], v[146:149], v[210:213], v[42:45]
	v_mfma_f32_16x16x32_bf16 v[30:33], v[138:141], v[218:221], v[30:33]
	v_mfma_f32_16x16x32_bf16 v[26:29], v[146:149], v[218:221], v[26:29]
	v_mfma_f32_16x16x32_bf16 v[14:17], v[138:141], v[226:229], v[14:17]
	v_mfma_f32_16x16x32_bf16 v[10:13], v[146:149], v[226:229], v[10:13]
	v_mfma_f32_16x16x32_bf16 v[54:57], v[150:153], v[198:201], v[54:57]
	v_mfma_f32_16x16x32_bf16 v[50:53], v[174:177], v[198:201], v[50:53]
	v_mfma_f32_16x16x32_bf16 v[38:41], v[150:153], v[206:209], v[38:41]
	v_mfma_f32_16x16x32_bf16 v[34:37], v[174:177], v[206:209], v[34:37]
	v_mfma_f32_16x16x32_bf16 v[22:25], v[150:153], v[214:217], v[22:25]
	v_mfma_f32_16x16x32_bf16 v[18:21], v[174:177], v[214:217], v[18:21]
	v_mfma_f32_16x16x32_bf16 v[6:9], v[150:153], v[222:225], v[6:9]
	v_mfma_f32_16x16x32_bf16 v[2:5], v[174:177], v[222:225], v[2:5]
	v_mfma_f32_16x16x32_bf16 v[54:57], v[170:173], v[202:205], v[54:57]
	v_mfma_f32_16x16x32_bf16 v[50:53], v[194:197], v[202:205], v[50:53]
	v_mfma_f32_16x16x32_bf16 v[38:41], v[170:173], v[210:213], v[38:41]
	v_mfma_f32_16x16x32_bf16 v[34:37], v[194:197], v[210:213], v[34:37]
	v_mfma_f32_16x16x32_bf16 v[22:25], v[170:173], v[218:221], v[22:25]
	v_mfma_f32_16x16x32_bf16 v[18:21], v[194:197], v[218:221], v[18:21]
	v_mfma_f32_16x16x32_bf16 v[6:9], v[170:173], v[226:229], v[6:9]
	v_mfma_f32_16x16x32_bf16 v[2:5], v[194:197], v[226:229], v[2:5]
	s_setprio 1
	s_barrier
	s_add_i32 s2, 0, 0x18000
	s_add_i32 s60, 0, 0x1c000
	v_add_u32_e32 v146, s2, v181
	v_add_u32_e32 v180, s60, v181
	ds_read_b128 v[134:137], v146
	ds_read_b128 v[138:141], v146 offset:1024
	ds_read_b128 v[142:145], v146 offset:2048
	ds_read_b128 v[146:149], v146 offset:3072
	ds_read_b128 v[150:153], v180
	ds_read_b128 v[170:173], v180 offset:1024
	ds_read_b128 v[174:177], v180 offset:2048
	ds_read_b128 v[194:197], v180 offset:3072
	s_add_u32 s54, s54, 0x80000
	s_addc_u32 s55, s55, 0
	s_mov_b32 m0, s48
	v_lshl_add_u64 v[232:233], s[54:55], 0, v[154:155]
	ds_read_b128 v[198:201], v191 offset:32768
	ds_read_b128 v[202:205], v191 offset:33792
	ds_read_b128 v[206:209], v191 offset:34816
	ds_read_b128 v[210:213], v191 offset:35840
	ds_read_b128 v[214:217], v191 offset:36864
	ds_read_b128 v[218:221], v191 offset:37888
	ds_read_b128 v[222:225], v191 offset:38912
	ds_read_b128 v[226:229], v191 offset:39936
	global_load_lds_dwordx4 v[232:233], off
	v_lshl_add_u64 v[232:233], s[54:55], 0, v[158:159]
	s_mov_b32 m0, s49
	s_nop 0
	global_load_lds_dwordx4 v[232:233], off
	s_waitcnt vmcnt(8)
	s_waitcnt lgkmcnt(0)
	s_barrier
	s_setprio 0
	s_waitcnt lgkmcnt(0)
	v_mfma_f32_16x16x32_bf16 v[126:129], v[134:137], v[198:201], v[126:129]
	v_mfma_f32_16x16x32_bf16 v[122:125], v[142:145], v[198:201], v[122:125]
	v_mfma_f32_16x16x32_bf16 v[110:113], v[134:137], v[206:209], v[110:113]
	v_mfma_f32_16x16x32_bf16 v[106:109], v[142:145], v[206:209], v[106:109]
	v_mfma_f32_16x16x32_bf16 v[94:97], v[134:137], v[214:217], v[94:97]
	v_mfma_f32_16x16x32_bf16 v[90:93], v[142:145], v[214:217], v[90:93]
	v_mfma_f32_16x16x32_bf16 v[78:81], v[134:137], v[222:225], v[78:81]
	v_mfma_f32_16x16x32_bf16 v[74:77], v[142:145], v[222:225], v[74:77]
	v_mfma_f32_16x16x32_bf16 v[126:129], v[138:141], v[202:205], v[126:129]
	v_mfma_f32_16x16x32_bf16 v[122:125], v[146:149], v[202:205], v[122:125]
	v_mfma_f32_16x16x32_bf16 v[110:113], v[138:141], v[210:213], v[110:113]
	v_mfma_f32_16x16x32_bf16 v[106:109], v[146:149], v[210:213], v[106:109]
	v_mfma_f32_16x16x32_bf16 v[94:97], v[138:141], v[218:221], v[94:97]
	v_mfma_f32_16x16x32_bf16 v[90:93], v[146:149], v[218:221], v[90:93]
	v_mfma_f32_16x16x32_bf16 v[78:81], v[138:141], v[226:229], v[78:81]
	v_mfma_f32_16x16x32_bf16 v[74:77], v[146:149], v[226:229], v[74:77]
	v_mfma_f32_16x16x32_bf16 v[118:121], v[150:153], v[198:201], v[118:121]
	v_mfma_f32_16x16x32_bf16 v[114:117], v[174:177], v[198:201], v[114:117]
	v_mfma_f32_16x16x32_bf16 v[102:105], v[150:153], v[206:209], v[102:105]
	v_mfma_f32_16x16x32_bf16 v[98:101], v[174:177], v[206:209], v[98:101]
	v_mfma_f32_16x16x32_bf16 v[86:89], v[150:153], v[214:217], v[86:89]
	v_mfma_f32_16x16x32_bf16 v[82:85], v[174:177], v[214:217], v[82:85]
	v_mfma_f32_16x16x32_bf16 v[70:73], v[150:153], v[222:225], v[70:73]
	v_mfma_f32_16x16x32_bf16 v[66:69], v[174:177], v[222:225], v[66:69]
	v_mfma_f32_16x16x32_bf16 v[118:121], v[170:173], v[202:205], v[118:121]
	v_mfma_f32_16x16x32_bf16 v[114:117], v[194:197], v[202:205], v[114:117]
	v_mfma_f32_16x16x32_bf16 v[102:105], v[170:173], v[210:213], v[102:105]
	v_mfma_f32_16x16x32_bf16 v[98:101], v[194:197], v[210:213], v[98:101]
	v_mfma_f32_16x16x32_bf16 v[86:89], v[170:173], v[218:221], v[86:89]
	v_mfma_f32_16x16x32_bf16 v[82:85], v[194:197], v[218:221], v[82:85]
	v_mfma_f32_16x16x32_bf16 v[70:73], v[170:173], v[226:229], v[70:73]
	v_mfma_f32_16x16x32_bf16 v[66:69], v[194:197], v[226:229], v[66:69]
	s_setprio 1
	s_barrier
	s_add_i32 s2, s2, s42
	v_lshl_add_u64 v[178:179], v[178:179], 0, s[26:27]
	s_mov_b32 m0, s2
	ds_read_b128 v[198:201], v191 offset:49152
	ds_read_b128 v[202:205], v191 offset:50176
	ds_read_b128 v[206:209], v191 offset:51200
	ds_read_b128 v[210:213], v191 offset:52224
	ds_read_b128 v[214:217], v191 offset:53248
	ds_read_b128 v[218:221], v191 offset:54272
	ds_read_b128 v[222:225], v191 offset:55296
	ds_read_b128 v[226:229], v191 offset:56320
	global_load_lds_dwordx4 v[178:179], off
	s_add_i32 m0, s2, 0x2000
	s_add_u32 s54, s58, 0x80080
	v_lshl_add_u64 v[178:179], v[182:183], 0, s[26:27]
	s_addc_u32 s55, s59, 0
	s_add_i32 s2, s60, s42
	global_load_lds_dwordx4 v[178:179], off
	v_lshl_add_u64 v[178:179], s[54:55], 0, v[156:157]
	s_mov_b32 m0, s2
	s_nop 0
	global_load_lds_dwordx4 v[178:179], off
	v_lshl_add_u64 v[178:179], s[54:55], 0, v[160:161]
	s_add_i32 m0, s2, 0x2000
	s_nop 0
	global_load_lds_dwordx4 v[178:179], off
	v_lshl_add_u64 v[178:179], v[186:187], 0, s[26:27]
	s_mov_b32 m0, s51
	s_nop 0
	global_load_lds_dwordx4 v[178:179], off
	v_lshl_add_u64 v[178:179], v[230:231], 0, s[26:27]
	s_mov_b32 m0, s52
	s_nop 0
	global_load_lds_dwordx4 v[178:179], off
	s_waitcnt vmcnt(8)
	s_waitcnt lgkmcnt(0)
	s_barrier
	s_setprio 0
	s_waitcnt lgkmcnt(0)
	v_mfma_f32_16x16x32_bf16 v[62:65], v[134:137], v[198:201], v[62:65]
	v_mfma_f32_16x16x32_bf16 v[58:61], v[142:145], v[198:201], v[58:61]
	v_mfma_f32_16x16x32_bf16 v[46:49], v[134:137], v[206:209], v[46:49]
	v_mfma_f32_16x16x32_bf16 v[42:45], v[142:145], v[206:209], v[42:45]
	v_mfma_f32_16x16x32_bf16 v[30:33], v[134:137], v[214:217], v[30:33]
	v_mfma_f32_16x16x32_bf16 v[26:29], v[142:145], v[214:217], v[26:29]
	v_mfma_f32_16x16x32_bf16 v[14:17], v[134:137], v[222:225], v[14:17]
	v_mfma_f32_16x16x32_bf16 v[10:13], v[142:145], v[222:225], v[10:13]
	v_mfma_f32_16x16x32_bf16 v[62:65], v[138:141], v[202:205], v[62:65]
	v_mfma_f32_16x16x32_bf16 v[58:61], v[146:149], v[202:205], v[58:61]
	v_mfma_f32_16x16x32_bf16 v[46:49], v[138:141], v[210:213], v[46:49]
	v_mfma_f32_16x16x32_bf16 v[42:45], v[146:149], v[210:213], v[42:45]
	v_mfma_f32_16x16x32_bf16 v[30:33], v[138:141], v[218:221], v[30:33]
	v_mfma_f32_16x16x32_bf16 v[26:29], v[146:149], v[218:221], v[26:29]
	v_mfma_f32_16x16x32_bf16 v[14:17], v[138:141], v[226:229], v[14:17]
	v_mfma_f32_16x16x32_bf16 v[10:13], v[146:149], v[226:229], v[10:13]
	v_mfma_f32_16x16x32_bf16 v[54:57], v[150:153], v[198:201], v[54:57]
	v_mfma_f32_16x16x32_bf16 v[50:53], v[174:177], v[198:201], v[50:53]
	v_mfma_f32_16x16x32_bf16 v[38:41], v[150:153], v[206:209], v[38:41]
	v_mfma_f32_16x16x32_bf16 v[34:37], v[174:177], v[206:209], v[34:37]
	v_mfma_f32_16x16x32_bf16 v[22:25], v[150:153], v[214:217], v[22:25]
	v_mfma_f32_16x16x32_bf16 v[18:21], v[174:177], v[214:217], v[18:21]
	v_mfma_f32_16x16x32_bf16 v[6:9], v[150:153], v[222:225], v[6:9]
	v_mfma_f32_16x16x32_bf16 v[2:5], v[174:177], v[222:225], v[2:5]
	v_mfma_f32_16x16x32_bf16 v[54:57], v[170:173], v[202:205], v[54:57]
	v_mfma_f32_16x16x32_bf16 v[50:53], v[194:197], v[202:205], v[50:53]
	v_mfma_f32_16x16x32_bf16 v[38:41], v[170:173], v[210:213], v[38:41]
	v_mfma_f32_16x16x32_bf16 v[34:37], v[194:197], v[210:213], v[34:37]
	v_mfma_f32_16x16x32_bf16 v[22:25], v[170:173], v[218:221], v[22:25]
	v_mfma_f32_16x16x32_bf16 v[18:21], v[194:197], v[218:221], v[18:21]
	v_mfma_f32_16x16x32_bf16 v[6:9], v[170:173], v[226:229], v[6:9]
	v_mfma_f32_16x16x32_bf16 v[2:5], v[194:197], v[226:229], v[2:5]
	s_setprio 1
	s_barrier
	s_add_i32 s68, s68, 2
	s_cmp_gt_u32 s68, 29
	s_mov_b64 s[54:55], s[56:57]
	s_cbranch_scc0 .LBB0_1547
	s_and_b64 vcc, exec, s[28:29]
	s_cbranch_vccz .LBB0_1550
	s_barrier

.LBB0_1936:
	s_setprio 0
	s_waitcnt lgkmcnt(0)
	v_mfma_f32_16x16x32_bf16 v[126:129], v[146:149], v[186:189], v[126:129]
	v_mfma_f32_16x16x32_bf16 v[122:125], v[154:157], v[186:189], v[122:125]
	v_mfma_f32_16x16x32_bf16 v[110:113], v[146:149], v[178:181], v[110:113]
	v_mfma_f32_16x16x32_bf16 v[106:109], v[154:157], v[178:181], v[106:109]
	v_mfma_f32_16x16x32_bf16 v[94:97], v[146:149], v[170:173], v[94:97]
	v_mfma_f32_16x16x32_bf16 v[90:93], v[154:157], v[170:173], v[90:93]
	v_mfma_f32_16x16x32_bf16 v[22:25], v[146:149], v[162:165], v[22:25]
	v_mfma_f32_16x16x32_bf16 v[10:13], v[154:157], v[162:165], v[10:13]
	v_mfma_f32_16x16x32_bf16 v[126:129], v[150:153], v[190:193], v[126:129]
	v_mfma_f32_16x16x32_bf16 v[122:125], v[158:161], v[190:193], v[122:125]
	v_mfma_f32_16x16x32_bf16 v[110:113], v[150:153], v[182:185], v[110:113]
	v_mfma_f32_16x16x32_bf16 v[106:109], v[158:161], v[182:185], v[106:109]
	v_mfma_f32_16x16x32_bf16 v[94:97], v[150:153], v[174:177], v[94:97]
	v_mfma_f32_16x16x32_bf16 v[90:93], v[158:161], v[174:177], v[90:93]
	v_mfma_f32_16x16x32_bf16 v[22:25], v[150:153], v[166:169], v[22:25]
	v_mfma_f32_16x16x32_bf16 v[10:13], v[158:161], v[166:169], v[10:13]
	v_mfma_f32_16x16x32_bf16 v[118:121], v[130:133], v[186:189], v[118:121]
	v_mfma_f32_16x16x32_bf16 v[114:117], v[138:141], v[186:189], v[114:117]
	v_mfma_f32_16x16x32_bf16 v[102:105], v[130:133], v[178:181], v[102:105]
	v_mfma_f32_16x16x32_bf16 v[98:101], v[138:141], v[178:181], v[98:101]
	v_mfma_f32_16x16x32_bf16 v[38:41], v[130:133], v[170:173], v[38:41]
	v_mfma_f32_16x16x32_bf16 v[26:29], v[138:141], v[170:173], v[26:29]
	v_mfma_f32_16x16x32_bf16 v[6:9], v[130:133], v[162:165], v[6:9]
	v_mfma_f32_16x16x32_bf16 v[2:5], v[138:141], v[162:165], v[2:5]
	v_mfma_f32_16x16x32_bf16 v[118:121], v[134:137], v[190:193], v[118:121]
	v_mfma_f32_16x16x32_bf16 v[114:117], v[142:145], v[190:193], v[114:117]
	v_mfma_f32_16x16x32_bf16 v[102:105], v[134:137], v[182:185], v[102:105]
	v_mfma_f32_16x16x32_bf16 v[98:101], v[142:145], v[182:185], v[98:101]
	v_mfma_f32_16x16x32_bf16 v[38:41], v[134:137], v[174:177], v[38:41]
	v_mfma_f32_16x16x32_bf16 v[26:29], v[142:145], v[174:177], v[26:29]
	v_mfma_f32_16x16x32_bf16 v[6:9], v[134:137], v[166:169], v[6:9]
	v_mfma_f32_16x16x32_bf16 v[2:5], v[142:145], v[166:169], v[2:5]
	s_setprio 1
	s_barrier
	s_add_i32 s2, s89, 2
	s_cmp_gt_u32 s89, 5
	s_mov_b32 s89, s2
	s_cbranch_scc1 .LBB0_1956

.LBB0_1954:
	s_lshl_b32 s2, s89, 7
	v_add_u32_e32 v142, s82, v205
	v_add_u32_e32 v158, s83, v205
	s_add_u32 s66, s40, s2
	ds_read_b128 v[130:133], v142
	ds_read_b128 v[134:137], v142 offset:1024
	ds_read_b128 v[138:141], v142 offset:2048
	ds_read_b128 v[142:145], v142 offset:3072
	ds_read_b128 v[146:149], v158
	ds_read_b128 v[150:153], v158 offset:1024
	ds_read_b128 v[154:157], v158 offset:2048
	ds_read_b128 v[158:161], v158 offset:3072
	s_addc_u32 s67, s41, 0
	s_add_u32 s68, s66, 0x100
	s_addc_u32 s69, s67, 0
	s_and_b64 s[66:67], s[62:63], exec
	s_cselect_b32 s67, s37, s69
	s_cselect_b32 s66, s85, s68
	s_add_i32 s70, s2, 0x100
	s_and_b64 s[68:69], s[62:63], exec
	s_cselect_b32 s70, 0, s70
	s_add_u32 s2, s38, s2
	s_addc_u32 s69, s39, 0
	s_add_u32 s68, s2, 0x20080
	s_addc_u32 s69, s69, 0
	v_lshl_add_u64 v[210:211], s[68:69], 0, v[194:195]
	s_add_i32 m0, s50, 0xc000
	ds_read_b128 v[162:165], v209
	ds_read_b128 v[166:169], v209 offset:1024
	ds_read_b128 v[170:173], v209 offset:2048
	ds_read_b128 v[174:177], v209 offset:3072
	ds_read_b128 v[178:181], v209 offset:4096
	ds_read_b128 v[182:185], v209 offset:5120
	ds_read_b128 v[186:189], v209 offset:6144
	ds_read_b128 v[190:193], v209 offset:7168
	global_load_lds_dwordx4 v[210:211], off
	v_lshl_add_u64 v[210:211], s[68:69], 0, v[198:199]
	s_add_i32 m0, s50, 0xe000
	s_nop 0
	global_load_lds_dwordx4 v[210:211], off
	s_waitcnt vmcnt(8)
	s_waitcnt lgkmcnt(0)
	s_barrier
	s_setprio 0
	s_waitcnt lgkmcnt(0)
	v_mfma_f32_16x16x32_bf16 v[86:89], v[130:133], v[162:165], v[86:89]
	v_mfma_f32_16x16x32_bf16 v[82:85], v[138:141], v[162:165], v[82:85]
	v_mfma_f32_16x16x32_bf16 v[78:81], v[130:133], v[170:173], v[78:81]
	v_mfma_f32_16x16x32_bf16 v[74:77], v[138:141], v[170:173], v[74:77]
	v_mfma_f32_16x16x32_bf16 v[70:73], v[130:133], v[178:181], v[70:73]
	v_mfma_f32_16x16x32_bf16 v[66:69], v[138:141], v[178:181], v[66:69]
	v_mfma_f32_16x16x32_bf16 v[62:65], v[130:133], v[186:189], v[62:65]
	v_mfma_f32_16x16x32_bf16 v[58:61], v[138:141], v[186:189], v[58:61]
	v_mfma_f32_16x16x32_bf16 v[86:89], v[134:137], v[166:169], v[86:89]
	v_mfma_f32_16x16x32_bf16 v[82:85], v[142:145], v[166:169], v[82:85]
	v_mfma_f32_16x16x32_bf16 v[78:81], v[134:137], v[174:177], v[78:81]
	v_mfma_f32_16x16x32_bf16 v[74:77], v[142:145], v[174:177], v[74:77]
	v_mfma_f32_16x16x32_bf16 v[70:73], v[134:137], v[182:185], v[70:73]
	v_mfma_f32_16x16x32_bf16 v[66:69], v[142:145], v[182:185], v[66:69]
	v_mfma_f32_16x16x32_bf16 v[62:65], v[134:137], v[190:193], v[62:65]
	v_mfma_f32_16x16x32_bf16 v[58:61], v[142:145], v[190:193], v[58:61]
	v_mfma_f32_16x16x32_bf16 v[54:57], v[146:149], v[162:165], v[54:57]
	v_mfma_f32_16x16x32_bf16 v[50:53], v[154:157], v[162:165], v[50:53]
	v_mfma_f32_16x16x32_bf16 v[46:49], v[146:149], v[170:173], v[46:49]
	v_mfma_f32_16x16x32_bf16 v[42:45], v[154:157], v[170:173], v[42:45]
	v_mfma_f32_16x16x32_bf16 v[34:37], v[146:149], v[178:181], v[34:37]
	v_mfma_f32_16x16x32_bf16 v[30:33], v[154:157], v[178:181], v[30:33]
	v_mfma_f32_16x16x32_bf16 v[18:21], v[146:149], v[186:189], v[18:21]
	v_mfma_f32_16x16x32_bf16 v[14:17], v[154:157], v[186:189], v[14:17]
	v_mfma_f32_16x16x32_bf16 v[54:57], v[150:153], v[166:169], v[54:57]
	v_mfma_f32_16x16x32_bf16 v[50:53], v[158:161], v[166:169], v[50:53]
	v_mfma_f32_16x16x32_bf16 v[46:49], v[150:153], v[174:177], v[46:49]
	v_mfma_f32_16x16x32_bf16 v[42:45], v[158:161], v[174:177], v[42:45]
	v_mfma_f32_16x16x32_bf16 v[34:37], v[150:153], v[182:185], v[34:37]
	v_mfma_f32_16x16x32_bf16 v[30:33], v[158:161], v[182:185], v[30:33]
	v_mfma_f32_16x16x32_bf16 v[18:21], v[150:153], v[190:193], v[18:21]
	v_mfma_f32_16x16x32_bf16 v[14:17], v[158:161], v[190:193], v[14:17]
	s_setprio 1
	s_barrier
	s_add_i32 s2, s82, s49
	v_lshl_add_u64 v[210:211], s[66:67], 0, v[196:197]
	s_mov_b32 m0, s2
	ds_read_b128 v[162:165], v209 offset:16384
	ds_read_b128 v[166:169], v209 offset:17408
	ds_read_b128 v[170:173], v209 offset:18432
	ds_read_b128 v[174:177], v209 offset:19456
	ds_read_b128 v[178:181], v209 offset:20480
	ds_read_b128 v[182:185], v209 offset:21504
	ds_read_b128 v[186:189], v209 offset:22528
	ds_read_b128 v[190:193], v209 offset:23552
	global_load_lds_dwordx4 v[210:211], off
	s_add_i32 m0, s2, 0x2000
	s_add_u32 s68, s66, 0x20000
	v_lshl_add_u64 v[212:213], s[66:67], 0, v[200:201]
	s_addc_u32 s69, s67, 0
	s_add_i32 s2, s83, s49
	global_load_lds_dwordx4 v[212:213], off
	v_lshl_add_u64 v[214:215], s[68:69], 0, v[196:197]
	s_mov_b32 m0, s2
	s_nop 0
	global_load_lds_dwordx4 v[214:215], off
	s_add_i32 m0, s2, 0x2000
	s_add_u32 s64, s64, s70
	v_lshl_add_u64 v[214:215], s[68:69], 0, v[200:201]
	s_addc_u32 s65, s65, 0
	global_load_lds_dwordx4 v[214:215], off
	v_lshl_add_u64 v[214:215], s[64:65], 0, v[194:195]
	s_mov_b32 m0, s50
	v_lshl_add_u64 v[216:217], s[64:65], 0, v[198:199]
	global_load_lds_dwordx4 v[214:215], off
	s_mov_b32 m0, s51
	s_nop 0
	global_load_lds_dwordx4 v[216:217], off
	s_waitcnt vmcnt(8)
	s_waitcnt lgkmcnt(0)
	s_barrier
	s_setprio 0
	s_waitcnt lgkmcnt(0)
	v_mfma_f32_16x16x32_bf16 v[126:129], v[130:133], v[162:165], v[126:129]
	v_mfma_f32_16x16x32_bf16 v[122:125], v[138:141], v[162:165], v[122:125]
	v_mfma_f32_16x16x32_bf16 v[110:113], v[130:133], v[170:173], v[110:113]
	v_mfma_f32_16x16x32_bf16 v[106:109], v[138:141], v[170:173], v[106:109]
	v_mfma_f32_16x16x32_bf16 v[94:97], v[130:133], v[178:181], v[94:97]
	v_mfma_f32_16x16x32_bf16 v[90:93], v[138:141], v[178:181], v[90:93]
	v_mfma_f32_16x16x32_bf16 v[22:25], v[130:133], v[186:189], v[22:25]
	v_mfma_f32_16x16x32_bf16 v[10:13], v[138:141], v[186:189], v[10:13]
	v_mfma_f32_16x16x32_bf16 v[126:129], v[134:137], v[166:169], v[126:129]
	v_mfma_f32_16x16x32_bf16 v[122:125], v[142:145], v[166:169], v[122:125]
	v_mfma_f32_16x16x32_bf16 v[110:113], v[134:137], v[174:177], v[110:113]
	v_mfma_f32_16x16x32_bf16 v[106:109], v[142:145], v[174:177], v[106:109]
	v_mfma_f32_16x16x32_bf16 v[94:97], v[134:137], v[182:185], v[94:97]
	v_mfma_f32_16x16x32_bf16 v[90:93], v[142:145], v[182:185], v[90:93]
	v_mfma_f32_16x16x32_bf16 v[22:25], v[134:137], v[190:193], v[22:25]
	v_mfma_f32_16x16x32_bf16 v[10:13], v[142:145], v[190:193], v[10:13]
	v_mfma_f32_16x16x32_bf16 v[118:121], v[146:149], v[162:165], v[118:121]
	v_mfma_f32_16x16x32_bf16 v[114:117], v[154:157], v[162:165], v[114:117]
	v_mfma_f32_16x16x32_bf16 v[102:105], v[146:149], v[170:173], v[102:105]
	v_mfma_f32_16x16x32_bf16 v[98:101], v[154:157], v[170:173], v[98:101]
	v_mfma_f32_16x16x32_bf16 v[38:41], v[146:149], v[178:181], v[38:41]
	v_mfma_f32_16x16x32_bf16 v[26:29], v[154:157], v[178:181], v[26:29]
	v_mfma_f32_16x16x32_bf16 v[6:9], v[146:149], v[186:189], v[6:9]
	v_mfma_f32_16x16x32_bf16 v[2:5], v[154:157], v[186:189], v[2:5]
	v_mfma_f32_16x16x32_bf16 v[118:121], v[150:153], v[166:169], v[118:121]
	v_mfma_f32_16x16x32_bf16 v[114:117], v[158:161], v[166:169], v[114:117]
	v_mfma_f32_16x16x32_bf16 v[102:105], v[150:153], v[174:177], v[102:105]
	v_mfma_f32_16x16x32_bf16 v[98:101], v[158:161], v[174:177], v[98:101]
	v_mfma_f32_16x16x32_bf16 v[38:41], v[150:153], v[182:185], v[38:41]
	v_mfma_f32_16x16x32_bf16 v[26:29], v[158:161], v[182:185], v[26:29]
	v_mfma_f32_16x16x32_bf16 v[6:9], v[150:153], v[190:193], v[6:9]
	v_mfma_f32_16x16x32_bf16 v[2:5], v[158:161], v[190:193], v[2:5]
	s_setprio 1
	s_barrier
	s_add_i32 s2, 0, 0x18000
	s_add_i32 s68, 0, 0x1c000
	v_add_u32_e32 v130, s2, v205
	v_add_u32_e32 v142, s68, v205
	ds_read_b128 v[146:149], v130
	ds_read_b128 v[150:153], v130 offset:1024
	ds_read_b128 v[154:157], v130 offset:2048
	ds_read_b128 v[158:161], v130 offset:3072
	ds_read_b128 v[130:133], v142
	ds_read_b128 v[134:137], v142 offset:1024
	ds_read_b128 v[138:141], v142 offset:2048
	ds_read_b128 v[142:145], v142 offset:3072
	s_add_u32 s64, s64, 0x20000
	s_addc_u32 s65, s65, 0
	s_mov_b32 m0, s52
	v_lshl_add_u64 v[218:219], s[64:65], 0, v[194:195]
	ds_read_b128 v[162:165], v209 offset:32768
	ds_read_b128 v[166:169], v209 offset:33792
	ds_read_b128 v[170:173], v209 offset:34816
	ds_read_b128 v[174:177], v209 offset:35840
	ds_read_b128 v[178:181], v209 offset:36864
	ds_read_b128 v[182:185], v209 offset:37888
	ds_read_b128 v[186:189], v209 offset:38912
	ds_read_b128 v[190:193], v209 offset:39936
	global_load_lds_dwordx4 v[218:219], off
	v_lshl_add_u64 v[218:219], s[64:65], 0, v[198:199]
	s_mov_b32 m0, s53
	s_nop 0
	global_load_lds_dwordx4 v[218:219], off
	s_waitcnt vmcnt(8)
	s_waitcnt lgkmcnt(0)
	s_barrier
	s_setprio 0
	s_waitcnt lgkmcnt(0)
	v_mfma_f32_16x16x32_bf16 v[86:89], v[146:149], v[162:165], v[86:89]
	v_mfma_f32_16x16x32_bf16 v[82:85], v[154:157], v[162:165], v[82:85]
	v_mfma_f32_16x16x32_bf16 v[78:81], v[146:149], v[170:173], v[78:81]
	v_mfma_f32_16x16x32_bf16 v[74:77], v[154:157], v[170:173], v[74:77]
	v_mfma_f32_16x16x32_bf16 v[70:73], v[146:149], v[178:181], v[70:73]
	v_mfma_f32_16x16x32_bf16 v[66:69], v[154:157], v[178:181], v[66:69]
	v_mfma_f32_16x16x32_bf16 v[62:65], v[146:149], v[186:189], v[62:65]
	v_mfma_f32_16x16x32_bf16 v[58:61], v[154:157], v[186:189], v[58:61]
	v_mfma_f32_16x16x32_bf16 v[86:89], v[150:153], v[166:169], v[86:89]
	v_mfma_f32_16x16x32_bf16 v[82:85], v[158:161], v[166:169], v[82:85]
	v_mfma_f32_16x16x32_bf16 v[78:81], v[150:153], v[174:177], v[78:81]
	v_mfma_f32_16x16x32_bf16 v[74:77], v[158:161], v[174:177], v[74:77]
	v_mfma_f32_16x16x32_bf16 v[70:73], v[150:153], v[182:185], v[70:73]
	v_mfma_f32_16x16x32_bf16 v[66:69], v[158:161], v[182:185], v[66:69]
	v_mfma_f32_16x16x32_bf16 v[62:65], v[150:153], v[190:193], v[62:65]
	v_mfma_f32_16x16x32_bf16 v[58:61], v[158:161], v[190:193], v[58:61]
	v_mfma_f32_16x16x32_bf16 v[54:57], v[130:133], v[162:165], v[54:57]
	v_mfma_f32_16x16x32_bf16 v[50:53], v[138:141], v[162:165], v[50:53]
	v_mfma_f32_16x16x32_bf16 v[46:49], v[130:133], v[170:173], v[46:49]
	v_mfma_f32_16x16x32_bf16 v[42:45], v[138:141], v[170:173], v[42:45]
	v_mfma_f32_16x16x32_bf16 v[34:37], v[130:133], v[178:181], v[34:37]
	v_mfma_f32_16x16x32_bf16 v[30:33], v[138:141], v[178:181], v[30:33]
	v_mfma_f32_16x16x32_bf16 v[18:21], v[130:133], v[186:189], v[18:21]
	v_mfma_f32_16x16x32_bf16 v[14:17], v[138:141], v[186:189], v[14:17]
	v_mfma_f32_16x16x32_bf16 v[54:57], v[134:137], v[166:169], v[54:57]
	v_mfma_f32_16x16x32_bf16 v[50:53], v[142:145], v[166:169], v[50:53]
	v_mfma_f32_16x16x32_bf16 v[46:49], v[134:137], v[174:177], v[46:49]
	v_mfma_f32_16x16x32_bf16 v[42:45], v[142:145], v[174:177], v[42:45]
	v_mfma_f32_16x16x32_bf16 v[34:37], v[134:137], v[182:185], v[34:37]
	v_mfma_f32_16x16x32_bf16 v[30:33], v[142:145], v[182:185], v[30:33]
	v_mfma_f32_16x16x32_bf16 v[18:21], v[134:137], v[190:193], v[18:21]
	v_mfma_f32_16x16x32_bf16 v[14:17], v[142:145], v[190:193], v[14:17]
	s_setprio 1
	s_barrier
	s_add_i32 s2, s2, s49
	v_lshl_add_u64 v[210:211], v[210:211], 0, s[12:13]
	s_mov_b32 m0, s2
	ds_read_b128 v[186:189], v209 offset:49152
	ds_read_b128 v[190:193], v209 offset:50176
	ds_read_b128 v[178:181], v209 offset:51200
	ds_read_b128 v[182:185], v209 offset:52224
	ds_read_b128 v[170:173], v209 offset:53248
	ds_read_b128 v[174:177], v209 offset:54272
	ds_read_b128 v[162:165], v209 offset:55296
	ds_read_b128 v[166:169], v209 offset:56320
	global_load_lds_dwordx4 v[210:211], off
	s_add_i32 m0, s2, 0x2000
	s_add_u32 s64, s66, 0x20080
	v_lshl_add_u64 v[210:211], v[212:213], 0, s[12:13]
	s_addc_u32 s65, s67, 0
	s_add_i32 s2, s68, s49
	global_load_lds_dwordx4 v[210:211], off
	v_lshl_add_u64 v[210:211], s[64:65], 0, v[196:197]
	s_mov_b32 m0, s2
	s_andn2_b64 vcc, exec, s[62:63]
	global_load_lds_dwordx4 v[210:211], off
	v_lshl_add_u64 v[210:211], s[64:65], 0, v[200:201]
	s_add_i32 m0, s2, 0x2000
	s_nop 0
	global_load_lds_dwordx4 v[210:211], off
	v_lshl_add_u64 v[210:211], v[214:215], 0, s[12:13]
	s_mov_b32 m0, s75
	s_nop 0
	global_load_lds_dwordx4 v[210:211], off
	v_lshl_add_u64 v[210:211], v[216:217], 0, s[12:13]
	s_mov_b32 m0, s76
	s_nop 0
	global_load_lds_dwordx4 v[210:211], off
	s_waitcnt vmcnt(8)
	s_waitcnt lgkmcnt(0)
	s_barrier
	s_cbranch_vccnz .LBB0_1936
	v_pk_mul_f32 v[214:215], v[86:87], s[20:21] op_sel_hi:[1,0]
	v_pk_mul_f32 v[216:217], v[82:83], s[20:21] op_sel_hi:[1,0]
	v_mov_b32_e32 v218, 0
	v_mov_b32_e32 v219, 0
	v_cvt_pk_fp8_f32 v218, v214, v215
	v_cvt_pk_fp8_f32 v219, v216, v217
	v_pk_mul_f32 v[214:215], v[88:89], s[20:21] op_sel_hi:[1,0]
	v_pk_mul_f32 v[216:217], v[84:85], s[20:21] op_sel_hi:[1,0]
	v_cvt_pk_fp8_f32 v218, v214, v215 op_sel:[0,0,1]
	v_cvt_pk_fp8_f32 v219, v216, v217 op_sel:[0,0,1]
	v_pk_mul_f32 v[214:215], v[54:55], s[20:21] op_sel_hi:[1,0]
	v_pk_mul_f32 v[216:217], v[50:51], s[20:21] op_sel_hi:[1,0]
	v_mov_b32_e32 v220, 0
	v_mov_b32_e32 v221, 0
	v_mov_b32_e32 v210, v1
	v_mov_b32_e32 v211, v204
	v_cvt_pk_fp8_f32 v220, v214, v215
	v_cvt_pk_fp8_f32 v221, v216, v217
	v_pk_mul_f32 v[214:215], v[56:57], s[20:21] op_sel_hi:[1,0]
	v_add_u32_e32 v210, s87, v210
	v_lshl_add_u32 v212, v211, 3, s88
	v_ashrrev_i32_e32 v211, 31, v210
	v_pk_mul_f32 v[216:217], v[52:53], s[20:21] op_sel_hi:[1,0]
	v_lshlrev_b64 v[210:211], 11, v[210:211]
	v_cvt_pk_fp8_f32 v220, v214, v215 op_sel:[0,0,1]
	v_cvt_pk_fp8_f32 v221, v216, v217 op_sel:[0,0,1]
	v_ashrrev_i32_e32 v213, 31, v212
	v_lshl_add_u64 v[210:211], s[10:11], 0, v[210:211]
	v_lshl_add_u64 v[210:211], v[210:211], 0, v[212:213]
	global_store_dwordx2 v[210:211], v[218:219], off
	global_store_dwordx2 v[210:211], v[220:221], off offset:128
	v_pk_mul_f32 v[214:215], v[78:79], s[20:21] op_sel_hi:[1,0]
	v_pk_mul_f32 v[216:217], v[74:75], s[20:21] op_sel_hi:[1,0]
	v_mov_b32_e32 v218, 0
	v_mov_b32_e32 v219, 0
	v_cvt_pk_fp8_f32 v218, v214, v215
	v_cvt_pk_fp8_f32 v219, v216, v217
	v_pk_mul_f32 v[214:215], v[80:81], s[20:21] op_sel_hi:[1,0]
	v_pk_mul_f32 v[216:217], v[76:77], s[20:21] op_sel_hi:[1,0]
	v_cvt_pk_fp8_f32 v218, v214, v215 op_sel:[0,0,1]
	v_cvt_pk_fp8_f32 v219, v216, v217 op_sel:[0,0,1]
	v_pk_mul_f32 v[214:215], v[46:47], s[20:21] op_sel_hi:[1,0]
	v_pk_mul_f32 v[216:217], v[42:43], s[20:21] op_sel_hi:[1,0]
	v_mov_b32_e32 v220, 0
	v_mov_b32_e32 v221, 0
	v_cvt_pk_fp8_f32 v220, v214, v215
	v_cvt_pk_fp8_f32 v221, v216, v217
	v_pk_mul_f32 v[214:215], v[48:49], s[20:21] op_sel_hi:[1,0]
	v_pk_mul_f32 v[216:217], v[44:45], s[20:21] op_sel_hi:[1,0]
	v_cvt_pk_fp8_f32 v220, v214, v215 op_sel:[0,0,1]
	v_cvt_pk_fp8_f32 v221, v216, v217 op_sel:[0,0,1]
	s_mov_b32 s2, 0x8000
	v_add_co_u32_e32 v214, vcc, s2, v210
	v_lshl_add_u64 v[212:213], v[210:211], 0, s[24:25]
	s_nop 0
	v_addc_co_u32_e32 v215, vcc, 0, v211, vcc
	global_store_dwordx2 v[214:215], v[218:219], off
	global_store_dwordx2 v[212:213], v[220:221], off offset:128
	v_pk_mul_f32 v[214:215], v[70:71], s[20:21] op_sel_hi:[1,0]
	v_pk_mul_f32 v[216:217], v[66:67], s[20:21] op_sel_hi:[1,0]
	v_mov_b32_e32 v218, 0
	v_mov_b32_e32 v219, 0
	v_cvt_pk_fp8_f32 v218, v214, v215
	v_cvt_pk_fp8_f32 v219, v216, v217
	v_pk_mul_f32 v[214:215], v[72:73], s[20:21] op_sel_hi:[1,0]
	v_pk_mul_f32 v[216:217], v[68:69], s[20:21] op_sel_hi:[1,0]
	v_cvt_pk_fp8_f32 v218, v214, v215 op_sel:[0,0,1]
	v_cvt_pk_fp8_f32 v219, v216, v217 op_sel:[0,0,1]
	v_pk_mul_f32 v[214:215], v[34:35], s[20:21] op_sel_hi:[1,0]
	v_pk_mul_f32 v[216:217], v[30:31], s[20:21] op_sel_hi:[1,0]
	v_mov_b32_e32 v220, 0
	v_mov_b32_e32 v221, 0
	v_cvt_pk_fp8_f32 v220, v214, v215
	v_cvt_pk_fp8_f32 v221, v216, v217
	v_pk_mul_f32 v[214:215], v[36:37], s[20:21] op_sel_hi:[1,0]
	v_pk_mul_f32 v[216:217], v[32:33], s[20:21] op_sel_hi:[1,0]
	v_cvt_pk_fp8_f32 v220, v214, v215 op_sel:[0,0,1]
	v_cvt_pk_fp8_f32 v221, v216, v217 op_sel:[0,0,1]
	s_mov_b32 s2, 0x10000
	v_add_co_u32_e32 v214, vcc, s2, v210
	v_lshl_add_u64 v[212:213], v[210:211], 0, s[28:29]
	s_nop 0
	v_addc_co_u32_e32 v215, vcc, 0, v211, vcc
	global_store_dwordx2 v[214:215], v[218:219], off
	global_store_dwordx2 v[212:213], v[220:221], off offset:128
	v_pk_mul_f32 v[214:215], v[62:63], s[20:21] op_sel_hi:[1,0]
	v_pk_mul_f32 v[216:217], v[58:59], s[20:21] op_sel_hi:[1,0]
	v_mov_b32_e32 v218, 0
	v_mov_b32_e32 v219, 0
	v_cvt_pk_fp8_f32 v218, v214, v215
	v_cvt_pk_fp8_f32 v219, v216, v217
	v_pk_mul_f32 v[214:215], v[64:65], s[20:21] op_sel_hi:[1,0]
	v_pk_mul_f32 v[216:217], v[60:61], s[20:21] op_sel_hi:[1,0]
	v_cvt_pk_fp8_f32 v218, v214, v215 op_sel:[0,0,1]
	v_cvt_pk_fp8_f32 v219, v216, v217 op_sel:[0,0,1]
	v_pk_mul_f32 v[214:215], v[18:19], s[20:21] op_sel_hi:[1,0]
	v_pk_mul_f32 v[216:217], v[14:15], s[20:21] op_sel_hi:[1,0]
	v_mov_b32_e32 v220, 0
	v_mov_b32_e32 v221, 0
	v_cvt_pk_fp8_f32 v220, v214, v215
	v_cvt_pk_fp8_f32 v221, v216, v217
	v_pk_mul_f32 v[214:215], v[20:21], s[20:21] op_sel_hi:[1,0]
	v_pk_mul_f32 v[216:217], v[16:17], s[20:21] op_sel_hi:[1,0]
	v_cvt_pk_fp8_f32 v220, v214, v215 op_sel:[0,0,1]
	v_cvt_pk_fp8_f32 v221, v216, v217 op_sel:[0,0,1]
	s_mov_b32 s2, 0x18000
	v_lshl_add_u64 v[212:213], v[210:211], 0, s[30:31]
	v_add_co_u32_e32 v210, vcc, s2, v210
	s_nop 1
	v_addc_co_u32_e32 v211, vcc, 0, v211, vcc
	global_store_dwordx2 v[210:211], v[218:219], off
	global_store_dwordx2 v[212:213], v[220:221], off offset:128
	s_branch .LBB0_1936
